# in-proj epilogue: the 64 nontemporal output stores per layer made plain (write-back) stores
# baseline (speedup 1.0000x reference)
; __device__ __forceinline__ unsigned cvt_pk_bf16(float lo, float hi) { const bf16x2_t r = __builtin_convertvector((f32x2_t){lo, hi}, bf16x2_t); return __builtin_bit_cast(unsigned, r); }
; __device__ __forceinline__ float silu_fast(float x) { return x * __builtin_amdgcn_rcpf(1.0f + __builtin_amdgcn_exp2f(-x * 1.4426950408889634f)); }
;     __device__ __forceinline__ void operator()(const f32x4 (&acc)[2][2][4][2], const Unit& u, int wr, int wc, int fr, int fq) const {
;     ...
;         } else {
;             const bool isog = u.pn >= 20;
;             size_t woff; int cb;
;             if (u.pn < 20) { woff = WS_VG; cb = (u.pn - 16) * 256; }
;             else { woff = WS_OG; cb = (u.pn - 20) * 256; }
;             bf16_t* dst = (bf16_t*)(ws + woff);
; #pragma unroll
;             for (int ai = 0; ai < 2; ++ai)
; #pragma unroll
;                 for (int m = 0; m < 4; ++m) {
;                     const int r = row0 + ai * HALF + m * 16;
; #pragma unroll
;                     for (int bj = 0; bj < 2; ++bj) {
;                         f32x4 v0 = acc[ai][bj][m][0], v1 = acc[ai][bj][m][1];
;                         if (isog) {
; #pragma unroll
;                             for (int i = 0; i < 4; ++i) { v0[i] = silu_fast(v0[i]); v1[i] = silu_fast(v1[i]); }
;                         }
;                         u32x4 o; o[0] = cvt_pk_bf16(v0[0], v0[1]); o[1] = cvt_pk_bf16(v0[2], v0[3]); o[2] = cvt_pk_bf16(v1[0], v1[1]); o[3] = cvt_pk_bf16(v1[2], v1[3]);
;                         __builtin_nontemporal_store(o, (u32x4*)(dst + ((size_t)((r >> 11) * 4 + (cb >> 8)) * SEQ + (r & (SEQ - 1))) * 256 + bj * HALF + lc));
;                     }
;                 }
.LBB0_325:
	s_cmp_lt_u32 s78, 20
	s_cselect_b64 s[8:9], -1, 0
	s_and_b64 s[8:9], s[8:9], exec
	s_mov_b32 s8, 0x48188000
	s_cselect_b32 s18, s8, 0x4a188000
	s_mov_b32 s8, 0xfffff0
	s_cselect_b32 s8, s8, 0xffffec
	s_add_i32 s8, s8, s78
	s_and_b32 s10, s8, 0xffffff
	s_ashr_i32 s8, s15, 9
	s_and_b32 s8, s8, -4
	s_add_i32 s8, s8, s10
	s_ashr_i32 s9, s8, 31
	v_lshl_add_u64 v[136:137], v[174:175], 0, s[18:19]
	s_lshl_b64 s[8:9], s[8:9], 20
	v_lshlrev_b32_e32 v140, 9, v192
	v_lshl_add_u64 v[138:139], v[136:137], 0, s[8:9]
	v_and_b32_e32 v168, 0xf9e00, v140
	v_lshl_add_u64 v[138:139], v[138:139], 0, v[168:169]
	v_cvt_pk_bf16_f32 v128, v128, v129
	v_cvt_pk_bf16_f32 v129, v130, v131
	v_cvt_pk_bf16_f32 v130, v132, v133
	v_cvt_pk_bf16_f32 v131, v134, v135
	global_store_dwordx4 v[138:139], v[128:131], off
	v_mov_b64_e32 v[134:135], v[114:115]
	s_andn2_b64 vcc, exec, s[2:3]
	v_cndmask_b32_e64 v128, 0, 1, s[2:3]
	v_cmp_ne_u32_e64 s[8:9], 1, v128
	v_mov_b64_e32 v[130:131], v[118:119]
	v_mov_b64_e32 v[128:129], v[116:117]
	v_mov_b64_e32 v[132:133], v[112:113]
	s_cbranch_vccnz .LBB0_327
	v_mul_f32_e32 v129, 0xbfb8aa3b, v112
	v_mul_f32_e32 v130, 0xbfb8aa3b, v117
	v_exp_f32_e32 v129, v129
	v_exp_f32_e32 v130, v130
	v_mul_f32_e32 v131, 0xbfb8aa3b, v118
	v_mul_f32_e32 v133, 0xbfb8aa3b, v114
	v_add_f32_e32 v129, 1.0, v129
	v_rcp_f32_e32 v132, v129
	v_add_f32_e32 v129, 1.0, v130
	v_mul_f32_e32 v130, 0xbfb8aa3b, v113
	v_exp_f32_e32 v130, v130
	v_exp_f32_e32 v131, v131
	v_exp_f32_e32 v133, v133
	v_mul_f32_e32 v128, 0xbfb8aa3b, v116
	v_add_f32_e32 v140, 1.0, v130
	v_add_f32_e32 v130, 1.0, v131
	v_add_f32_e32 v131, 1.0, v133
	v_mul_f32_e32 v133, 0xbfb8aa3b, v119
	v_mul_f32_e32 v134, 0xbfb8aa3b, v115
	v_exp_f32_e32 v128, v128
	v_exp_f32_e32 v133, v133
	v_exp_f32_e32 v135, v134
	v_rcp_f32_e32 v134, v131
	v_add_f32_e32 v128, 1.0, v128
	v_add_f32_e32 v131, 1.0, v133
	v_add_f32_e32 v133, 1.0, v135
	v_rcp_f32_e32 v128, v128
	v_rcp_f32_e32 v129, v129
	v_rcp_f32_e32 v130, v130
	v_rcp_f32_e32 v131, v131
	v_rcp_f32_e32 v135, v133
	v_rcp_f32_e32 v133, v140
	v_pk_mul_f32 v[128:129], v[116:117], v[128:129]
	v_pk_mul_f32 v[130:131], v[118:119], v[130:131]
	v_pk_mul_f32 v[134:135], v[114:115], v[134:135]
	v_pk_mul_f32 v[132:133], v[112:113], v[132:133]
.LBB0_327:
	v_cvt_pk_bf16_f32 v128, v128, v129
	v_cvt_pk_bf16_f32 v129, v130, v131
	v_cvt_pk_bf16_f32 v130, v132, v133
	v_cvt_pk_bf16_f32 v131, v134, v135
	global_store_dwordx4 v[138:139], v[128:131], off offset:256
	v_mov_b64_e32 v[134:135], v[106:107]
	s_and_b64 vcc, exec, s[8:9]
	v_mov_b64_e32 v[130:131], v[110:111]
	v_mov_b64_e32 v[128:129], v[108:109]
	v_mov_b64_e32 v[132:133], v[104:105]
	s_cbranch_vccnz .LBB0_329
	v_mul_f32_e32 v129, 0xbfb8aa3b, v104
	v_mul_f32_e32 v130, 0xbfb8aa3b, v109
	v_exp_f32_e32 v129, v129
	v_exp_f32_e32 v130, v130
	v_mul_f32_e32 v131, 0xbfb8aa3b, v110
	v_mul_f32_e32 v133, 0xbfb8aa3b, v106
	v_add_f32_e32 v129, 1.0, v129
	v_rcp_f32_e32 v132, v129
	v_add_f32_e32 v129, 1.0, v130
	v_mul_f32_e32 v130, 0xbfb8aa3b, v105
	v_exp_f32_e32 v130, v130
	v_exp_f32_e32 v131, v131
	v_exp_f32_e32 v133, v133
	v_mul_f32_e32 v128, 0xbfb8aa3b, v108
	v_add_f32_e32 v140, 1.0, v130
	v_add_f32_e32 v130, 1.0, v131
	v_add_f32_e32 v131, 1.0, v133
	v_mul_f32_e32 v133, 0xbfb8aa3b, v111
	v_mul_f32_e32 v134, 0xbfb8aa3b, v107
	v_exp_f32_e32 v128, v128
	v_exp_f32_e32 v133, v133
	v_exp_f32_e32 v135, v134
	v_rcp_f32_e32 v134, v131
	v_add_f32_e32 v128, 1.0, v128
	v_add_f32_e32 v131, 1.0, v133
	v_add_f32_e32 v133, 1.0, v135
	v_rcp_f32_e32 v128, v128
	v_rcp_f32_e32 v129, v129
	v_rcp_f32_e32 v130, v130
	v_rcp_f32_e32 v131, v131
	v_rcp_f32_e32 v135, v133
	v_rcp_f32_e32 v133, v140
	v_pk_mul_f32 v[128:129], v[108:109], v[128:129]
	v_pk_mul_f32 v[130:131], v[110:111], v[130:131]
	v_pk_mul_f32 v[134:135], v[106:107], v[134:135]
	v_pk_mul_f32 v[132:133], v[104:105], v[132:133]
.LBB0_329:
	v_cvt_pk_bf16_f32 v128, v128, v129
	v_cvt_pk_bf16_f32 v129, v130, v131
	v_cvt_pk_bf16_f32 v130, v132, v133
	v_add_co_u32_e32 v132, vcc, 0x2000, v138
	v_cvt_pk_bf16_f32 v131, v134, v135
	s_nop 0
	v_addc_co_u32_e32 v133, vcc, 0, v139, vcc
	global_store_dwordx4 v[132:133], v[128:131], off
	v_mov_b64_e32 v[134:135], v[98:99]
	s_and_b64 vcc, exec, s[8:9]
	v_mov_b64_e32 v[130:131], v[102:103]
	v_mov_b64_e32 v[128:129], v[100:101]
	v_mov_b64_e32 v[132:133], v[96:97]
	s_cbranch_vccnz .LBB0_331
	v_mul_f32_e32 v129, 0xbfb8aa3b, v96
	v_mul_f32_e32 v130, 0xbfb8aa3b, v101
	v_exp_f32_e32 v129, v129
	v_exp_f32_e32 v130, v130
	v_mul_f32_e32 v131, 0xbfb8aa3b, v102
	v_mul_f32_e32 v133, 0xbfb8aa3b, v98
	v_add_f32_e32 v129, 1.0, v129
	v_rcp_f32_e32 v132, v129
	v_add_f32_e32 v129, 1.0, v130
	v_mul_f32_e32 v130, 0xbfb8aa3b, v97
	v_exp_f32_e32 v130, v130
	v_exp_f32_e32 v131, v131
	v_exp_f32_e32 v133, v133
	v_mul_f32_e32 v128, 0xbfb8aa3b, v100
	v_add_f32_e32 v140, 1.0, v130
	v_add_f32_e32 v130, 1.0, v131
	v_add_f32_e32 v131, 1.0, v133
	v_mul_f32_e32 v133, 0xbfb8aa3b, v103
	v_mul_f32_e32 v134, 0xbfb8aa3b, v99
	v_exp_f32_e32 v128, v128
	v_exp_f32_e32 v133, v133
	v_exp_f32_e32 v135, v134
	v_rcp_f32_e32 v134, v131
	v_add_f32_e32 v128, 1.0, v128
	v_add_f32_e32 v131, 1.0, v133
	v_add_f32_e32 v133, 1.0, v135
	v_rcp_f32_e32 v128, v128
	v_rcp_f32_e32 v129, v129
	v_rcp_f32_e32 v130, v130
	v_rcp_f32_e32 v131, v131
	v_rcp_f32_e32 v135, v133
	v_rcp_f32_e32 v133, v140
	v_pk_mul_f32 v[128:129], v[100:101], v[128:129]
	v_pk_mul_f32 v[130:131], v[102:103], v[130:131]
	v_pk_mul_f32 v[134:135], v[98:99], v[134:135]
	v_pk_mul_f32 v[132:133], v[96:97], v[132:133]
; __device__ __forceinline__ unsigned cvt_pk_bf16(float lo, float hi) { const bf16x2_t r = __builtin_convertvector((f32x2_t){lo, hi}, bf16x2_t); return __builtin_bit_cast(unsigned, r); }
; __device__ __forceinline__ float silu_fast(float x) { return x * __builtin_amdgcn_rcpf(1.0f + __builtin_amdgcn_exp2f(-x * 1.4426950408889634f)); }
;     __device__ __forceinline__ void operator()(const f32x4 (&acc)[2][2][4][2], const Unit& u, int wr, int wc, int fr, int fq) const {
;     ...
;             for (int ai = 0; ai < 2; ++ai)
; #pragma unroll
;                 for (int m = 0; m < 4; ++m) {
;                     const int r = row0 + ai * HALF + m * 16;
; #pragma unroll
;                     for (int bj = 0; bj < 2; ++bj) {
;                         f32x4 v0 = acc[ai][bj][m][0], v1 = acc[ai][bj][m][1];
;                         if (isog) {
; #pragma unroll
;                             for (int i = 0; i < 4; ++i) { v0[i] = silu_fast(v0[i]); v1[i] = silu_fast(v1[i]); }
;                         }
;                         u32x4 o; o[0] = cvt_pk_bf16(v0[0], v0[1]); o[1] = cvt_pk_bf16(v0[2], v0[3]); o[2] = cvt_pk_bf16(v1[0], v1[1]); o[3] = cvt_pk_bf16(v1[2], v1[3]);
;                         __builtin_nontemporal_store(o, (u32x4*)(dst + ((size_t)((r >> 11) * 4 + (cb >> 8)) * SEQ + (r & (SEQ - 1))) * 256 + bj * HALF + lc));
;                     }
;                 }
.LBB0_331:
	v_cvt_pk_bf16_f32 v128, v128, v129
	v_cvt_pk_bf16_f32 v129, v130, v131
	v_cvt_pk_bf16_f32 v130, v132, v133
	v_add_co_u32_e32 v132, vcc, 0x2000, v138
	v_cvt_pk_bf16_f32 v131, v134, v135
	s_nop 0
	v_addc_co_u32_e32 v133, vcc, 0, v139, vcc
	global_store_dwordx4 v[132:133], v[128:131], off offset:256
	v_mov_b64_e32 v[134:135], v[90:91]
	s_and_b64 vcc, exec, s[8:9]
	v_mov_b64_e32 v[130:131], v[94:95]
	v_mov_b64_e32 v[128:129], v[92:93]
	v_mov_b64_e32 v[132:133], v[88:89]
	s_cbranch_vccnz .LBB0_333
	v_mul_f32_e32 v129, 0xbfb8aa3b, v88
	v_mul_f32_e32 v130, 0xbfb8aa3b, v93
	v_exp_f32_e32 v129, v129
	v_exp_f32_e32 v130, v130
	v_mul_f32_e32 v131, 0xbfb8aa3b, v94
	v_mul_f32_e32 v133, 0xbfb8aa3b, v90
	v_add_f32_e32 v129, 1.0, v129
	v_rcp_f32_e32 v132, v129
	v_add_f32_e32 v129, 1.0, v130
	v_mul_f32_e32 v130, 0xbfb8aa3b, v89
	v_exp_f32_e32 v130, v130
	v_exp_f32_e32 v131, v131
	v_exp_f32_e32 v133, v133
	v_mul_f32_e32 v128, 0xbfb8aa3b, v92
	v_add_f32_e32 v140, 1.0, v130
	v_add_f32_e32 v130, 1.0, v131
	v_add_f32_e32 v131, 1.0, v133
	v_mul_f32_e32 v133, 0xbfb8aa3b, v95
	v_mul_f32_e32 v134, 0xbfb8aa3b, v91
	v_exp_f32_e32 v128, v128
	v_exp_f32_e32 v133, v133
	v_exp_f32_e32 v135, v134
	v_rcp_f32_e32 v134, v131
	v_add_f32_e32 v128, 1.0, v128
	v_add_f32_e32 v131, 1.0, v133
	v_add_f32_e32 v133, 1.0, v135
	v_rcp_f32_e32 v128, v128
	v_rcp_f32_e32 v129, v129
	v_rcp_f32_e32 v130, v130
	v_rcp_f32_e32 v131, v131
	v_rcp_f32_e32 v135, v133
	v_rcp_f32_e32 v133, v140
	v_pk_mul_f32 v[128:129], v[92:93], v[128:129]
	v_pk_mul_f32 v[130:131], v[94:95], v[130:131]
	v_pk_mul_f32 v[134:135], v[90:91], v[134:135]
	v_pk_mul_f32 v[132:133], v[88:89], v[132:133]
.LBB0_333:
	v_cvt_pk_bf16_f32 v128, v128, v129
	v_cvt_pk_bf16_f32 v129, v130, v131
	v_cvt_pk_bf16_f32 v130, v132, v133
	v_add_co_u32_e32 v132, vcc, 0x4000, v138
	v_cvt_pk_bf16_f32 v131, v134, v135
	s_nop 0
	v_addc_co_u32_e32 v133, vcc, 0, v139, vcc
	global_store_dwordx4 v[132:133], v[128:131], off
	v_mov_b64_e32 v[134:135], v[82:83]
	s_and_b64 vcc, exec, s[8:9]
	v_mov_b64_e32 v[130:131], v[86:87]
	v_mov_b64_e32 v[128:129], v[84:85]
	v_mov_b64_e32 v[132:133], v[80:81]
	s_cbranch_vccnz .LBB0_335
	v_mul_f32_e32 v129, 0xbfb8aa3b, v80
	v_mul_f32_e32 v130, 0xbfb8aa3b, v85
	v_exp_f32_e32 v129, v129
	v_exp_f32_e32 v130, v130
	v_mul_f32_e32 v131, 0xbfb8aa3b, v86
	v_mul_f32_e32 v133, 0xbfb8aa3b, v82
	v_add_f32_e32 v129, 1.0, v129
	v_rcp_f32_e32 v132, v129
	v_add_f32_e32 v129, 1.0, v130
	v_mul_f32_e32 v130, 0xbfb8aa3b, v81
	v_exp_f32_e32 v130, v130
	v_exp_f32_e32 v131, v131
	v_exp_f32_e32 v133, v133
	v_mul_f32_e32 v128, 0xbfb8aa3b, v84
	v_add_f32_e32 v140, 1.0, v130
	v_add_f32_e32 v130, 1.0, v131
	v_add_f32_e32 v131, 1.0, v133
	v_mul_f32_e32 v133, 0xbfb8aa3b, v87
	v_mul_f32_e32 v134, 0xbfb8aa3b, v83
	v_exp_f32_e32 v128, v128
	v_exp_f32_e32 v133, v133
	v_exp_f32_e32 v135, v134
	v_rcp_f32_e32 v134, v131
	v_add_f32_e32 v128, 1.0, v128
	v_add_f32_e32 v131, 1.0, v133
	v_add_f32_e32 v133, 1.0, v135
	v_rcp_f32_e32 v128, v128
	v_rcp_f32_e32 v129, v129
	v_rcp_f32_e32 v130, v130
	v_rcp_f32_e32 v131, v131
	v_rcp_f32_e32 v135, v133
	v_rcp_f32_e32 v133, v140
	v_pk_mul_f32 v[128:129], v[84:85], v[128:129]
	v_pk_mul_f32 v[130:131], v[86:87], v[130:131]
	v_pk_mul_f32 v[134:135], v[82:83], v[134:135]
	v_pk_mul_f32 v[132:133], v[80:81], v[132:133]
.LBB0_335:
	v_cvt_pk_bf16_f32 v128, v128, v129
	v_cvt_pk_bf16_f32 v129, v130, v131
	v_cvt_pk_bf16_f32 v130, v132, v133
	v_add_co_u32_e32 v132, vcc, 0x4000, v138
	v_cvt_pk_bf16_f32 v131, v134, v135
	s_nop 0
	v_addc_co_u32_e32 v133, vcc, 0, v139, vcc
	global_store_dwordx4 v[132:133], v[128:131], off offset:256
	v_mov_b64_e32 v[134:135], v[74:75]
	s_and_b64 vcc, exec, s[8:9]
	v_mov_b64_e32 v[130:131], v[78:79]
	v_mov_b64_e32 v[128:129], v[76:77]
	v_mov_b64_e32 v[132:133], v[72:73]
	s_cbranch_vccnz .LBB0_337
	v_mul_f32_e32 v129, 0xbfb8aa3b, v72
	v_mul_f32_e32 v130, 0xbfb8aa3b, v77
	v_exp_f32_e32 v129, v129
	v_exp_f32_e32 v130, v130
	v_mul_f32_e32 v131, 0xbfb8aa3b, v78
	v_mul_f32_e32 v133, 0xbfb8aa3b, v74
	v_add_f32_e32 v129, 1.0, v129
	v_rcp_f32_e32 v132, v129
	v_add_f32_e32 v129, 1.0, v130
	v_mul_f32_e32 v130, 0xbfb8aa3b, v73
	v_exp_f32_e32 v130, v130
	v_exp_f32_e32 v131, v131
	v_exp_f32_e32 v133, v133
	v_mul_f32_e32 v128, 0xbfb8aa3b, v76
	v_add_f32_e32 v140, 1.0, v130
	v_add_f32_e32 v130, 1.0, v131
	v_add_f32_e32 v131, 1.0, v133
	v_mul_f32_e32 v133, 0xbfb8aa3b, v79
	v_mul_f32_e32 v134, 0xbfb8aa3b, v75
	v_exp_f32_e32 v128, v128
	v_exp_f32_e32 v133, v133
	v_exp_f32_e32 v135, v134
	v_rcp_f32_e32 v134, v131
	v_add_f32_e32 v128, 1.0, v128
	v_add_f32_e32 v131, 1.0, v133
	v_add_f32_e32 v133, 1.0, v135
	v_rcp_f32_e32 v128, v128
	v_rcp_f32_e32 v129, v129
	v_rcp_f32_e32 v130, v130
	v_rcp_f32_e32 v131, v131
	v_rcp_f32_e32 v135, v133
	v_rcp_f32_e32 v133, v140
	v_pk_mul_f32 v[128:129], v[76:77], v[128:129]
	v_pk_mul_f32 v[130:131], v[78:79], v[130:131]
	v_pk_mul_f32 v[134:135], v[74:75], v[134:135]
	v_pk_mul_f32 v[132:133], v[72:73], v[132:133]
; __device__ __forceinline__ unsigned cvt_pk_bf16(float lo, float hi) { const bf16x2_t r = __builtin_convertvector((f32x2_t){lo, hi}, bf16x2_t); return __builtin_bit_cast(unsigned, r); }
; __device__ __forceinline__ float silu_fast(float x) { return x * __builtin_amdgcn_rcpf(1.0f + __builtin_amdgcn_exp2f(-x * 1.4426950408889634f)); }
;     __device__ __forceinline__ void operator()(const f32x4 (&acc)[2][2][4][2], const Unit& u, int wr, int wc, int fr, int fq) const {
;     ...
;             for (int ai = 0; ai < 2; ++ai)
; #pragma unroll
;                 for (int m = 0; m < 4; ++m) {
;                     const int r = row0 + ai * HALF + m * 16;
; #pragma unroll
;                     for (int bj = 0; bj < 2; ++bj) {
;                         f32x4 v0 = acc[ai][bj][m][0], v1 = acc[ai][bj][m][1];
;                         if (isog) {
; #pragma unroll
;                             for (int i = 0; i < 4; ++i) { v0[i] = silu_fast(v0[i]); v1[i] = silu_fast(v1[i]); }
;                         }
;                         u32x4 o; o[0] = cvt_pk_bf16(v0[0], v0[1]); o[1] = cvt_pk_bf16(v0[2], v0[3]); o[2] = cvt_pk_bf16(v1[0], v1[1]); o[3] = cvt_pk_bf16(v1[2], v1[3]);
;                         __builtin_nontemporal_store(o, (u32x4*)(dst + ((size_t)((r >> 11) * 4 + (cb >> 8)) * SEQ + (r & (SEQ - 1))) * 256 + bj * HALF + lc));
;                     }
;                 }
.LBB0_337:
	v_cvt_pk_bf16_f32 v128, v128, v129
	v_cvt_pk_bf16_f32 v129, v130, v131
	v_cvt_pk_bf16_f32 v130, v132, v133
	v_add_co_u32_e32 v132, vcc, 0x6000, v138
	v_cvt_pk_bf16_f32 v131, v134, v135
	s_nop 0
	v_addc_co_u32_e32 v133, vcc, 0, v139, vcc
	global_store_dwordx4 v[132:133], v[128:131], off
	v_mov_b64_e32 v[134:135], v[66:67]
	s_and_b64 vcc, exec, s[8:9]
	v_mov_b64_e32 v[130:131], v[70:71]
	v_mov_b64_e32 v[128:129], v[68:69]
	v_mov_b64_e32 v[132:133], v[64:65]
	s_cbranch_vccnz .LBB0_339
	v_mul_f32_e32 v129, 0xbfb8aa3b, v64
	v_mul_f32_e32 v130, 0xbfb8aa3b, v69
	v_exp_f32_e32 v129, v129
	v_exp_f32_e32 v130, v130
	v_mul_f32_e32 v131, 0xbfb8aa3b, v70
	v_mul_f32_e32 v133, 0xbfb8aa3b, v66
	v_add_f32_e32 v129, 1.0, v129
	v_rcp_f32_e32 v132, v129
	v_add_f32_e32 v129, 1.0, v130
	v_mul_f32_e32 v130, 0xbfb8aa3b, v65
	v_exp_f32_e32 v130, v130
	v_exp_f32_e32 v131, v131
	v_exp_f32_e32 v133, v133
	v_mul_f32_e32 v128, 0xbfb8aa3b, v68
	v_add_f32_e32 v140, 1.0, v130
	v_add_f32_e32 v130, 1.0, v131
	v_add_f32_e32 v131, 1.0, v133
	v_mul_f32_e32 v133, 0xbfb8aa3b, v71
	v_mul_f32_e32 v134, 0xbfb8aa3b, v67
	v_exp_f32_e32 v128, v128
	v_exp_f32_e32 v133, v133
	v_exp_f32_e32 v135, v134
	v_rcp_f32_e32 v134, v131
	v_add_f32_e32 v128, 1.0, v128
	v_add_f32_e32 v131, 1.0, v133
	v_add_f32_e32 v133, 1.0, v135
	v_rcp_f32_e32 v128, v128
	v_rcp_f32_e32 v129, v129
	v_rcp_f32_e32 v130, v130
	v_rcp_f32_e32 v131, v131
	v_rcp_f32_e32 v135, v133
	v_rcp_f32_e32 v133, v140
	v_pk_mul_f32 v[128:129], v[68:69], v[128:129]
	v_pk_mul_f32 v[130:131], v[70:71], v[130:131]
	v_pk_mul_f32 v[134:135], v[66:67], v[134:135]
	v_pk_mul_f32 v[132:133], v[64:65], v[132:133]
.LBB0_339:
	v_cvt_pk_bf16_f32 v128, v128, v129
	v_cvt_pk_bf16_f32 v129, v130, v131
	v_cvt_pk_bf16_f32 v130, v132, v133
	v_add_co_u32_e32 v132, vcc, 0x6000, v138
	v_cvt_pk_bf16_f32 v131, v134, v135
	s_nop 0
	v_addc_co_u32_e32 v133, vcc, 0, v139, vcc
	global_store_dwordx4 v[132:133], v[128:131], off offset:256
	v_mov_b64_e32 v[134:135], v[58:59]
	s_and_b64 vcc, exec, s[8:9]
	v_mov_b64_e32 v[130:131], v[62:63]
	v_mov_b64_e32 v[128:129], v[60:61]
	v_mov_b64_e32 v[132:133], v[56:57]
	s_cbranch_vccnz .LBB0_341
	v_mul_f32_e32 v129, 0xbfb8aa3b, v56
	v_mul_f32_e32 v130, 0xbfb8aa3b, v61
	v_exp_f32_e32 v129, v129
	v_exp_f32_e32 v130, v130
	v_mul_f32_e32 v131, 0xbfb8aa3b, v62
	v_mul_f32_e32 v133, 0xbfb8aa3b, v58
	v_add_f32_e32 v129, 1.0, v129
	v_rcp_f32_e32 v132, v129
	v_add_f32_e32 v129, 1.0, v130
	v_mul_f32_e32 v130, 0xbfb8aa3b, v57
	v_exp_f32_e32 v130, v130
	v_exp_f32_e32 v131, v131
	v_exp_f32_e32 v133, v133
	v_mul_f32_e32 v128, 0xbfb8aa3b, v60
	v_add_f32_e32 v138, 1.0, v130
	v_add_f32_e32 v130, 1.0, v131
	v_add_f32_e32 v131, 1.0, v133
	v_mul_f32_e32 v133, 0xbfb8aa3b, v63
	v_mul_f32_e32 v134, 0xbfb8aa3b, v59
	v_exp_f32_e32 v128, v128
	v_exp_f32_e32 v133, v133
	v_exp_f32_e32 v135, v134
	v_rcp_f32_e32 v134, v131
	v_add_f32_e32 v128, 1.0, v128
	v_add_f32_e32 v131, 1.0, v133
	v_add_f32_e32 v133, 1.0, v135
	v_rcp_f32_e32 v128, v128
	v_rcp_f32_e32 v129, v129
	v_rcp_f32_e32 v130, v130
	v_rcp_f32_e32 v131, v131
	v_rcp_f32_e32 v135, v133
	v_rcp_f32_e32 v133, v138
	v_pk_mul_f32 v[128:129], v[60:61], v[128:129]
	v_pk_mul_f32 v[130:131], v[62:63], v[130:131]
	v_pk_mul_f32 v[134:135], v[58:59], v[134:135]
	v_pk_mul_f32 v[132:133], v[56:57], v[132:133]
.LBB0_341:
	v_add_u32_e32 v140, 0x80, v192
	v_ashrrev_i32_e32 v138, 9, v140
	v_and_b32_e32 v138, -4, v138
	v_add_u32_e32 v138, s10, v138
	v_ashrrev_i32_e32 v139, 31, v138
	v_lshlrev_b64 v[138:139], 20, v[138:139]
	v_lshl_add_u64 v[136:137], v[136:137], 0, v[138:139]
	v_lshlrev_b32_e32 v138, 9, v140
	v_and_b32_e32 v168, 0xf9e00, v138
	v_lshl_add_u64 v[136:137], v[136:137], 0, v[168:169]
	v_cvt_pk_bf16_f32 v128, v128, v129
	v_cvt_pk_bf16_f32 v129, v130, v131
	v_cvt_pk_bf16_f32 v130, v132, v133
	v_cvt_pk_bf16_f32 v131, v134, v135
	global_store_dwordx4 v[136:137], v[128:131], off
	v_mov_b64_e32 v[134:135], v[50:51]
	s_and_b64 vcc, exec, s[8:9]
	v_mov_b64_e32 v[130:131], v[54:55]
	v_mov_b64_e32 v[128:129], v[52:53]
	v_mov_b64_e32 v[132:133], v[48:49]
	s_cbranch_vccnz .LBB0_343
	v_mul_f32_e32 v129, 0xbfb8aa3b, v48
	v_mul_f32_e32 v130, 0xbfb8aa3b, v53
	v_exp_f32_e32 v129, v129
	v_exp_f32_e32 v130, v130
	v_mul_f32_e32 v131, 0xbfb8aa3b, v54
	v_mul_f32_e32 v133, 0xbfb8aa3b, v50
	v_add_f32_e32 v129, 1.0, v129
	v_rcp_f32_e32 v132, v129
	v_add_f32_e32 v129, 1.0, v130
	v_mul_f32_e32 v130, 0xbfb8aa3b, v49
	v_exp_f32_e32 v130, v130
	v_exp_f32_e32 v131, v131
	v_exp_f32_e32 v133, v133
	v_mul_f32_e32 v128, 0xbfb8aa3b, v52
	v_add_f32_e32 v138, 1.0, v130
	v_add_f32_e32 v130, 1.0, v131
	v_add_f32_e32 v131, 1.0, v133
	v_mul_f32_e32 v133, 0xbfb8aa3b, v55
	v_mul_f32_e32 v134, 0xbfb8aa3b, v51
	v_exp_f32_e32 v128, v128
	v_exp_f32_e32 v133, v133
	v_exp_f32_e32 v135, v134
	v_rcp_f32_e32 v134, v131
	v_add_f32_e32 v128, 1.0, v128
	v_add_f32_e32 v131, 1.0, v133
	v_add_f32_e32 v133, 1.0, v135
	v_rcp_f32_e32 v128, v128
	v_rcp_f32_e32 v129, v129
	v_rcp_f32_e32 v130, v130
	v_rcp_f32_e32 v131, v131
	v_rcp_f32_e32 v135, v133
	v_rcp_f32_e32 v133, v138
	v_pk_mul_f32 v[128:129], v[52:53], v[128:129]
	v_pk_mul_f32 v[130:131], v[54:55], v[130:131]
	v_pk_mul_f32 v[134:135], v[50:51], v[134:135]
	v_pk_mul_f32 v[132:133], v[48:49], v[132:133]
; __device__ __forceinline__ unsigned cvt_pk_bf16(float lo, float hi) { const bf16x2_t r = __builtin_convertvector((f32x2_t){lo, hi}, bf16x2_t); return __builtin_bit_cast(unsigned, r); }
; __device__ __forceinline__ float silu_fast(float x) { return x * __builtin_amdgcn_rcpf(1.0f + __builtin_amdgcn_exp2f(-x * 1.4426950408889634f)); }
;     __device__ __forceinline__ void operator()(const f32x4 (&acc)[2][2][4][2], const Unit& u, int wr, int wc, int fr, int fq) const {
;     ...
;             for (int ai = 0; ai < 2; ++ai)
; #pragma unroll
;                 for (int m = 0; m < 4; ++m) {
;                     const int r = row0 + ai * HALF + m * 16;
; #pragma unroll
;                     for (int bj = 0; bj < 2; ++bj) {
;                         f32x4 v0 = acc[ai][bj][m][0], v1 = acc[ai][bj][m][1];
;                         if (isog) {
; #pragma unroll
;                             for (int i = 0; i < 4; ++i) { v0[i] = silu_fast(v0[i]); v1[i] = silu_fast(v1[i]); }
;                         }
;                         u32x4 o; o[0] = cvt_pk_bf16(v0[0], v0[1]); o[1] = cvt_pk_bf16(v0[2], v0[3]); o[2] = cvt_pk_bf16(v1[0], v1[1]); o[3] = cvt_pk_bf16(v1[2], v1[3]);
;                         __builtin_nontemporal_store(o, (u32x4*)(dst + ((size_t)((r >> 11) * 4 + (cb >> 8)) * SEQ + (r & (SEQ - 1))) * 256 + bj * HALF + lc));
;                     }
;                 }
.LBB0_343:
	v_cvt_pk_bf16_f32 v128, v128, v129
	v_cvt_pk_bf16_f32 v129, v130, v131
	v_cvt_pk_bf16_f32 v130, v132, v133
	v_cvt_pk_bf16_f32 v131, v134, v135
	global_store_dwordx4 v[136:137], v[128:131], off offset:256
	v_mov_b64_e32 v[134:135], v[42:43]
	s_and_b64 vcc, exec, s[8:9]
	v_mov_b64_e32 v[130:131], v[46:47]
	v_mov_b64_e32 v[128:129], v[44:45]
	v_mov_b64_e32 v[132:133], v[40:41]
	s_cbranch_vccnz .LBB0_345
	v_mul_f32_e32 v129, 0xbfb8aa3b, v40
	v_mul_f32_e32 v130, 0xbfb8aa3b, v45
	v_exp_f32_e32 v129, v129
	v_exp_f32_e32 v130, v130
	v_mul_f32_e32 v131, 0xbfb8aa3b, v46
	v_mul_f32_e32 v133, 0xbfb8aa3b, v42
	v_add_f32_e32 v129, 1.0, v129
	v_rcp_f32_e32 v132, v129
	v_add_f32_e32 v129, 1.0, v130
	v_mul_f32_e32 v130, 0xbfb8aa3b, v41
	v_exp_f32_e32 v130, v130
	v_exp_f32_e32 v131, v131
	v_exp_f32_e32 v133, v133
	v_mul_f32_e32 v128, 0xbfb8aa3b, v44
	v_add_f32_e32 v138, 1.0, v130
	v_add_f32_e32 v130, 1.0, v131
	v_add_f32_e32 v131, 1.0, v133
	v_mul_f32_e32 v133, 0xbfb8aa3b, v47
	v_mul_f32_e32 v134, 0xbfb8aa3b, v43
	v_exp_f32_e32 v128, v128
	v_exp_f32_e32 v133, v133
	v_exp_f32_e32 v135, v134
	v_rcp_f32_e32 v134, v131
	v_add_f32_e32 v128, 1.0, v128
	v_add_f32_e32 v131, 1.0, v133
	v_add_f32_e32 v133, 1.0, v135
	v_rcp_f32_e32 v128, v128
	v_rcp_f32_e32 v129, v129
	v_rcp_f32_e32 v130, v130
	v_rcp_f32_e32 v131, v131
	v_rcp_f32_e32 v135, v133
	v_rcp_f32_e32 v133, v138
	v_pk_mul_f32 v[128:129], v[44:45], v[128:129]
	v_pk_mul_f32 v[130:131], v[46:47], v[130:131]
	v_pk_mul_f32 v[134:135], v[42:43], v[134:135]
	v_pk_mul_f32 v[132:133], v[40:41], v[132:133]
.LBB0_345:
	v_cvt_pk_bf16_f32 v128, v128, v129
	v_cvt_pk_bf16_f32 v129, v130, v131
	v_cvt_pk_bf16_f32 v130, v132, v133
	v_add_co_u32_e32 v132, vcc, 0x2000, v136
	v_cvt_pk_bf16_f32 v131, v134, v135
	s_nop 0
	v_addc_co_u32_e32 v133, vcc, 0, v137, vcc
	global_store_dwordx4 v[132:133], v[128:131], off
	v_mov_b64_e32 v[134:135], v[34:35]
	s_and_b64 vcc, exec, s[8:9]
	v_mov_b64_e32 v[130:131], v[38:39]
	v_mov_b64_e32 v[128:129], v[36:37]
	v_mov_b64_e32 v[132:133], v[32:33]
	s_cbranch_vccnz .LBB0_347
	v_mul_f32_e32 v129, 0xbfb8aa3b, v32
	v_mul_f32_e32 v130, 0xbfb8aa3b, v37
	v_exp_f32_e32 v129, v129
	v_exp_f32_e32 v130, v130
	v_mul_f32_e32 v131, 0xbfb8aa3b, v38
	v_mul_f32_e32 v133, 0xbfb8aa3b, v34
	v_add_f32_e32 v129, 1.0, v129
	v_rcp_f32_e32 v132, v129
	v_add_f32_e32 v129, 1.0, v130
	v_mul_f32_e32 v130, 0xbfb8aa3b, v33
	v_exp_f32_e32 v130, v130
	v_exp_f32_e32 v131, v131
	v_exp_f32_e32 v133, v133
	v_mul_f32_e32 v128, 0xbfb8aa3b, v36
	v_add_f32_e32 v138, 1.0, v130
	v_add_f32_e32 v130, 1.0, v131
	v_add_f32_e32 v131, 1.0, v133
	v_mul_f32_e32 v133, 0xbfb8aa3b, v39
	v_mul_f32_e32 v134, 0xbfb8aa3b, v35
	v_exp_f32_e32 v128, v128
	v_exp_f32_e32 v133, v133
	v_exp_f32_e32 v135, v134
	v_rcp_f32_e32 v134, v131
	v_add_f32_e32 v128, 1.0, v128
	v_add_f32_e32 v131, 1.0, v133
	v_add_f32_e32 v133, 1.0, v135
	v_rcp_f32_e32 v128, v128
	v_rcp_f32_e32 v129, v129
	v_rcp_f32_e32 v130, v130
	v_rcp_f32_e32 v131, v131
	v_rcp_f32_e32 v135, v133
	v_rcp_f32_e32 v133, v138
	v_pk_mul_f32 v[128:129], v[36:37], v[128:129]
	v_pk_mul_f32 v[130:131], v[38:39], v[130:131]
	v_pk_mul_f32 v[134:135], v[34:35], v[134:135]
	v_pk_mul_f32 v[132:133], v[32:33], v[132:133]
.LBB0_347:
	v_cvt_pk_bf16_f32 v128, v128, v129
	v_cvt_pk_bf16_f32 v129, v130, v131
	v_cvt_pk_bf16_f32 v130, v132, v133
	v_add_co_u32_e32 v132, vcc, 0x2000, v136
	v_cvt_pk_bf16_f32 v131, v134, v135
	s_nop 0
	v_addc_co_u32_e32 v133, vcc, 0, v137, vcc
	global_store_dwordx4 v[132:133], v[128:131], off offset:256
	v_mov_b64_e32 v[134:135], v[26:27]
	s_and_b64 vcc, exec, s[8:9]
	v_mov_b64_e32 v[130:131], v[30:31]
	v_mov_b64_e32 v[128:129], v[28:29]
	v_mov_b64_e32 v[132:133], v[24:25]
	s_cbranch_vccnz .LBB0_349
	v_mul_f32_e32 v129, 0xbfb8aa3b, v24
	v_mul_f32_e32 v130, 0xbfb8aa3b, v29
	v_exp_f32_e32 v129, v129
	v_exp_f32_e32 v130, v130
	v_mul_f32_e32 v131, 0xbfb8aa3b, v30
	v_mul_f32_e32 v133, 0xbfb8aa3b, v26
	v_add_f32_e32 v129, 1.0, v129
	v_rcp_f32_e32 v132, v129
	v_add_f32_e32 v129, 1.0, v130
	v_mul_f32_e32 v130, 0xbfb8aa3b, v25
	v_exp_f32_e32 v130, v130
	v_exp_f32_e32 v131, v131
	v_exp_f32_e32 v133, v133
	v_mul_f32_e32 v128, 0xbfb8aa3b, v28
	v_add_f32_e32 v138, 1.0, v130
	v_add_f32_e32 v130, 1.0, v131
	v_add_f32_e32 v131, 1.0, v133
	v_mul_f32_e32 v133, 0xbfb8aa3b, v31
	v_mul_f32_e32 v134, 0xbfb8aa3b, v27
	v_exp_f32_e32 v128, v128
	v_exp_f32_e32 v133, v133
	v_exp_f32_e32 v135, v134
	v_rcp_f32_e32 v134, v131
	v_add_f32_e32 v128, 1.0, v128
	v_add_f32_e32 v131, 1.0, v133
	v_add_f32_e32 v133, 1.0, v135
	v_rcp_f32_e32 v128, v128
	v_rcp_f32_e32 v129, v129
	v_rcp_f32_e32 v130, v130
	v_rcp_f32_e32 v131, v131
	v_rcp_f32_e32 v135, v133
	v_rcp_f32_e32 v133, v138
	v_pk_mul_f32 v[128:129], v[28:29], v[128:129]
	v_pk_mul_f32 v[130:131], v[30:31], v[130:131]
	v_pk_mul_f32 v[134:135], v[26:27], v[134:135]
	v_pk_mul_f32 v[132:133], v[24:25], v[132:133]
; __device__ __forceinline__ unsigned cvt_pk_bf16(float lo, float hi) { const bf16x2_t r = __builtin_convertvector((f32x2_t){lo, hi}, bf16x2_t); return __builtin_bit_cast(unsigned, r); }
; __device__ __forceinline__ float silu_fast(float x) { return x * __builtin_amdgcn_rcpf(1.0f + __builtin_amdgcn_exp2f(-x * 1.4426950408889634f)); }
;     __device__ __forceinline__ void operator()(const f32x4 (&acc)[2][2][4][2], const Unit& u, int wr, int wc, int fr, int fq) const {
;     ...
;             for (int ai = 0; ai < 2; ++ai)
; #pragma unroll
;                 for (int m = 0; m < 4; ++m) {
;                     const int r = row0 + ai * HALF + m * 16;
; #pragma unroll
;                     for (int bj = 0; bj < 2; ++bj) {
;                         f32x4 v0 = acc[ai][bj][m][0], v1 = acc[ai][bj][m][1];
;                         if (isog) {
; #pragma unroll
;                             for (int i = 0; i < 4; ++i) { v0[i] = silu_fast(v0[i]); v1[i] = silu_fast(v1[i]); }
;                         }
;                         u32x4 o; o[0] = cvt_pk_bf16(v0[0], v0[1]); o[1] = cvt_pk_bf16(v0[2], v0[3]); o[2] = cvt_pk_bf16(v1[0], v1[1]); o[3] = cvt_pk_bf16(v1[2], v1[3]);
;                         __builtin_nontemporal_store(o, (u32x4*)(dst + ((size_t)((r >> 11) * 4 + (cb >> 8)) * SEQ + (r & (SEQ - 1))) * 256 + bj * HALF + lc));
;                     }
;                 }
.LBB0_349:
	v_cvt_pk_bf16_f32 v128, v128, v129
	v_cvt_pk_bf16_f32 v129, v130, v131
	v_cvt_pk_bf16_f32 v130, v132, v133
	v_add_co_u32_e32 v132, vcc, 0x4000, v136
	v_cvt_pk_bf16_f32 v131, v134, v135
	s_nop 0
	v_addc_co_u32_e32 v133, vcc, 0, v137, vcc
	global_store_dwordx4 v[132:133], v[128:131], off
	v_mov_b64_e32 v[134:135], v[18:19]
	s_and_b64 vcc, exec, s[8:9]
	v_mov_b64_e32 v[130:131], v[22:23]
	v_mov_b64_e32 v[128:129], v[20:21]
	v_mov_b64_e32 v[132:133], v[16:17]
	s_cbranch_vccnz .LBB0_351
	v_mul_f32_e32 v129, 0xbfb8aa3b, v16
	v_mul_f32_e32 v130, 0xbfb8aa3b, v21
	v_exp_f32_e32 v129, v129
	v_exp_f32_e32 v130, v130
	v_mul_f32_e32 v131, 0xbfb8aa3b, v22
	v_mul_f32_e32 v133, 0xbfb8aa3b, v18
	v_add_f32_e32 v129, 1.0, v129
	v_rcp_f32_e32 v132, v129
	v_add_f32_e32 v129, 1.0, v130
	v_mul_f32_e32 v130, 0xbfb8aa3b, v17
	v_exp_f32_e32 v130, v130
	v_exp_f32_e32 v131, v131
	v_exp_f32_e32 v133, v133
	v_mul_f32_e32 v128, 0xbfb8aa3b, v20
	v_add_f32_e32 v138, 1.0, v130
	v_add_f32_e32 v130, 1.0, v131
	v_add_f32_e32 v131, 1.0, v133
	v_mul_f32_e32 v133, 0xbfb8aa3b, v23
	v_mul_f32_e32 v134, 0xbfb8aa3b, v19
	v_exp_f32_e32 v128, v128
	v_exp_f32_e32 v133, v133
	v_exp_f32_e32 v135, v134
	v_rcp_f32_e32 v134, v131
	v_add_f32_e32 v128, 1.0, v128
	v_add_f32_e32 v131, 1.0, v133
	v_add_f32_e32 v133, 1.0, v135
	v_rcp_f32_e32 v128, v128
	v_rcp_f32_e32 v129, v129
	v_rcp_f32_e32 v130, v130
	v_rcp_f32_e32 v131, v131
	v_rcp_f32_e32 v135, v133
	v_rcp_f32_e32 v133, v138
	v_pk_mul_f32 v[128:129], v[20:21], v[128:129]
	v_pk_mul_f32 v[130:131], v[22:23], v[130:131]
	v_pk_mul_f32 v[134:135], v[18:19], v[134:135]
	v_pk_mul_f32 v[132:133], v[16:17], v[132:133]
.LBB0_351:
	v_cvt_pk_bf16_f32 v128, v128, v129
	v_cvt_pk_bf16_f32 v129, v130, v131
	v_cvt_pk_bf16_f32 v130, v132, v133
	v_add_co_u32_e32 v132, vcc, 0x4000, v136
	v_cvt_pk_bf16_f32 v131, v134, v135
	s_nop 0
	v_addc_co_u32_e32 v133, vcc, 0, v137, vcc
	global_store_dwordx4 v[132:133], v[128:131], off offset:256
	v_mov_b64_e32 v[134:135], v[10:11]
	s_and_b64 vcc, exec, s[8:9]
	v_mov_b64_e32 v[130:131], v[14:15]
	v_mov_b64_e32 v[128:129], v[12:13]
	v_mov_b64_e32 v[132:133], v[8:9]
	s_cbranch_vccnz .LBB0_353
	v_mul_f32_e32 v129, 0xbfb8aa3b, v8
	v_mul_f32_e32 v130, 0xbfb8aa3b, v13
	v_exp_f32_e32 v129, v129
	v_exp_f32_e32 v130, v130
	v_mul_f32_e32 v131, 0xbfb8aa3b, v14
	v_mul_f32_e32 v133, 0xbfb8aa3b, v10
	v_add_f32_e32 v129, 1.0, v129
	v_rcp_f32_e32 v132, v129
	v_add_f32_e32 v129, 1.0, v130
	v_mul_f32_e32 v130, 0xbfb8aa3b, v9
	v_exp_f32_e32 v130, v130
	v_exp_f32_e32 v131, v131
	v_exp_f32_e32 v133, v133
	v_mul_f32_e32 v128, 0xbfb8aa3b, v12
	v_add_f32_e32 v138, 1.0, v130
	v_add_f32_e32 v130, 1.0, v131
	v_add_f32_e32 v131, 1.0, v133
	v_mul_f32_e32 v133, 0xbfb8aa3b, v15
	v_mul_f32_e32 v134, 0xbfb8aa3b, v11
	v_exp_f32_e32 v128, v128
	v_exp_f32_e32 v133, v133
	v_exp_f32_e32 v135, v134
	v_rcp_f32_e32 v134, v131
	v_add_f32_e32 v128, 1.0, v128
	v_add_f32_e32 v131, 1.0, v133
	v_add_f32_e32 v133, 1.0, v135
	v_rcp_f32_e32 v128, v128
	v_rcp_f32_e32 v129, v129
	v_rcp_f32_e32 v130, v130
	v_rcp_f32_e32 v131, v131
	v_rcp_f32_e32 v135, v133
	v_rcp_f32_e32 v133, v138
	v_pk_mul_f32 v[128:129], v[12:13], v[128:129]
	v_pk_mul_f32 v[130:131], v[14:15], v[130:131]
	v_pk_mul_f32 v[134:135], v[10:11], v[134:135]
	v_pk_mul_f32 v[132:133], v[8:9], v[132:133]
.LBB0_353:
	v_cvt_pk_bf16_f32 v128, v128, v129
	v_cvt_pk_bf16_f32 v129, v130, v131
	v_cvt_pk_bf16_f32 v130, v132, v133
	v_add_co_u32_e32 v132, vcc, 0x6000, v136
	v_cvt_pk_bf16_f32 v131, v134, v135
	s_nop 0
	v_addc_co_u32_e32 v133, vcc, 0, v137, vcc
	global_store_dwordx4 v[132:133], v[128:131], off
	v_mov_b64_e32 v[134:135], v[2:3]
	s_and_b64 vcc, exec, s[8:9]
	v_mov_b64_e32 v[130:131], v[6:7]
	v_mov_b64_e32 v[128:129], v[4:5]
	v_mov_b64_e32 v[132:133], v[0:1]
	s_cbranch_vccnz .LBB0_355
	v_mul_f32_e32 v129, 0xbfb8aa3b, v0
	v_mul_f32_e32 v130, 0xbfb8aa3b, v5
	v_exp_f32_e32 v129, v129
	v_exp_f32_e32 v130, v130
	v_mul_f32_e32 v131, 0xbfb8aa3b, v6
	v_mul_f32_e32 v133, 0xbfb8aa3b, v2
	v_add_f32_e32 v129, 1.0, v129
	v_rcp_f32_e32 v132, v129
	v_add_f32_e32 v129, 1.0, v130
	v_mul_f32_e32 v130, 0xbfb8aa3b, v1
	v_exp_f32_e32 v130, v130
	v_exp_f32_e32 v131, v131
	v_exp_f32_e32 v133, v133
	v_mul_f32_e32 v128, 0xbfb8aa3b, v4
	v_add_f32_e32 v138, 1.0, v130
	v_add_f32_e32 v130, 1.0, v131
	v_add_f32_e32 v131, 1.0, v133
	v_mul_f32_e32 v133, 0xbfb8aa3b, v7
	v_mul_f32_e32 v134, 0xbfb8aa3b, v3
	v_exp_f32_e32 v128, v128
	v_exp_f32_e32 v133, v133
	v_exp_f32_e32 v135, v134
	v_rcp_f32_e32 v134, v131
	v_add_f32_e32 v128, 1.0, v128
	v_add_f32_e32 v131, 1.0, v133
	v_add_f32_e32 v133, 1.0, v135
	v_rcp_f32_e32 v128, v128
	v_rcp_f32_e32 v129, v129
	v_rcp_f32_e32 v130, v130
	v_rcp_f32_e32 v131, v131
	v_rcp_f32_e32 v135, v133
	v_rcp_f32_e32 v133, v138
	v_pk_mul_f32 v[128:129], v[4:5], v[128:129]
	v_pk_mul_f32 v[130:131], v[6:7], v[130:131]
	v_pk_mul_f32 v[134:135], v[2:3], v[134:135]
	v_pk_mul_f32 v[132:133], v[0:1], v[132:133]
.LBB0_355:
	v_cvt_pk_bf16_f32 v128, v128, v129
	v_cvt_pk_bf16_f32 v129, v130, v131
	v_cvt_pk_bf16_f32 v130, v132, v133
	v_add_co_u32_e32 v132, vcc, 0x6000, v136
	v_cvt_pk_bf16_f32 v131, v134, v135
	s_nop 0
	v_addc_co_u32_e32 v133, vcc, 0, v137, vcc
	global_store_dwordx4 v[132:133], v[128:131], off offset:256
	s_mov_b64 s[2:3], 0

;     __device__ __forceinline__ void operator()(const f32x4 (&acc)[2][2][4][2], const Unit& u, int wr, int wc, int fr, int fq) const {
;     ...
;             BC_LOAD(0, 0);
; #pragma unroll
;             for (int g = 0; g < 16; ++g) {
;                 const int ai = g >> 3, m = (g >> 1) & 3, bj = g & 1;
;                 const int r = row0 + ai * HALF + m * 16;
;                 if (g + 1 < 16) BC_LOAD((g + 1) & 1, g + 1);
;                 {
;                     {
;                         const int col = cb + bj * HALF + lc;
;                         const size_t hoff = ((size_t)((r >> 11) * 4 + (col >> 7)) * SEQ + (r & (SEQ - 1))) * 128 + (col & 127);
;                         const f32x4 b0 = bc[g & 1][0], b1 = bc[g & 1][1];
;                         const f32x4 v0 = acc[ai][bj][m][0], v1 = acc[ai][bj][m][1];
;                         const float L2E = 1.4426950408889634f;
;                         if (isq) {
;                             const float s = 0.08838834764831845f;
;                             u32x4 o; o[0] = cvt_pk_bf16(v0[0] * s * __builtin_amdgcn_exp2f(b0[0] * L2E), v0[1] * s * __builtin_amdgcn_exp2f(b0[1] * L2E));
;                             o[1] = cvt_pk_bf16(v0[2] * s * __builtin_amdgcn_exp2f(b0[2] * L2E), v0[3] * s * __builtin_amdgcn_exp2f(b0[3] * L2E));
;                             o[2] = cvt_pk_bf16(v1[0] * s * __builtin_amdgcn_exp2f(b1[0] * L2E), v1[1] * s * __builtin_amdgcn_exp2f(b1[1] * L2E));
;                             o[3] = cvt_pk_bf16(v1[2] * s * __builtin_amdgcn_exp2f(b1[2] * L2E), v1[3] * s * __builtin_amdgcn_exp2f(b1[3] * L2E));
;                             __builtin_nontemporal_store(o, (u32x4*)(d0 + hoff));
;                         } else {
;                             u32x4 o;
;                             o[0] = cvt_pk_bf16(v0[0] * __builtin_amdgcn_exp2f(-b0[0] * L2E), v0[1] * __builtin_amdgcn_exp2f(-b0[1] * L2E));
;                             o[1] = cvt_pk_bf16(v0[2] * __builtin_amdgcn_exp2f(-b0[2] * L2E), v0[3] * __builtin_amdgcn_exp2f(-b0[3] * L2E));
;                             o[2] = cvt_pk_bf16(v1[0] * __builtin_amdgcn_exp2f(-b1[0] * L2E), v1[1] * __builtin_amdgcn_exp2f(-b1[1] * L2E));
;                             o[3] = cvt_pk_bf16(v1[2] * __builtin_amdgcn_exp2f(-b1[2] * L2E), v1[3] * __builtin_amdgcn_exp2f(-b1[3] * L2E));
;                             __builtin_nontemporal_store(o, (u32x4*)(d0 + hoff));
.LBB0_361:
	s_and_b64 s[2:3], s[2:3], exec
	s_mov_b32 s2, 0x46188000
	s_cselect_b32 s2, s2, 0x47188000
	v_readlane_b32 s80, v252, 28
	v_readlane_b32 s81, v252, 29
	s_add_u32 s2, s80, s2
	s_addc_u32 s3, s81, 0
	s_ashr_i32 s9, s15, 9
	s_and_b32 s33, s9, -4
	s_lshl_b32 s17, s10, 1
	s_waitcnt vmcnt(2)
	v_mul_f32_e32 v132, s8, v135
	s_add_i32 s10, s33, s17
	v_exp_f32_e32 v132, v132
	s_ashr_i32 s11, s10, 31
	v_lshlrev_b32_e32 v133, 7, v192
	s_lshl_b64 s[8:9], s[10:11], 19
	v_and_b32_e32 v156, 0x3e780, v133
	s_add_u32 s10, s2, s8
	v_mul_f32_e32 v132, v149, v132
	s_addc_u32 s11, s3, s9
	v_lshlrev_b32_e32 v150, 1, v156
	v_mov_b32_e32 v151, v169
	v_cvt_pk_bf16_f32 v143, v148, v132
	v_lshl_add_u64 v[132:133], s[10:11], 0, v[150:151]
	v_lshlrev_b32_e32 v148, 1, v170
	v_mov_b32_e32 v149, v169
	v_lshl_add_u64 v[132:133], v[132:133], 0, v[148:149]
	global_store_dwordx4 v[132:133], v[140:143], off
	v_or_b32_e32 v132, 16, v192
	v_ashrrev_i32_e32 v133, 31, v132
	v_lshlrev_b64 v[132:133], 11, v[132:133]
	v_lshl_add_u64 v[132:133], s[22:23], 0, v[132:133]
	v_lshl_add_u64 v[152:153], v[168:169], 2, v[132:133]
	global_load_dwordx4 v[132:135], v[152:153], off offset:16
	global_load_dwordx4 v[140:143], v[152:153], off
	s_waitcnt vmcnt(3)
	v_cndmask_b32_e64 v144, 0, 1, s[42:43]
	v_cmp_ne_u32_e64 s[8:9], 1, v144
	s_andn2_b64 vcc, exec, s[42:43]
	s_mov_b64 s[42:43], -1
	v_readlane_b32 s82, v252, 30
	v_readlane_b32 s83, v252, 31
	s_cbranch_vccnz .LBB0_363
	v_mul_f32_e32 v144, 0xbfb8aa3b, v136
	v_mul_f32_e32 v145, 0xbfb8aa3b, v137
	v_exp_f32_e32 v144, v144
	v_exp_f32_e32 v145, v145
	s_mov_b64 s[42:43], 0
	v_mov_b32_e32 v155, v115
	v_pk_mul_f32 v[144:145], v[116:117], v[144:145]
	s_nop 0
	v_cvt_pk_bf16_f32 v144, v144, v145
	v_mul_f32_e32 v145, 0xbfb8aa3b, v138
	v_exp_f32_e32 v146, v145
	v_mul_f32_e32 v145, 0xbfb8aa3b, v139
	v_exp_f32_e32 v147, v145
	s_nop 0
	v_pk_mul_f32 v[146:147], v[118:119], v[146:147]
	s_nop 0
	v_cvt_pk_bf16_f32 v145, v146, v147
	v_mul_f32_e32 v146, 0xbfb8aa3b, v128
	v_mul_f32_e32 v147, 0xbfb8aa3b, v129
	v_exp_f32_e32 v146, v146
	v_exp_f32_e32 v147, v147
	s_nop 0
	v_pk_mul_f32 v[146:147], v[112:113], v[146:147]
	s_nop 0
	v_cvt_pk_bf16_f32 v146, v146, v147
	v_mul_f32_e32 v147, 0xbfb8aa3b, v130
	v_exp_f32_e32 v147, v147
	s_nop 0
	v_mul_f32_e32 v154, v114, v147

;     __device__ __forceinline__ void operator()(const f32x4 (&acc)[2][2][4][2], const Unit& u, int wr, int wc, int fr, int fq) const {
;     ...
;             BC_LOAD(0, 0);
; #pragma unroll
;             for (int g = 0; g < 16; ++g) {
;                 const int ai = g >> 3, m = (g >> 1) & 3, bj = g & 1;
;                 const int r = row0 + ai * HALF + m * 16;
;                 if (g + 1 < 16) BC_LOAD((g + 1) & 1, g + 1);
;                 {
;                     {
;                         const int col = cb + bj * HALF + lc;
;                         const size_t hoff = ((size_t)((r >> 11) * 4 + (col >> 7)) * SEQ + (r & (SEQ - 1))) * 128 + (col & 127);
;                         const f32x4 b0 = bc[g & 1][0], b1 = bc[g & 1][1];
;                         const f32x4 v0 = acc[ai][bj][m][0], v1 = acc[ai][bj][m][1];
;                         const float L2E = 1.4426950408889634f;
;                         if (isq) {
;                             const float s = 0.08838834764831845f;
;                             u32x4 o; o[0] = cvt_pk_bf16(v0[0] * s * __builtin_amdgcn_exp2f(b0[0] * L2E), v0[1] * s * __builtin_amdgcn_exp2f(b0[1] * L2E));
;                             o[1] = cvt_pk_bf16(v0[2] * s * __builtin_amdgcn_exp2f(b0[2] * L2E), v0[3] * s * __builtin_amdgcn_exp2f(b0[3] * L2E));
;                             o[2] = cvt_pk_bf16(v1[0] * s * __builtin_amdgcn_exp2f(b1[0] * L2E), v1[1] * s * __builtin_amdgcn_exp2f(b1[1] * L2E));
;                             o[3] = cvt_pk_bf16(v1[2] * s * __builtin_amdgcn_exp2f(b1[2] * L2E), v1[3] * s * __builtin_amdgcn_exp2f(b1[3] * L2E));
;                             __builtin_nontemporal_store(o, (u32x4*)(d0 + hoff));
;                         } else {
;                             u32x4 o;
;                             o[0] = cvt_pk_bf16(v0[0] * __builtin_amdgcn_exp2f(-b0[0] * L2E), v0[1] * __builtin_amdgcn_exp2f(-b0[1] * L2E));
;                             o[1] = cvt_pk_bf16(v0[2] * __builtin_amdgcn_exp2f(-b0[2] * L2E), v0[3] * __builtin_amdgcn_exp2f(-b0[3] * L2E));
;                             o[2] = cvt_pk_bf16(v1[0] * __builtin_amdgcn_exp2f(-b1[0] * L2E), v1[1] * __builtin_amdgcn_exp2f(-b1[1] * L2E));
;                             o[3] = cvt_pk_bf16(v1[2] * __builtin_amdgcn_exp2f(-b1[2] * L2E), v1[3] * __builtin_amdgcn_exp2f(-b1[3] * L2E));
;                             __builtin_nontemporal_store(o, (u32x4*)(d0 + hoff));
.LBB0_365:
	v_mul_f32_e32 v128, s18, v131
	s_or_b32 s18, s17, 1
	v_exp_f32_e32 v128, v128
	s_add_i32 s42, s33, s18
	s_ashr_i32 s43, s42, 31
	s_lshl_b64 s[42:43], s[42:43], 19
	s_add_u32 s42, s2, s42
	v_mul_f32_e32 v128, v155, v128
	s_addc_u32 s43, s3, s43
	v_mov_b32_e32 v151, v169
	v_cvt_pk_bf16_f32 v147, v154, v128
	v_lshl_add_u64 v[128:129], s[42:43], 0, v[150:151]
	v_mov_b32_e32 v149, v169
	v_lshl_add_u64 v[128:129], v[128:129], 0, v[148:149]
	global_store_dwordx4 v[128:129], v[144:147], off
	global_load_dwordx4 v[128:131], v[152:153], off offset:528
	s_nop 0
	global_load_dwordx4 v[136:139], v[152:153], off offset:512
	s_and_b64 vcc, exec, s[8:9]
	s_mov_b64 s[54:55], -1
	s_cbranch_vccnz .LBB0_367
	s_waitcnt vmcnt(3)
	v_mul_f32_e32 v144, 0xbfb8aa3b, v140
	v_mul_f32_e32 v145, 0xbfb8aa3b, v141
	v_exp_f32_e32 v144, v144
	v_exp_f32_e32 v145, v145
	s_mov_b64 s[54:55], 0
	v_mov_b32_e32 v153, v107
	v_pk_mul_f32 v[144:145], v[108:109], v[144:145]
	s_nop 0
	v_cvt_pk_bf16_f32 v144, v144, v145
	v_mul_f32_e32 v145, 0xbfb8aa3b, v142
	v_exp_f32_e32 v146, v145
	v_mul_f32_e32 v145, 0xbfb8aa3b, v143
	v_exp_f32_e32 v147, v145
	s_nop 0
	v_pk_mul_f32 v[146:147], v[110:111], v[146:147]
	s_nop 0
	v_cvt_pk_bf16_f32 v145, v146, v147
	v_mul_f32_e32 v146, 0xbfb8aa3b, v132
	v_mul_f32_e32 v147, 0xbfb8aa3b, v133
	v_exp_f32_e32 v146, v146
	v_exp_f32_e32 v147, v147
	s_nop 0
	v_pk_mul_f32 v[146:147], v[104:105], v[146:147]
	s_nop 0
	v_cvt_pk_bf16_f32 v146, v146, v147
	v_mul_f32_e32 v147, 0xbfb8aa3b, v134
	v_exp_f32_e32 v147, v147
	s_nop 0
	v_mul_f32_e32 v152, v106, v147

;     __device__ __forceinline__ void operator()(const f32x4 (&acc)[2][2][4][2], const Unit& u, int wr, int wc, int fr, int fq) const {
;     ...
;             BC_LOAD(0, 0);
; #pragma unroll
;             for (int g = 0; g < 16; ++g) {
;                 const int ai = g >> 3, m = (g >> 1) & 3, bj = g & 1;
;                 const int r = row0 + ai * HALF + m * 16;
;                 if (g + 1 < 16) BC_LOAD((g + 1) & 1, g + 1);
;                 {
;                     {
;                         const int col = cb + bj * HALF + lc;
;                         const size_t hoff = ((size_t)((r >> 11) * 4 + (col >> 7)) * SEQ + (r & (SEQ - 1))) * 128 + (col & 127);
;                         const f32x4 b0 = bc[g & 1][0], b1 = bc[g & 1][1];
;                         const f32x4 v0 = acc[ai][bj][m][0], v1 = acc[ai][bj][m][1];
;                         const float L2E = 1.4426950408889634f;
;                         if (isq) {
;                             const float s = 0.08838834764831845f;
;                             u32x4 o; o[0] = cvt_pk_bf16(v0[0] * s * __builtin_amdgcn_exp2f(b0[0] * L2E), v0[1] * s * __builtin_amdgcn_exp2f(b0[1] * L2E));
;                             o[1] = cvt_pk_bf16(v0[2] * s * __builtin_amdgcn_exp2f(b0[2] * L2E), v0[3] * s * __builtin_amdgcn_exp2f(b0[3] * L2E));
;                             o[2] = cvt_pk_bf16(v1[0] * s * __builtin_amdgcn_exp2f(b1[0] * L2E), v1[1] * s * __builtin_amdgcn_exp2f(b1[1] * L2E));
;                             o[3] = cvt_pk_bf16(v1[2] * s * __builtin_amdgcn_exp2f(b1[2] * L2E), v1[3] * s * __builtin_amdgcn_exp2f(b1[3] * L2E));
;                             __builtin_nontemporal_store(o, (u32x4*)(d0 + hoff));
;                         } else {
;                             u32x4 o;
;                             o[0] = cvt_pk_bf16(v0[0] * __builtin_amdgcn_exp2f(-b0[0] * L2E), v0[1] * __builtin_amdgcn_exp2f(-b0[1] * L2E));
;                             o[1] = cvt_pk_bf16(v0[2] * __builtin_amdgcn_exp2f(-b0[2] * L2E), v0[3] * __builtin_amdgcn_exp2f(-b0[3] * L2E));
;                             o[2] = cvt_pk_bf16(v1[0] * __builtin_amdgcn_exp2f(-b1[0] * L2E), v1[1] * __builtin_amdgcn_exp2f(-b1[1] * L2E));
;                             o[3] = cvt_pk_bf16(v1[2] * __builtin_amdgcn_exp2f(-b1[2] * L2E), v1[3] * __builtin_amdgcn_exp2f(-b1[3] * L2E));
;                             __builtin_nontemporal_store(o, (u32x4*)(d0 + hoff));
.LBB0_369:
	s_waitcnt vmcnt(3)
	v_mul_f32_e32 v132, s33, v135
	v_exp_f32_e32 v132, v132
	v_or_b32_e32 v133, 0x800, v156
	v_mov_b32_e32 v151, v169
	v_lshlrev_b32_e32 v150, 1, v133
	v_mul_f32_e32 v132, v153, v132
	v_cvt_pk_bf16_f32 v147, v152, v132
	v_lshl_add_u64 v[132:133], s[10:11], 0, v[150:151]
	v_mov_b32_e32 v149, v169
	v_lshl_add_u64 v[132:133], v[132:133], 0, v[148:149]
	global_store_dwordx4 v[132:133], v[144:147], off
	v_or_b32_e32 v132, 32, v192
	v_ashrrev_i32_e32 v133, 31, v132
	v_lshlrev_b64 v[132:133], 11, v[132:133]
	v_lshl_add_u64 v[132:133], s[22:23], 0, v[132:133]
	v_lshl_add_u64 v[152:153], v[168:169], 2, v[132:133]
	global_load_dwordx4 v[132:135], v[152:153], off offset:16
	global_load_dwordx4 v[140:143], v[152:153], off
	s_waitcnt vmcnt(3)
	s_and_b64 vcc, exec, s[8:9]
	s_mov_b64 s[54:55], -1
	s_cbranch_vccnz .LBB0_371
	v_mul_f32_e32 v144, 0xbfb8aa3b, v136
	v_mul_f32_e32 v145, 0xbfb8aa3b, v137
	v_exp_f32_e32 v144, v144
	v_exp_f32_e32 v145, v145
	s_mov_b64 s[54:55], 0
	v_mov_b32_e32 v155, v99
	v_pk_mul_f32 v[144:145], v[100:101], v[144:145]
	s_nop 0
	v_cvt_pk_bf16_f32 v144, v144, v145
	v_mul_f32_e32 v145, 0xbfb8aa3b, v138
	v_exp_f32_e32 v146, v145
	v_mul_f32_e32 v145, 0xbfb8aa3b, v139
	v_exp_f32_e32 v147, v145
	s_nop 0
	v_pk_mul_f32 v[146:147], v[102:103], v[146:147]
	s_nop 0
	v_cvt_pk_bf16_f32 v145, v146, v147
	v_mul_f32_e32 v146, 0xbfb8aa3b, v128
	v_mul_f32_e32 v147, 0xbfb8aa3b, v129
	v_exp_f32_e32 v146, v146
	v_exp_f32_e32 v147, v147
	s_nop 0
	v_pk_mul_f32 v[146:147], v[96:97], v[146:147]
	s_nop 0
	v_cvt_pk_bf16_f32 v146, v146, v147
	v_mul_f32_e32 v147, 0xbfb8aa3b, v130
	v_exp_f32_e32 v147, v147
	s_nop 0
	v_mul_f32_e32 v154, v98, v147

;     __device__ __forceinline__ void operator()(const f32x4 (&acc)[2][2][4][2], const Unit& u, int wr, int wc, int fr, int fq) const {
;     ...
;             BC_LOAD(0, 0);
; #pragma unroll
;             for (int g = 0; g < 16; ++g) {
;                 const int ai = g >> 3, m = (g >> 1) & 3, bj = g & 1;
;                 const int r = row0 + ai * HALF + m * 16;
;                 if (g + 1 < 16) BC_LOAD((g + 1) & 1, g + 1);
;                 {
;                     {
;                         const int col = cb + bj * HALF + lc;
;                         const size_t hoff = ((size_t)((r >> 11) * 4 + (col >> 7)) * SEQ + (r & (SEQ - 1))) * 128 + (col & 127);
;                         const f32x4 b0 = bc[g & 1][0], b1 = bc[g & 1][1];
;                         const f32x4 v0 = acc[ai][bj][m][0], v1 = acc[ai][bj][m][1];
;                         const float L2E = 1.4426950408889634f;
;                         if (isq) {
;                             const float s = 0.08838834764831845f;
;                             u32x4 o; o[0] = cvt_pk_bf16(v0[0] * s * __builtin_amdgcn_exp2f(b0[0] * L2E), v0[1] * s * __builtin_amdgcn_exp2f(b0[1] * L2E));
;                             o[1] = cvt_pk_bf16(v0[2] * s * __builtin_amdgcn_exp2f(b0[2] * L2E), v0[3] * s * __builtin_amdgcn_exp2f(b0[3] * L2E));
;                             o[2] = cvt_pk_bf16(v1[0] * s * __builtin_amdgcn_exp2f(b1[0] * L2E), v1[1] * s * __builtin_amdgcn_exp2f(b1[1] * L2E));
;                             o[3] = cvt_pk_bf16(v1[2] * s * __builtin_amdgcn_exp2f(b1[2] * L2E), v1[3] * s * __builtin_amdgcn_exp2f(b1[3] * L2E));
;                             __builtin_nontemporal_store(o, (u32x4*)(d0 + hoff));
;                         } else {
;                             u32x4 o;
;                             o[0] = cvt_pk_bf16(v0[0] * __builtin_amdgcn_exp2f(-b0[0] * L2E), v0[1] * __builtin_amdgcn_exp2f(-b0[1] * L2E));
;                             o[1] = cvt_pk_bf16(v0[2] * __builtin_amdgcn_exp2f(-b0[2] * L2E), v0[3] * __builtin_amdgcn_exp2f(-b0[3] * L2E));
;                             o[2] = cvt_pk_bf16(v1[0] * __builtin_amdgcn_exp2f(-b1[0] * L2E), v1[1] * __builtin_amdgcn_exp2f(-b1[1] * L2E));
;                             o[3] = cvt_pk_bf16(v1[2] * __builtin_amdgcn_exp2f(-b1[2] * L2E), v1[3] * __builtin_amdgcn_exp2f(-b1[3] * L2E));
;                             __builtin_nontemporal_store(o, (u32x4*)(d0 + hoff));
.LBB0_373:
	v_mul_f32_e32 v128, s33, v131
	v_exp_f32_e32 v130, v128
	v_mov_b32_e32 v151, v169
	v_mov_b32_e32 v149, v169
	v_lshl_add_u64 v[128:129], s[42:43], 0, v[150:151]
	v_mul_f32_e32 v130, v155, v130
	v_cvt_pk_bf16_f32 v147, v154, v130
	v_lshl_add_u64 v[128:129], v[128:129], 0, v[148:149]
	global_store_dwordx4 v[128:129], v[144:147], off
	global_load_dwordx4 v[128:131], v[152:153], off offset:528
	s_nop 0
	global_load_dwordx4 v[136:139], v[152:153], off offset:512
	s_and_b64 vcc, exec, s[8:9]
	s_mov_b64 s[54:55], -1
	s_cbranch_vccnz .LBB0_375
	s_waitcnt vmcnt(3)
	v_mul_f32_e32 v144, 0xbfb8aa3b, v140
	v_mul_f32_e32 v145, 0xbfb8aa3b, v141
	v_exp_f32_e32 v144, v144
	v_exp_f32_e32 v145, v145
	s_mov_b64 s[54:55], 0
	v_mov_b32_e32 v153, v91
	v_pk_mul_f32 v[144:145], v[92:93], v[144:145]
	s_nop 0
	v_cvt_pk_bf16_f32 v144, v144, v145
	v_mul_f32_e32 v145, 0xbfb8aa3b, v142
	v_exp_f32_e32 v146, v145
	v_mul_f32_e32 v145, 0xbfb8aa3b, v143
	v_exp_f32_e32 v147, v145
	s_nop 0
	v_pk_mul_f32 v[146:147], v[94:95], v[146:147]
	s_nop 0
	v_cvt_pk_bf16_f32 v145, v146, v147
	v_mul_f32_e32 v146, 0xbfb8aa3b, v132
	v_mul_f32_e32 v147, 0xbfb8aa3b, v133
	v_exp_f32_e32 v146, v146
	v_exp_f32_e32 v147, v147
	s_nop 0
	v_pk_mul_f32 v[146:147], v[88:89], v[146:147]
	s_nop 0
	v_cvt_pk_bf16_f32 v146, v146, v147
	v_mul_f32_e32 v147, 0xbfb8aa3b, v134
	v_exp_f32_e32 v147, v147
	s_nop 0
	v_mul_f32_e32 v152, v90, v147

;     __device__ __forceinline__ void operator()(const f32x4 (&acc)[2][2][4][2], const Unit& u, int wr, int wc, int fr, int fq) const {
;     ...
;             BC_LOAD(0, 0);
; #pragma unroll
;             for (int g = 0; g < 16; ++g) {
;                 const int ai = g >> 3, m = (g >> 1) & 3, bj = g & 1;
;                 const int r = row0 + ai * HALF + m * 16;
;                 if (g + 1 < 16) BC_LOAD((g + 1) & 1, g + 1);
;                 {
;                     {
;                         const int col = cb + bj * HALF + lc;
;                         const size_t hoff = ((size_t)((r >> 11) * 4 + (col >> 7)) * SEQ + (r & (SEQ - 1))) * 128 + (col & 127);
;                         const f32x4 b0 = bc[g & 1][0], b1 = bc[g & 1][1];
;                         const f32x4 v0 = acc[ai][bj][m][0], v1 = acc[ai][bj][m][1];
;                         const float L2E = 1.4426950408889634f;
;                         if (isq) {
;                             const float s = 0.08838834764831845f;
;                             u32x4 o; o[0] = cvt_pk_bf16(v0[0] * s * __builtin_amdgcn_exp2f(b0[0] * L2E), v0[1] * s * __builtin_amdgcn_exp2f(b0[1] * L2E));
;                             o[1] = cvt_pk_bf16(v0[2] * s * __builtin_amdgcn_exp2f(b0[2] * L2E), v0[3] * s * __builtin_amdgcn_exp2f(b0[3] * L2E));
;                             o[2] = cvt_pk_bf16(v1[0] * s * __builtin_amdgcn_exp2f(b1[0] * L2E), v1[1] * s * __builtin_amdgcn_exp2f(b1[1] * L2E));
;                             o[3] = cvt_pk_bf16(v1[2] * s * __builtin_amdgcn_exp2f(b1[2] * L2E), v1[3] * s * __builtin_amdgcn_exp2f(b1[3] * L2E));
;                             __builtin_nontemporal_store(o, (u32x4*)(d0 + hoff));
;                         } else {
;                             u32x4 o;
;                             o[0] = cvt_pk_bf16(v0[0] * __builtin_amdgcn_exp2f(-b0[0] * L2E), v0[1] * __builtin_amdgcn_exp2f(-b0[1] * L2E));
;                             o[1] = cvt_pk_bf16(v0[2] * __builtin_amdgcn_exp2f(-b0[2] * L2E), v0[3] * __builtin_amdgcn_exp2f(-b0[3] * L2E));
;                             o[2] = cvt_pk_bf16(v1[0] * __builtin_amdgcn_exp2f(-b1[0] * L2E), v1[1] * __builtin_amdgcn_exp2f(-b1[1] * L2E));
;                             o[3] = cvt_pk_bf16(v1[2] * __builtin_amdgcn_exp2f(-b1[2] * L2E), v1[3] * __builtin_amdgcn_exp2f(-b1[3] * L2E));
;                             __builtin_nontemporal_store(o, (u32x4*)(d0 + hoff));
.LBB0_377:
	s_waitcnt vmcnt(3)
	v_mul_f32_e32 v132, s33, v135
	v_exp_f32_e32 v132, v132
	v_or_b32_e32 v133, 0x1000, v156
	v_mov_b32_e32 v151, v169
	v_lshlrev_b32_e32 v150, 1, v133
	v_mul_f32_e32 v132, v153, v132
	v_cvt_pk_bf16_f32 v147, v152, v132
	v_lshl_add_u64 v[132:133], s[10:11], 0, v[150:151]
	v_mov_b32_e32 v149, v169
	v_lshl_add_u64 v[132:133], v[132:133], 0, v[148:149]
	global_store_dwordx4 v[132:133], v[144:147], off
	v_or_b32_e32 v132, 48, v192
	v_ashrrev_i32_e32 v133, 31, v132
	v_lshlrev_b64 v[132:133], 11, v[132:133]
	v_lshl_add_u64 v[132:133], s[22:23], 0, v[132:133]
	v_lshl_add_u64 v[152:153], v[168:169], 2, v[132:133]
	global_load_dwordx4 v[132:135], v[152:153], off offset:16
	global_load_dwordx4 v[140:143], v[152:153], off
	s_waitcnt vmcnt(3)
	s_and_b64 vcc, exec, s[8:9]
	s_mov_b64 s[54:55], -1
	s_cbranch_vccnz .LBB0_379
	v_mul_f32_e32 v144, 0xbfb8aa3b, v136
	v_mul_f32_e32 v145, 0xbfb8aa3b, v137
	v_exp_f32_e32 v144, v144
	v_exp_f32_e32 v145, v145
	s_mov_b64 s[54:55], 0
	v_mov_b32_e32 v155, v83
	v_pk_mul_f32 v[144:145], v[84:85], v[144:145]
	s_nop 0
	v_cvt_pk_bf16_f32 v144, v144, v145
	v_mul_f32_e32 v145, 0xbfb8aa3b, v138
	v_exp_f32_e32 v146, v145
	v_mul_f32_e32 v145, 0xbfb8aa3b, v139
	v_exp_f32_e32 v147, v145
	s_nop 0
	v_pk_mul_f32 v[146:147], v[86:87], v[146:147]
	s_nop 0
	v_cvt_pk_bf16_f32 v145, v146, v147
	v_mul_f32_e32 v146, 0xbfb8aa3b, v128
	v_mul_f32_e32 v147, 0xbfb8aa3b, v129
	v_exp_f32_e32 v146, v146
	v_exp_f32_e32 v147, v147
	s_nop 0
	v_pk_mul_f32 v[146:147], v[80:81], v[146:147]
	s_nop 0
	v_cvt_pk_bf16_f32 v146, v146, v147
	v_mul_f32_e32 v147, 0xbfb8aa3b, v130
	v_exp_f32_e32 v147, v147
	s_nop 0
	v_mul_f32_e32 v154, v82, v147

;     __device__ __forceinline__ void operator()(const f32x4 (&acc)[2][2][4][2], const Unit& u, int wr, int wc, int fr, int fq) const {
;     ...
;             BC_LOAD(0, 0);
; #pragma unroll
;             for (int g = 0; g < 16; ++g) {
;                 const int ai = g >> 3, m = (g >> 1) & 3, bj = g & 1;
;                 const int r = row0 + ai * HALF + m * 16;
;                 if (g + 1 < 16) BC_LOAD((g + 1) & 1, g + 1);
;                 {
;                     {
;                         const int col = cb + bj * HALF + lc;
;                         const size_t hoff = ((size_t)((r >> 11) * 4 + (col >> 7)) * SEQ + (r & (SEQ - 1))) * 128 + (col & 127);
;                         const f32x4 b0 = bc[g & 1][0], b1 = bc[g & 1][1];
;                         const f32x4 v0 = acc[ai][bj][m][0], v1 = acc[ai][bj][m][1];
;                         const float L2E = 1.4426950408889634f;
;                         if (isq) {
;                             const float s = 0.08838834764831845f;
;                             u32x4 o; o[0] = cvt_pk_bf16(v0[0] * s * __builtin_amdgcn_exp2f(b0[0] * L2E), v0[1] * s * __builtin_amdgcn_exp2f(b0[1] * L2E));
;                             o[1] = cvt_pk_bf16(v0[2] * s * __builtin_amdgcn_exp2f(b0[2] * L2E), v0[3] * s * __builtin_amdgcn_exp2f(b0[3] * L2E));
;                             o[2] = cvt_pk_bf16(v1[0] * s * __builtin_amdgcn_exp2f(b1[0] * L2E), v1[1] * s * __builtin_amdgcn_exp2f(b1[1] * L2E));
;                             o[3] = cvt_pk_bf16(v1[2] * s * __builtin_amdgcn_exp2f(b1[2] * L2E), v1[3] * s * __builtin_amdgcn_exp2f(b1[3] * L2E));
;                             __builtin_nontemporal_store(o, (u32x4*)(d0 + hoff));
;                         } else {
;                             u32x4 o;
;                             o[0] = cvt_pk_bf16(v0[0] * __builtin_amdgcn_exp2f(-b0[0] * L2E), v0[1] * __builtin_amdgcn_exp2f(-b0[1] * L2E));
;                             o[1] = cvt_pk_bf16(v0[2] * __builtin_amdgcn_exp2f(-b0[2] * L2E), v0[3] * __builtin_amdgcn_exp2f(-b0[3] * L2E));
;                             o[2] = cvt_pk_bf16(v1[0] * __builtin_amdgcn_exp2f(-b1[0] * L2E), v1[1] * __builtin_amdgcn_exp2f(-b1[1] * L2E));
;                             o[3] = cvt_pk_bf16(v1[2] * __builtin_amdgcn_exp2f(-b1[2] * L2E), v1[3] * __builtin_amdgcn_exp2f(-b1[3] * L2E));
;                             __builtin_nontemporal_store(o, (u32x4*)(d0 + hoff));
.LBB0_381:
	v_mul_f32_e32 v128, s33, v131
	v_exp_f32_e32 v130, v128
	v_mov_b32_e32 v151, v169
	v_mov_b32_e32 v149, v169
	v_lshl_add_u64 v[128:129], s[42:43], 0, v[150:151]
	v_mul_f32_e32 v130, v155, v130
	v_cvt_pk_bf16_f32 v147, v154, v130
	v_lshl_add_u64 v[128:129], v[128:129], 0, v[148:149]
	global_store_dwordx4 v[128:129], v[144:147], off
	global_load_dwordx4 v[128:131], v[152:153], off offset:528
	s_nop 0
	global_load_dwordx4 v[136:139], v[152:153], off offset:512
	s_and_b64 vcc, exec, s[8:9]
	s_mov_b64 s[54:55], -1
	s_cbranch_vccnz .LBB0_383
	s_waitcnt vmcnt(3)
	v_mul_f32_e32 v144, 0xbfb8aa3b, v140
	v_mul_f32_e32 v145, 0xbfb8aa3b, v141
	v_exp_f32_e32 v144, v144
	v_exp_f32_e32 v145, v145
	s_mov_b64 s[54:55], 0
	v_mov_b32_e32 v151, v75
	v_pk_mul_f32 v[144:145], v[76:77], v[144:145]
	s_nop 0
	v_cvt_pk_bf16_f32 v144, v144, v145
	v_mul_f32_e32 v145, 0xbfb8aa3b, v142
	v_exp_f32_e32 v146, v145
	v_mul_f32_e32 v145, 0xbfb8aa3b, v143
	v_exp_f32_e32 v147, v145
	s_nop 0
	v_pk_mul_f32 v[146:147], v[78:79], v[146:147]
	s_nop 0
	v_cvt_pk_bf16_f32 v145, v146, v147
	v_mul_f32_e32 v146, 0xbfb8aa3b, v132
	v_mul_f32_e32 v147, 0xbfb8aa3b, v133
	v_exp_f32_e32 v146, v146
	v_exp_f32_e32 v147, v147
	s_nop 0
	v_pk_mul_f32 v[146:147], v[72:73], v[146:147]
	s_nop 0
	v_cvt_pk_bf16_f32 v146, v146, v147
	v_mul_f32_e32 v147, 0xbfb8aa3b, v134
	v_exp_f32_e32 v147, v147
	s_nop 0
	v_mul_f32_e32 v150, v74, v147

;     __device__ __forceinline__ void operator()(const f32x4 (&acc)[2][2][4][2], const Unit& u, int wr, int wc, int fr, int fq) const {
;     ...
;             BC_LOAD(0, 0);
; #pragma unroll
;             for (int g = 0; g < 16; ++g) {
;                 const int ai = g >> 3, m = (g >> 1) & 3, bj = g & 1;
;                 const int r = row0 + ai * HALF + m * 16;
;                 if (g + 1 < 16) BC_LOAD((g + 1) & 1, g + 1);
;                 {
;                     {
;                         const int col = cb + bj * HALF + lc;
;                         const size_t hoff = ((size_t)((r >> 11) * 4 + (col >> 7)) * SEQ + (r & (SEQ - 1))) * 128 + (col & 127);
;                         const f32x4 b0 = bc[g & 1][0], b1 = bc[g & 1][1];
;                         const f32x4 v0 = acc[ai][bj][m][0], v1 = acc[ai][bj][m][1];
;                         const float L2E = 1.4426950408889634f;
;                         if (isq) {
;                             const float s = 0.08838834764831845f;
;                             u32x4 o; o[0] = cvt_pk_bf16(v0[0] * s * __builtin_amdgcn_exp2f(b0[0] * L2E), v0[1] * s * __builtin_amdgcn_exp2f(b0[1] * L2E));
;                             o[1] = cvt_pk_bf16(v0[2] * s * __builtin_amdgcn_exp2f(b0[2] * L2E), v0[3] * s * __builtin_amdgcn_exp2f(b0[3] * L2E));
;                             o[2] = cvt_pk_bf16(v1[0] * s * __builtin_amdgcn_exp2f(b1[0] * L2E), v1[1] * s * __builtin_amdgcn_exp2f(b1[1] * L2E));
;                             o[3] = cvt_pk_bf16(v1[2] * s * __builtin_amdgcn_exp2f(b1[2] * L2E), v1[3] * s * __builtin_amdgcn_exp2f(b1[3] * L2E));
;                             __builtin_nontemporal_store(o, (u32x4*)(d0 + hoff));
;                         } else {
;                             u32x4 o;
;                             o[0] = cvt_pk_bf16(v0[0] * __builtin_amdgcn_exp2f(-b0[0] * L2E), v0[1] * __builtin_amdgcn_exp2f(-b0[1] * L2E));
;                             o[1] = cvt_pk_bf16(v0[2] * __builtin_amdgcn_exp2f(-b0[2] * L2E), v0[3] * __builtin_amdgcn_exp2f(-b0[3] * L2E));
;                             o[2] = cvt_pk_bf16(v1[0] * __builtin_amdgcn_exp2f(-b1[0] * L2E), v1[1] * __builtin_amdgcn_exp2f(-b1[1] * L2E));
;                             o[3] = cvt_pk_bf16(v1[2] * __builtin_amdgcn_exp2f(-b1[2] * L2E), v1[3] * __builtin_amdgcn_exp2f(-b1[3] * L2E));
;                             __builtin_nontemporal_store(o, (u32x4*)(d0 + hoff));
.LBB0_385:
	s_waitcnt vmcnt(3)
	v_mul_f32_e32 v132, s33, v135
	v_exp_f32_e32 v132, v132
	v_or_b32_e32 v133, 0x1800, v156
	v_mov_b32_e32 v153, v169
	v_lshlrev_b32_e32 v152, 1, v133
	v_mul_f32_e32 v132, v151, v132
	v_cvt_pk_bf16_f32 v147, v150, v132
	v_lshl_add_u64 v[132:133], s[10:11], 0, v[152:153]
	v_mov_b32_e32 v149, v169
	v_add_u32_e32 v150, 0x80, v192
	v_lshl_add_u64 v[132:133], v[132:133], 0, v[148:149]
	v_ashrrev_i32_e32 v151, 31, v150
	global_store_dwordx4 v[132:133], v[144:147], off
	v_lshlrev_b64 v[132:133], 11, v[150:151]
	v_lshl_add_u64 v[132:133], s[22:23], 0, v[132:133]
	v_lshl_add_u64 v[154:155], v[168:169], 2, v[132:133]
	global_load_dwordx4 v[132:135], v[154:155], off offset:16
	global_load_dwordx4 v[140:143], v[154:155], off
	s_waitcnt vmcnt(3)
	s_and_b64 vcc, exec, s[8:9]
	s_mov_b64 s[10:11], -1
	s_cbranch_vccnz .LBB0_387
	v_mul_f32_e32 v144, 0xbfb8aa3b, v136
	v_mul_f32_e32 v145, 0xbfb8aa3b, v137
	v_exp_f32_e32 v144, v144
	v_exp_f32_e32 v145, v145
	s_mov_b64 s[10:11], 0
	v_mov_b32_e32 v157, v67
	v_pk_mul_f32 v[144:145], v[68:69], v[144:145]
	s_nop 0
	v_cvt_pk_bf16_f32 v144, v144, v145
	v_mul_f32_e32 v145, 0xbfb8aa3b, v138
	v_exp_f32_e32 v146, v145
	v_mul_f32_e32 v145, 0xbfb8aa3b, v139
	v_exp_f32_e32 v147, v145
	s_nop 0
	v_pk_mul_f32 v[146:147], v[70:71], v[146:147]
	s_nop 0
	v_cvt_pk_bf16_f32 v145, v146, v147
	v_mul_f32_e32 v146, 0xbfb8aa3b, v128
	v_mul_f32_e32 v147, 0xbfb8aa3b, v129
	v_exp_f32_e32 v146, v146
	v_exp_f32_e32 v147, v147
	s_nop 0
	v_pk_mul_f32 v[146:147], v[64:65], v[146:147]
	s_nop 0
	v_cvt_pk_bf16_f32 v146, v146, v147
	v_mul_f32_e32 v147, 0xbfb8aa3b, v130
	v_exp_f32_e32 v147, v147
	s_nop 0
	v_mul_f32_e32 v156, v66, v147

;     __device__ __forceinline__ void operator()(const f32x4 (&acc)[2][2][4][2], const Unit& u, int wr, int wc, int fr, int fq) const {
;     ...
;             BC_LOAD(0, 0);
; #pragma unroll
;             for (int g = 0; g < 16; ++g) {
;                 const int ai = g >> 3, m = (g >> 1) & 3, bj = g & 1;
;                 const int r = row0 + ai * HALF + m * 16;
;                 if (g + 1 < 16) BC_LOAD((g + 1) & 1, g + 1);
;                 {
;                     {
;                         const int col = cb + bj * HALF + lc;
;                         const size_t hoff = ((size_t)((r >> 11) * 4 + (col >> 7)) * SEQ + (r & (SEQ - 1))) * 128 + (col & 127);
;                         const f32x4 b0 = bc[g & 1][0], b1 = bc[g & 1][1];
;                         const f32x4 v0 = acc[ai][bj][m][0], v1 = acc[ai][bj][m][1];
;                         const float L2E = 1.4426950408889634f;
;                         if (isq) {
;                             const float s = 0.08838834764831845f;
;                             u32x4 o; o[0] = cvt_pk_bf16(v0[0] * s * __builtin_amdgcn_exp2f(b0[0] * L2E), v0[1] * s * __builtin_amdgcn_exp2f(b0[1] * L2E));
;                             o[1] = cvt_pk_bf16(v0[2] * s * __builtin_amdgcn_exp2f(b0[2] * L2E), v0[3] * s * __builtin_amdgcn_exp2f(b0[3] * L2E));
;                             o[2] = cvt_pk_bf16(v1[0] * s * __builtin_amdgcn_exp2f(b1[0] * L2E), v1[1] * s * __builtin_amdgcn_exp2f(b1[1] * L2E));
;                             o[3] = cvt_pk_bf16(v1[2] * s * __builtin_amdgcn_exp2f(b1[2] * L2E), v1[3] * s * __builtin_amdgcn_exp2f(b1[3] * L2E));
;                             __builtin_nontemporal_store(o, (u32x4*)(d0 + hoff));
;                         } else {
;                             u32x4 o;
;                             o[0] = cvt_pk_bf16(v0[0] * __builtin_amdgcn_exp2f(-b0[0] * L2E), v0[1] * __builtin_amdgcn_exp2f(-b0[1] * L2E));
;                             o[1] = cvt_pk_bf16(v0[2] * __builtin_amdgcn_exp2f(-b0[2] * L2E), v0[3] * __builtin_amdgcn_exp2f(-b0[3] * L2E));
;                             o[2] = cvt_pk_bf16(v1[0] * __builtin_amdgcn_exp2f(-b1[0] * L2E), v1[1] * __builtin_amdgcn_exp2f(-b1[1] * L2E));
;                             o[3] = cvt_pk_bf16(v1[2] * __builtin_amdgcn_exp2f(-b1[2] * L2E), v1[3] * __builtin_amdgcn_exp2f(-b1[3] * L2E));
;                             __builtin_nontemporal_store(o, (u32x4*)(d0 + hoff));
.LBB0_389:
	v_mul_f32_e32 v128, s10, v131
	v_exp_f32_e32 v130, v128
	v_mov_b32_e32 v153, v169
	v_mov_b32_e32 v149, v169
	v_lshl_add_u64 v[128:129], s[42:43], 0, v[152:153]
	v_mul_f32_e32 v130, v157, v130
	v_cvt_pk_bf16_f32 v147, v156, v130
	v_lshl_add_u64 v[128:129], v[128:129], 0, v[148:149]
	global_store_dwordx4 v[128:129], v[144:147], off
	global_load_dwordx4 v[128:131], v[154:155], off offset:528
	s_nop 0
	global_load_dwordx4 v[136:139], v[154:155], off offset:512
	s_and_b64 vcc, exec, s[8:9]
	s_mov_b64 s[10:11], -1
	s_cbranch_vccnz .LBB0_391
	s_waitcnt vmcnt(3)
	v_mul_f32_e32 v144, 0xbfb8aa3b, v140
	v_mul_f32_e32 v145, 0xbfb8aa3b, v141
	v_exp_f32_e32 v144, v144
	v_exp_f32_e32 v145, v145
	s_mov_b64 s[10:11], 0
	v_mov_b32_e32 v153, v59
	v_pk_mul_f32 v[144:145], v[60:61], v[144:145]
	s_nop 0
	v_cvt_pk_bf16_f32 v144, v144, v145
	v_mul_f32_e32 v145, 0xbfb8aa3b, v142
	v_exp_f32_e32 v146, v145
	v_mul_f32_e32 v145, 0xbfb8aa3b, v143
	v_exp_f32_e32 v147, v145
	s_nop 0
	v_pk_mul_f32 v[146:147], v[62:63], v[146:147]
	s_nop 0
	v_cvt_pk_bf16_f32 v145, v146, v147
	v_mul_f32_e32 v146, 0xbfb8aa3b, v132
	v_mul_f32_e32 v147, 0xbfb8aa3b, v133
	v_exp_f32_e32 v146, v146
	v_exp_f32_e32 v147, v147
	s_nop 0
	v_pk_mul_f32 v[146:147], v[56:57], v[146:147]
	s_nop 0
	v_cvt_pk_bf16_f32 v146, v146, v147
	v_mul_f32_e32 v147, 0xbfb8aa3b, v134
	v_exp_f32_e32 v147, v147
	s_nop 0
	v_mul_f32_e32 v152, v58, v147

;     __device__ __forceinline__ void operator()(const f32x4 (&acc)[2][2][4][2], const Unit& u, int wr, int wc, int fr, int fq) const {
;     ...
;             BC_LOAD(0, 0);
; #pragma unroll
;             for (int g = 0; g < 16; ++g) {
;                 const int ai = g >> 3, m = (g >> 1) & 3, bj = g & 1;
;                 const int r = row0 + ai * HALF + m * 16;
;                 if (g + 1 < 16) BC_LOAD((g + 1) & 1, g + 1);
;                 {
;                     {
;                         const int col = cb + bj * HALF + lc;
;                         const size_t hoff = ((size_t)((r >> 11) * 4 + (col >> 7)) * SEQ + (r & (SEQ - 1))) * 128 + (col & 127);
;                         const f32x4 b0 = bc[g & 1][0], b1 = bc[g & 1][1];
;                         const f32x4 v0 = acc[ai][bj][m][0], v1 = acc[ai][bj][m][1];
;                         const float L2E = 1.4426950408889634f;
;                         if (isq) {
;                             const float s = 0.08838834764831845f;
;                             u32x4 o; o[0] = cvt_pk_bf16(v0[0] * s * __builtin_amdgcn_exp2f(b0[0] * L2E), v0[1] * s * __builtin_amdgcn_exp2f(b0[1] * L2E));
;                             o[1] = cvt_pk_bf16(v0[2] * s * __builtin_amdgcn_exp2f(b0[2] * L2E), v0[3] * s * __builtin_amdgcn_exp2f(b0[3] * L2E));
;                             o[2] = cvt_pk_bf16(v1[0] * s * __builtin_amdgcn_exp2f(b1[0] * L2E), v1[1] * s * __builtin_amdgcn_exp2f(b1[1] * L2E));
;                             o[3] = cvt_pk_bf16(v1[2] * s * __builtin_amdgcn_exp2f(b1[2] * L2E), v1[3] * s * __builtin_amdgcn_exp2f(b1[3] * L2E));
;                             __builtin_nontemporal_store(o, (u32x4*)(d0 + hoff));
;                         } else {
;                             u32x4 o;
;                             o[0] = cvt_pk_bf16(v0[0] * __builtin_amdgcn_exp2f(-b0[0] * L2E), v0[1] * __builtin_amdgcn_exp2f(-b0[1] * L2E));
;                             o[1] = cvt_pk_bf16(v0[2] * __builtin_amdgcn_exp2f(-b0[2] * L2E), v0[3] * __builtin_amdgcn_exp2f(-b0[3] * L2E));
;                             o[2] = cvt_pk_bf16(v1[0] * __builtin_amdgcn_exp2f(-b1[0] * L2E), v1[1] * __builtin_amdgcn_exp2f(-b1[1] * L2E));
;                             o[3] = cvt_pk_bf16(v1[2] * __builtin_amdgcn_exp2f(-b1[2] * L2E), v1[3] * __builtin_amdgcn_exp2f(-b1[3] * L2E));
;                             __builtin_nontemporal_store(o, (u32x4*)(d0 + hoff));
.LBB0_393:
	s_waitcnt vmcnt(3)
	v_mul_f32_e32 v133, s10, v135
	v_ashrrev_i32_e32 v132, 9, v150
	v_exp_f32_e32 v134, v133
	v_and_b32_e32 v151, -4, v132
	v_add_u32_e32 v132, s17, v151
	v_ashrrev_i32_e32 v133, 31, v132
	v_lshlrev_b32_e32 v135, 7, v150
	v_and_b32_e32 v193, 0x3e780, v135
	v_mul_f32_e32 v134, v153, v134
	v_lshlrev_b64 v[132:133], 19, v[132:133]
	v_cvt_pk_bf16_f32 v147, v152, v134
	v_lshl_add_u64 v[152:153], s[2:3], 0, v[132:133]
	v_lshlrev_b32_e32 v156, 1, v193
	v_mov_b32_e32 v157, v169
	v_lshl_add_u64 v[132:133], v[152:153], 0, v[156:157]
	v_mov_b32_e32 v149, v169
	v_lshl_add_u64 v[132:133], v[132:133], 0, v[148:149]
	global_store_dwordx4 v[132:133], v[144:147], off
	v_or_b32_e32 v132, 16, v150
	v_ashrrev_i32_e32 v133, 31, v132
	v_lshlrev_b64 v[132:133], 11, v[132:133]
	v_lshl_add_u64 v[132:133], s[22:23], 0, v[132:133]
	v_lshl_add_u64 v[158:159], v[168:169], 2, v[132:133]
	global_load_dwordx4 v[132:135], v[158:159], off offset:16
	global_load_dwordx4 v[140:143], v[158:159], off
	s_waitcnt vmcnt(3)
	s_and_b64 vcc, exec, s[8:9]
	s_mov_b64 s[10:11], -1
	s_cbranch_vccnz .LBB0_395
	v_mul_f32_e32 v144, 0xbfb8aa3b, v136
	v_mul_f32_e32 v145, 0xbfb8aa3b, v137
	v_exp_f32_e32 v144, v144
	v_exp_f32_e32 v145, v145
	s_mov_b64 s[10:11], 0
	v_mov_b32_e32 v155, v51
	v_pk_mul_f32 v[144:145], v[52:53], v[144:145]
	s_nop 0
	v_cvt_pk_bf16_f32 v144, v144, v145
	v_mul_f32_e32 v145, 0xbfb8aa3b, v138
	v_exp_f32_e32 v146, v145
	v_mul_f32_e32 v145, 0xbfb8aa3b, v139
	v_exp_f32_e32 v147, v145
	s_nop 0
	v_pk_mul_f32 v[146:147], v[54:55], v[146:147]
	s_nop 0
	v_cvt_pk_bf16_f32 v145, v146, v147
	v_mul_f32_e32 v146, 0xbfb8aa3b, v128
	v_mul_f32_e32 v147, 0xbfb8aa3b, v129
	v_exp_f32_e32 v146, v146
	v_exp_f32_e32 v147, v147
	s_nop 0
	v_pk_mul_f32 v[146:147], v[48:49], v[146:147]
	s_nop 0
	v_cvt_pk_bf16_f32 v146, v146, v147
	v_mul_f32_e32 v147, 0xbfb8aa3b, v130
	v_exp_f32_e32 v147, v147
	s_nop 0
	v_mul_f32_e32 v154, v50, v147

;     __device__ __forceinline__ void operator()(const f32x4 (&acc)[2][2][4][2], const Unit& u, int wr, int wc, int fr, int fq) const {
;     ...
;             BC_LOAD(0, 0);
; #pragma unroll
;             for (int g = 0; g < 16; ++g) {
;                 const int ai = g >> 3, m = (g >> 1) & 3, bj = g & 1;
;                 const int r = row0 + ai * HALF + m * 16;
;                 if (g + 1 < 16) BC_LOAD((g + 1) & 1, g + 1);
;                 {
;                     {
;                         const int col = cb + bj * HALF + lc;
;                         const size_t hoff = ((size_t)((r >> 11) * 4 + (col >> 7)) * SEQ + (r & (SEQ - 1))) * 128 + (col & 127);
;                         const f32x4 b0 = bc[g & 1][0], b1 = bc[g & 1][1];
;                         const f32x4 v0 = acc[ai][bj][m][0], v1 = acc[ai][bj][m][1];
;                         const float L2E = 1.4426950408889634f;
;                         if (isq) {
;                             const float s = 0.08838834764831845f;
;                             u32x4 o; o[0] = cvt_pk_bf16(v0[0] * s * __builtin_amdgcn_exp2f(b0[0] * L2E), v0[1] * s * __builtin_amdgcn_exp2f(b0[1] * L2E));
;                             o[1] = cvt_pk_bf16(v0[2] * s * __builtin_amdgcn_exp2f(b0[2] * L2E), v0[3] * s * __builtin_amdgcn_exp2f(b0[3] * L2E));
;                             o[2] = cvt_pk_bf16(v1[0] * s * __builtin_amdgcn_exp2f(b1[0] * L2E), v1[1] * s * __builtin_amdgcn_exp2f(b1[1] * L2E));
;                             o[3] = cvt_pk_bf16(v1[2] * s * __builtin_amdgcn_exp2f(b1[2] * L2E), v1[3] * s * __builtin_amdgcn_exp2f(b1[3] * L2E));
;                             __builtin_nontemporal_store(o, (u32x4*)(d0 + hoff));
;                         } else {
;                             u32x4 o;
;                             o[0] = cvt_pk_bf16(v0[0] * __builtin_amdgcn_exp2f(-b0[0] * L2E), v0[1] * __builtin_amdgcn_exp2f(-b0[1] * L2E));
;                             o[1] = cvt_pk_bf16(v0[2] * __builtin_amdgcn_exp2f(-b0[2] * L2E), v0[3] * __builtin_amdgcn_exp2f(-b0[3] * L2E));
;                             o[2] = cvt_pk_bf16(v1[0] * __builtin_amdgcn_exp2f(-b1[0] * L2E), v1[1] * __builtin_amdgcn_exp2f(-b1[1] * L2E));
;                             o[3] = cvt_pk_bf16(v1[2] * __builtin_amdgcn_exp2f(-b1[2] * L2E), v1[3] * __builtin_amdgcn_exp2f(-b1[3] * L2E));
;                             __builtin_nontemporal_store(o, (u32x4*)(d0 + hoff));
.LBB0_397:
	v_mul_f32_e32 v128, s10, v131
	v_exp_f32_e32 v130, v128
	v_add_u32_e32 v128, s18, v151
	v_ashrrev_i32_e32 v129, 31, v128
	v_lshlrev_b64 v[128:129], 19, v[128:129]
	v_mul_f32_e32 v130, v155, v130
	v_cvt_pk_bf16_f32 v147, v154, v130
	v_lshl_add_u64 v[154:155], s[2:3], 0, v[128:129]
	v_mov_b32_e32 v157, v169
	v_lshl_add_u64 v[128:129], v[154:155], 0, v[156:157]
	v_mov_b32_e32 v149, v169
	v_lshl_add_u64 v[128:129], v[128:129], 0, v[148:149]
	global_store_dwordx4 v[128:129], v[144:147], off
	global_load_dwordx4 v[128:131], v[158:159], off offset:528
	s_nop 0
	global_load_dwordx4 v[136:139], v[158:159], off offset:512
	s_and_b64 vcc, exec, s[8:9]
	s_mov_b64 s[2:3], -1
	s_cbranch_vccnz .LBB0_399
	s_waitcnt vmcnt(3)
	v_mul_f32_e32 v144, 0xbfb8aa3b, v140
	v_mul_f32_e32 v145, 0xbfb8aa3b, v141
	v_exp_f32_e32 v144, v144
	v_exp_f32_e32 v145, v145
	s_mov_b64 s[2:3], 0
	v_mov_b32_e32 v159, v43
	v_pk_mul_f32 v[144:145], v[44:45], v[144:145]
	s_nop 0
	v_cvt_pk_bf16_f32 v144, v144, v145
	v_mul_f32_e32 v145, 0xbfb8aa3b, v142
	v_exp_f32_e32 v146, v145
	v_mul_f32_e32 v145, 0xbfb8aa3b, v143
	v_exp_f32_e32 v147, v145
	s_nop 0
	v_pk_mul_f32 v[146:147], v[46:47], v[146:147]
	s_nop 0
	v_cvt_pk_bf16_f32 v145, v146, v147
	v_mul_f32_e32 v146, 0xbfb8aa3b, v132
	v_mul_f32_e32 v147, 0xbfb8aa3b, v133
	v_exp_f32_e32 v146, v146
	v_exp_f32_e32 v147, v147
	s_nop 0
	v_pk_mul_f32 v[146:147], v[40:41], v[146:147]
	s_nop 0
	v_cvt_pk_bf16_f32 v146, v146, v147
	v_mul_f32_e32 v147, 0xbfb8aa3b, v134
	v_exp_f32_e32 v147, v147
	s_nop 0
	v_mul_f32_e32 v158, v42, v147

;     __device__ __forceinline__ void operator()(const f32x4 (&acc)[2][2][4][2], const Unit& u, int wr, int wc, int fr, int fq) const {
;     ...
;             BC_LOAD(0, 0);
; #pragma unroll
;             for (int g = 0; g < 16; ++g) {
;                 const int ai = g >> 3, m = (g >> 1) & 3, bj = g & 1;
;                 const int r = row0 + ai * HALF + m * 16;
;                 if (g + 1 < 16) BC_LOAD((g + 1) & 1, g + 1);
;                 {
;                     {
;                         const int col = cb + bj * HALF + lc;
;                         const size_t hoff = ((size_t)((r >> 11) * 4 + (col >> 7)) * SEQ + (r & (SEQ - 1))) * 128 + (col & 127);
;                         const f32x4 b0 = bc[g & 1][0], b1 = bc[g & 1][1];
;                         const f32x4 v0 = acc[ai][bj][m][0], v1 = acc[ai][bj][m][1];
;                         const float L2E = 1.4426950408889634f;
;                         if (isq) {
;                             const float s = 0.08838834764831845f;
;                             u32x4 o; o[0] = cvt_pk_bf16(v0[0] * s * __builtin_amdgcn_exp2f(b0[0] * L2E), v0[1] * s * __builtin_amdgcn_exp2f(b0[1] * L2E));
;                             o[1] = cvt_pk_bf16(v0[2] * s * __builtin_amdgcn_exp2f(b0[2] * L2E), v0[3] * s * __builtin_amdgcn_exp2f(b0[3] * L2E));
;                             o[2] = cvt_pk_bf16(v1[0] * s * __builtin_amdgcn_exp2f(b1[0] * L2E), v1[1] * s * __builtin_amdgcn_exp2f(b1[1] * L2E));
;                             o[3] = cvt_pk_bf16(v1[2] * s * __builtin_amdgcn_exp2f(b1[2] * L2E), v1[3] * s * __builtin_amdgcn_exp2f(b1[3] * L2E));
;                             __builtin_nontemporal_store(o, (u32x4*)(d0 + hoff));
;                         } else {
;                             u32x4 o;
;                             o[0] = cvt_pk_bf16(v0[0] * __builtin_amdgcn_exp2f(-b0[0] * L2E), v0[1] * __builtin_amdgcn_exp2f(-b0[1] * L2E));
;                             o[1] = cvt_pk_bf16(v0[2] * __builtin_amdgcn_exp2f(-b0[2] * L2E), v0[3] * __builtin_amdgcn_exp2f(-b0[3] * L2E));
;                             o[2] = cvt_pk_bf16(v1[0] * __builtin_amdgcn_exp2f(-b1[0] * L2E), v1[1] * __builtin_amdgcn_exp2f(-b1[1] * L2E));
;                             o[3] = cvt_pk_bf16(v1[2] * __builtin_amdgcn_exp2f(-b1[2] * L2E), v1[3] * __builtin_amdgcn_exp2f(-b1[3] * L2E));
;                             __builtin_nontemporal_store(o, (u32x4*)(d0 + hoff));
.LBB0_401:
	s_waitcnt vmcnt(3)
	v_mul_f32_e32 v132, s2, v135
	v_exp_f32_e32 v132, v132
	v_or_b32_e32 v133, 0x800, v193
	v_mov_b32_e32 v157, v169
	v_lshlrev_b32_e32 v156, 1, v133
	v_mul_f32_e32 v132, v159, v132
	v_cvt_pk_bf16_f32 v147, v158, v132
	v_lshl_add_u64 v[132:133], v[152:153], 0, v[156:157]
	v_mov_b32_e32 v149, v169
	v_lshl_add_u64 v[132:133], v[132:133], 0, v[148:149]
	global_store_dwordx4 v[132:133], v[144:147], off
	v_or_b32_e32 v132, 32, v150
	v_ashrrev_i32_e32 v133, 31, v132
	v_lshlrev_b64 v[132:133], 11, v[132:133]
	v_lshl_add_u64 v[132:133], s[22:23], 0, v[132:133]
	v_lshl_add_u64 v[158:159], v[168:169], 2, v[132:133]
	global_load_dwordx4 v[132:135], v[158:159], off offset:16
	global_load_dwordx4 v[140:143], v[158:159], off
	s_waitcnt vmcnt(3)
	s_and_b64 vcc, exec, s[8:9]
	s_mov_b64 s[2:3], -1
	s_cbranch_vccnz .LBB0_403
	v_mul_f32_e32 v144, 0xbfb8aa3b, v136
	v_mul_f32_e32 v145, 0xbfb8aa3b, v137
	v_exp_f32_e32 v144, v144
	v_exp_f32_e32 v145, v145
	s_mov_b64 s[2:3], 0
	v_mov_b32_e32 v195, v35
	v_pk_mul_f32 v[144:145], v[36:37], v[144:145]
	s_nop 0
	v_cvt_pk_bf16_f32 v144, v144, v145
	v_mul_f32_e32 v145, 0xbfb8aa3b, v138
	v_exp_f32_e32 v146, v145
	v_mul_f32_e32 v145, 0xbfb8aa3b, v139
	v_exp_f32_e32 v147, v145
	s_nop 0
	v_pk_mul_f32 v[146:147], v[38:39], v[146:147]
	s_nop 0
	v_cvt_pk_bf16_f32 v145, v146, v147
	v_mul_f32_e32 v146, 0xbfb8aa3b, v128
	v_mul_f32_e32 v147, 0xbfb8aa3b, v129
	v_exp_f32_e32 v146, v146
	v_exp_f32_e32 v147, v147
	s_nop 0
	v_pk_mul_f32 v[146:147], v[32:33], v[146:147]
	s_nop 0
	v_cvt_pk_bf16_f32 v146, v146, v147
	v_mul_f32_e32 v147, 0xbfb8aa3b, v130
	v_exp_f32_e32 v147, v147
	s_nop 0
	v_mul_f32_e32 v194, v34, v147

;     __device__ __forceinline__ void operator()(const f32x4 (&acc)[2][2][4][2], const Unit& u, int wr, int wc, int fr, int fq) const {
;     ...
;             BC_LOAD(0, 0);
; #pragma unroll
;             for (int g = 0; g < 16; ++g) {
;                 const int ai = g >> 3, m = (g >> 1) & 3, bj = g & 1;
;                 const int r = row0 + ai * HALF + m * 16;
;                 if (g + 1 < 16) BC_LOAD((g + 1) & 1, g + 1);
;                 {
;                     {
;                         const int col = cb + bj * HALF + lc;
;                         const size_t hoff = ((size_t)((r >> 11) * 4 + (col >> 7)) * SEQ + (r & (SEQ - 1))) * 128 + (col & 127);
;                         const f32x4 b0 = bc[g & 1][0], b1 = bc[g & 1][1];
;                         const f32x4 v0 = acc[ai][bj][m][0], v1 = acc[ai][bj][m][1];
;                         const float L2E = 1.4426950408889634f;
;                         if (isq) {
;                             const float s = 0.08838834764831845f;
;                             u32x4 o; o[0] = cvt_pk_bf16(v0[0] * s * __builtin_amdgcn_exp2f(b0[0] * L2E), v0[1] * s * __builtin_amdgcn_exp2f(b0[1] * L2E));
;                             o[1] = cvt_pk_bf16(v0[2] * s * __builtin_amdgcn_exp2f(b0[2] * L2E), v0[3] * s * __builtin_amdgcn_exp2f(b0[3] * L2E));
;                             o[2] = cvt_pk_bf16(v1[0] * s * __builtin_amdgcn_exp2f(b1[0] * L2E), v1[1] * s * __builtin_amdgcn_exp2f(b1[1] * L2E));
;                             o[3] = cvt_pk_bf16(v1[2] * s * __builtin_amdgcn_exp2f(b1[2] * L2E), v1[3] * s * __builtin_amdgcn_exp2f(b1[3] * L2E));
;                             __builtin_nontemporal_store(o, (u32x4*)(d0 + hoff));
;                         } else {
;                             u32x4 o;
;                             o[0] = cvt_pk_bf16(v0[0] * __builtin_amdgcn_exp2f(-b0[0] * L2E), v0[1] * __builtin_amdgcn_exp2f(-b0[1] * L2E));
;                             o[1] = cvt_pk_bf16(v0[2] * __builtin_amdgcn_exp2f(-b0[2] * L2E), v0[3] * __builtin_amdgcn_exp2f(-b0[3] * L2E));
;                             o[2] = cvt_pk_bf16(v1[0] * __builtin_amdgcn_exp2f(-b1[0] * L2E), v1[1] * __builtin_amdgcn_exp2f(-b1[1] * L2E));
;                             o[3] = cvt_pk_bf16(v1[2] * __builtin_amdgcn_exp2f(-b1[2] * L2E), v1[3] * __builtin_amdgcn_exp2f(-b1[3] * L2E));
;                             __builtin_nontemporal_store(o, (u32x4*)(d0 + hoff));
.LBB0_405:
	v_mul_f32_e32 v128, s2, v131
	v_exp_f32_e32 v130, v128
	v_mov_b32_e32 v157, v169
	v_mov_b32_e32 v149, v169
	v_lshl_add_u64 v[128:129], v[154:155], 0, v[156:157]
	v_mul_f32_e32 v130, v195, v130
	v_cvt_pk_bf16_f32 v147, v194, v130
	v_lshl_add_u64 v[128:129], v[128:129], 0, v[148:149]
	global_store_dwordx4 v[128:129], v[144:147], off
	global_load_dwordx4 v[128:131], v[158:159], off offset:528
	s_nop 0
	global_load_dwordx4 v[136:139], v[158:159], off offset:512
	s_and_b64 vcc, exec, s[8:9]
	s_mov_b64 s[2:3], -1
	s_cbranch_vccnz .LBB0_407
	s_waitcnt vmcnt(3)
	v_mul_f32_e32 v144, 0xbfb8aa3b, v140
	v_mul_f32_e32 v145, 0xbfb8aa3b, v141
	v_exp_f32_e32 v144, v144
	v_exp_f32_e32 v145, v145
	s_mov_b64 s[2:3], 0
	v_mov_b32_e32 v159, v27
	v_pk_mul_f32 v[144:145], v[28:29], v[144:145]
	s_nop 0
	v_cvt_pk_bf16_f32 v144, v144, v145
	v_mul_f32_e32 v145, 0xbfb8aa3b, v142
	v_exp_f32_e32 v146, v145
	v_mul_f32_e32 v145, 0xbfb8aa3b, v143
	v_exp_f32_e32 v147, v145
	s_nop 0
	v_pk_mul_f32 v[146:147], v[30:31], v[146:147]
	s_nop 0
	v_cvt_pk_bf16_f32 v145, v146, v147
	v_mul_f32_e32 v146, 0xbfb8aa3b, v132
	v_mul_f32_e32 v147, 0xbfb8aa3b, v133
	v_exp_f32_e32 v146, v146
	v_exp_f32_e32 v147, v147
	s_nop 0
	v_pk_mul_f32 v[146:147], v[24:25], v[146:147]
	s_nop 0
	v_cvt_pk_bf16_f32 v146, v146, v147
	v_mul_f32_e32 v147, 0xbfb8aa3b, v134
	v_exp_f32_e32 v147, v147
	s_nop 0
	v_mul_f32_e32 v158, v26, v147

;     __device__ __forceinline__ void operator()(const f32x4 (&acc)[2][2][4][2], const Unit& u, int wr, int wc, int fr, int fq) const {
;     ...
;             BC_LOAD(0, 0);
; #pragma unroll
;             for (int g = 0; g < 16; ++g) {
;                 const int ai = g >> 3, m = (g >> 1) & 3, bj = g & 1;
;                 const int r = row0 + ai * HALF + m * 16;
;                 if (g + 1 < 16) BC_LOAD((g + 1) & 1, g + 1);
;                 {
;                     {
;                         const int col = cb + bj * HALF + lc;
;                         const size_t hoff = ((size_t)((r >> 11) * 4 + (col >> 7)) * SEQ + (r & (SEQ - 1))) * 128 + (col & 127);
;                         const f32x4 b0 = bc[g & 1][0], b1 = bc[g & 1][1];
;                         const f32x4 v0 = acc[ai][bj][m][0], v1 = acc[ai][bj][m][1];
;                         const float L2E = 1.4426950408889634f;
;                         if (isq) {
;                             const float s = 0.08838834764831845f;
;                             u32x4 o; o[0] = cvt_pk_bf16(v0[0] * s * __builtin_amdgcn_exp2f(b0[0] * L2E), v0[1] * s * __builtin_amdgcn_exp2f(b0[1] * L2E));
;                             o[1] = cvt_pk_bf16(v0[2] * s * __builtin_amdgcn_exp2f(b0[2] * L2E), v0[3] * s * __builtin_amdgcn_exp2f(b0[3] * L2E));
;                             o[2] = cvt_pk_bf16(v1[0] * s * __builtin_amdgcn_exp2f(b1[0] * L2E), v1[1] * s * __builtin_amdgcn_exp2f(b1[1] * L2E));
;                             o[3] = cvt_pk_bf16(v1[2] * s * __builtin_amdgcn_exp2f(b1[2] * L2E), v1[3] * s * __builtin_amdgcn_exp2f(b1[3] * L2E));
;                             __builtin_nontemporal_store(o, (u32x4*)(d0 + hoff));
;                         } else {
;                             u32x4 o;
;                             o[0] = cvt_pk_bf16(v0[0] * __builtin_amdgcn_exp2f(-b0[0] * L2E), v0[1] * __builtin_amdgcn_exp2f(-b0[1] * L2E));
;                             o[1] = cvt_pk_bf16(v0[2] * __builtin_amdgcn_exp2f(-b0[2] * L2E), v0[3] * __builtin_amdgcn_exp2f(-b0[3] * L2E));
;                             o[2] = cvt_pk_bf16(v1[0] * __builtin_amdgcn_exp2f(-b1[0] * L2E), v1[1] * __builtin_amdgcn_exp2f(-b1[1] * L2E));
;                             o[3] = cvt_pk_bf16(v1[2] * __builtin_amdgcn_exp2f(-b1[2] * L2E), v1[3] * __builtin_amdgcn_exp2f(-b1[3] * L2E));
;                             __builtin_nontemporal_store(o, (u32x4*)(d0 + hoff));
.LBB0_409:
	s_waitcnt vmcnt(3)
	v_mul_f32_e32 v132, s2, v135
	v_exp_f32_e32 v132, v132
	v_or_b32_e32 v133, 0x1000, v193
	v_mov_b32_e32 v157, v169
	v_lshlrev_b32_e32 v156, 1, v133
	v_mul_f32_e32 v132, v159, v132
	v_cvt_pk_bf16_f32 v147, v158, v132
	v_lshl_add_u64 v[132:133], v[152:153], 0, v[156:157]
	v_mov_b32_e32 v149, v169
	v_lshl_add_u64 v[132:133], v[132:133], 0, v[148:149]
	global_store_dwordx4 v[132:133], v[144:147], off
	v_or_b32_e32 v132, 48, v150
	v_ashrrev_i32_e32 v133, 31, v132
	v_lshlrev_b64 v[132:133], 11, v[132:133]
	v_lshl_add_u64 v[132:133], s[22:23], 0, v[132:133]
	v_lshl_add_u64 v[150:151], v[168:169], 2, v[132:133]
	global_load_dwordx4 v[132:135], v[150:151], off offset:16
	global_load_dwordx4 v[140:143], v[150:151], off
	s_waitcnt vmcnt(3)
	s_and_b64 vcc, exec, s[8:9]
	s_mov_b64 s[2:3], -1
	s_cbranch_vccnz .LBB0_411
	v_mul_f32_e32 v144, 0xbfb8aa3b, v136
	v_mul_f32_e32 v145, 0xbfb8aa3b, v137
	v_exp_f32_e32 v144, v144
	v_exp_f32_e32 v145, v145
	s_mov_b64 s[2:3], 0
	v_mov_b32_e32 v159, v19
	v_pk_mul_f32 v[144:145], v[20:21], v[144:145]
	s_nop 0
	v_cvt_pk_bf16_f32 v144, v144, v145
	v_mul_f32_e32 v145, 0xbfb8aa3b, v138
	v_exp_f32_e32 v146, v145
	v_mul_f32_e32 v145, 0xbfb8aa3b, v139
	v_exp_f32_e32 v147, v145
	s_nop 0
	v_pk_mul_f32 v[146:147], v[22:23], v[146:147]
	s_nop 0
	v_cvt_pk_bf16_f32 v145, v146, v147
	v_mul_f32_e32 v146, 0xbfb8aa3b, v128
	v_mul_f32_e32 v147, 0xbfb8aa3b, v129
	v_exp_f32_e32 v146, v146
	v_exp_f32_e32 v147, v147
	s_nop 0
	v_pk_mul_f32 v[146:147], v[16:17], v[146:147]
	s_nop 0
	v_cvt_pk_bf16_f32 v146, v146, v147
	v_mul_f32_e32 v147, 0xbfb8aa3b, v130
	v_exp_f32_e32 v147, v147
	s_nop 0
	v_mul_f32_e32 v158, v18, v147

;     __device__ __forceinline__ void operator()(const f32x4 (&acc)[2][2][4][2], const Unit& u, int wr, int wc, int fr, int fq) const {
;     ...
;             BC_LOAD(0, 0);
; #pragma unroll
;             for (int g = 0; g < 16; ++g) {
;                 const int ai = g >> 3, m = (g >> 1) & 3, bj = g & 1;
;                 const int r = row0 + ai * HALF + m * 16;
;                 if (g + 1 < 16) BC_LOAD((g + 1) & 1, g + 1);
;                 {
;                     {
;                         const int col = cb + bj * HALF + lc;
;                         const size_t hoff = ((size_t)((r >> 11) * 4 + (col >> 7)) * SEQ + (r & (SEQ - 1))) * 128 + (col & 127);
;                         const f32x4 b0 = bc[g & 1][0], b1 = bc[g & 1][1];
;                         const f32x4 v0 = acc[ai][bj][m][0], v1 = acc[ai][bj][m][1];
;                         const float L2E = 1.4426950408889634f;
;                         if (isq) {
;                             const float s = 0.08838834764831845f;
;                             u32x4 o; o[0] = cvt_pk_bf16(v0[0] * s * __builtin_amdgcn_exp2f(b0[0] * L2E), v0[1] * s * __builtin_amdgcn_exp2f(b0[1] * L2E));
;                             o[1] = cvt_pk_bf16(v0[2] * s * __builtin_amdgcn_exp2f(b0[2] * L2E), v0[3] * s * __builtin_amdgcn_exp2f(b0[3] * L2E));
;                             o[2] = cvt_pk_bf16(v1[0] * s * __builtin_amdgcn_exp2f(b1[0] * L2E), v1[1] * s * __builtin_amdgcn_exp2f(b1[1] * L2E));
;                             o[3] = cvt_pk_bf16(v1[2] * s * __builtin_amdgcn_exp2f(b1[2] * L2E), v1[3] * s * __builtin_amdgcn_exp2f(b1[3] * L2E));
;                             __builtin_nontemporal_store(o, (u32x4*)(d0 + hoff));
;                         } else {
;                             u32x4 o;
;                             o[0] = cvt_pk_bf16(v0[0] * __builtin_amdgcn_exp2f(-b0[0] * L2E), v0[1] * __builtin_amdgcn_exp2f(-b0[1] * L2E));
;                             o[1] = cvt_pk_bf16(v0[2] * __builtin_amdgcn_exp2f(-b0[2] * L2E), v0[3] * __builtin_amdgcn_exp2f(-b0[3] * L2E));
;                             o[2] = cvt_pk_bf16(v1[0] * __builtin_amdgcn_exp2f(-b1[0] * L2E), v1[1] * __builtin_amdgcn_exp2f(-b1[1] * L2E));
;                             o[3] = cvt_pk_bf16(v1[2] * __builtin_amdgcn_exp2f(-b1[2] * L2E), v1[3] * __builtin_amdgcn_exp2f(-b1[3] * L2E));
;                             __builtin_nontemporal_store(o, (u32x4*)(d0 + hoff));
.LBB0_413:
	v_mul_f32_e32 v128, s2, v131
	v_exp_f32_e32 v130, v128
	v_mov_b32_e32 v157, v169
	v_mov_b32_e32 v149, v169
	v_lshl_add_u64 v[128:129], v[154:155], 0, v[156:157]
	v_mul_f32_e32 v130, v159, v130
	v_cvt_pk_bf16_f32 v147, v158, v130
	v_lshl_add_u64 v[128:129], v[128:129], 0, v[148:149]
	global_store_dwordx4 v[128:129], v[144:147], off
	global_load_dwordx4 v[128:131], v[150:151], off offset:528
	s_nop 0
	global_load_dwordx4 v[136:139], v[150:151], off offset:512
	s_and_b64 vcc, exec, s[8:9]
	s_mov_b64 s[2:3], -1
	s_cbranch_vccnz .LBB0_415
	s_waitcnt vmcnt(3)
	v_mul_f32_e32 v144, 0xbfb8aa3b, v140
	v_mul_f32_e32 v145, 0xbfb8aa3b, v141
	v_exp_f32_e32 v144, v144
	v_exp_f32_e32 v145, v145
	s_mov_b64 s[2:3], 0
	v_mov_b32_e32 v151, v11
	v_pk_mul_f32 v[144:145], v[12:13], v[144:145]
	s_nop 0
	v_cvt_pk_bf16_f32 v144, v144, v145
	v_mul_f32_e32 v145, 0xbfb8aa3b, v142
	v_exp_f32_e32 v146, v145
	v_mul_f32_e32 v145, 0xbfb8aa3b, v143
	v_exp_f32_e32 v147, v145
	s_nop 0
	v_pk_mul_f32 v[146:147], v[14:15], v[146:147]
	s_nop 0
	v_cvt_pk_bf16_f32 v145, v146, v147
	v_mul_f32_e32 v146, 0xbfb8aa3b, v132
	v_mul_f32_e32 v147, 0xbfb8aa3b, v133
	v_exp_f32_e32 v146, v146
	v_exp_f32_e32 v147, v147
	s_nop 0
	v_pk_mul_f32 v[146:147], v[8:9], v[146:147]
	s_nop 0
	v_cvt_pk_bf16_f32 v146, v146, v147
	v_mul_f32_e32 v147, 0xbfb8aa3b, v134
	v_exp_f32_e32 v147, v147
	s_nop 0
	v_mul_f32_e32 v150, v10, v147

;     __device__ __forceinline__ void operator()(const f32x4 (&acc)[2][2][4][2], const Unit& u, int wr, int wc, int fr, int fq) const {
;     ...
;             BC_LOAD(0, 0);
; #pragma unroll
;             for (int g = 0; g < 16; ++g) {
;                 const int ai = g >> 3, m = (g >> 1) & 3, bj = g & 1;
;                 const int r = row0 + ai * HALF + m * 16;
;                 if (g + 1 < 16) BC_LOAD((g + 1) & 1, g + 1);
;                 {
;                     {
;                         const int col = cb + bj * HALF + lc;
;                         const size_t hoff = ((size_t)((r >> 11) * 4 + (col >> 7)) * SEQ + (r & (SEQ - 1))) * 128 + (col & 127);
;                         const f32x4 b0 = bc[g & 1][0], b1 = bc[g & 1][1];
;                         const f32x4 v0 = acc[ai][bj][m][0], v1 = acc[ai][bj][m][1];
;                         const float L2E = 1.4426950408889634f;
;                         if (isq) {
;                             const float s = 0.08838834764831845f;
;                             u32x4 o; o[0] = cvt_pk_bf16(v0[0] * s * __builtin_amdgcn_exp2f(b0[0] * L2E), v0[1] * s * __builtin_amdgcn_exp2f(b0[1] * L2E));
;                             o[1] = cvt_pk_bf16(v0[2] * s * __builtin_amdgcn_exp2f(b0[2] * L2E), v0[3] * s * __builtin_amdgcn_exp2f(b0[3] * L2E));
;                             o[2] = cvt_pk_bf16(v1[0] * s * __builtin_amdgcn_exp2f(b1[0] * L2E), v1[1] * s * __builtin_amdgcn_exp2f(b1[1] * L2E));
;                             o[3] = cvt_pk_bf16(v1[2] * s * __builtin_amdgcn_exp2f(b1[2] * L2E), v1[3] * s * __builtin_amdgcn_exp2f(b1[3] * L2E));
;                             __builtin_nontemporal_store(o, (u32x4*)(d0 + hoff));
;                         } else {
;                             u32x4 o;
;                             o[0] = cvt_pk_bf16(v0[0] * __builtin_amdgcn_exp2f(-b0[0] * L2E), v0[1] * __builtin_amdgcn_exp2f(-b0[1] * L2E));
;                             o[1] = cvt_pk_bf16(v0[2] * __builtin_amdgcn_exp2f(-b0[2] * L2E), v0[3] * __builtin_amdgcn_exp2f(-b0[3] * L2E));
;                             o[2] = cvt_pk_bf16(v1[0] * __builtin_amdgcn_exp2f(-b1[0] * L2E), v1[1] * __builtin_amdgcn_exp2f(-b1[1] * L2E));
;                             o[3] = cvt_pk_bf16(v1[2] * __builtin_amdgcn_exp2f(-b1[2] * L2E), v1[3] * __builtin_amdgcn_exp2f(-b1[3] * L2E));
;                             __builtin_nontemporal_store(o, (u32x4*)(d0 + hoff));
.LBB0_417:
	s_waitcnt vmcnt(3)
	v_mul_f32_e32 v132, s2, v135
	v_exp_f32_e32 v134, v132
	v_or_b32_e32 v132, 0x1800, v193
	v_lshlrev_b32_e32 v168, 1, v132
	v_lshl_add_u64 v[132:133], v[152:153], 0, v[168:169]
	v_mul_f32_e32 v134, v151, v134
	v_mov_b32_e32 v149, v169
	v_cvt_pk_bf16_f32 v147, v150, v134
	v_lshl_add_u64 v[132:133], v[132:133], 0, v[148:149]
	s_and_b64 vcc, exec, s[8:9]
	s_mov_b64 s[2:3], -1
	global_store_dwordx4 v[132:133], v[144:147], off
	s_waitcnt vmcnt(1)
	s_cbranch_vccnz .LBB0_419
	v_mul_f32_e32 v132, 0xbfb8aa3b, v136
	v_mul_f32_e32 v133, 0xbfb8aa3b, v137
	v_exp_f32_e32 v132, v132
	v_exp_f32_e32 v133, v133
	v_mul_f32_e32 v134, 0xbfb8aa3b, v138
	v_mul_f32_e32 v135, 0xbfb8aa3b, v139
	v_exp_f32_e32 v134, v134
	v_pk_mul_f32 v[132:133], v[4:5], v[132:133]
	v_exp_f32_e32 v135, v135
	v_cvt_pk_bf16_f32 v132, v132, v133
	v_mul_f32_e32 v133, 0xbfb8aa3b, v128
	v_exp_f32_e32 v140, v133
	v_mul_f32_e32 v133, 0xbfb8aa3b, v129
	v_exp_f32_e32 v141, v133
	v_mul_f32_e32 v133, 0xbfb8aa3b, v130
	v_exp_f32_e32 v142, v133
	v_pk_mul_f32 v[134:135], v[6:7], v[134:135]
	s_mov_b64 s[2:3], 0
	v_cvt_pk_bf16_f32 v133, v134, v135
	v_pk_mul_f32 v[134:135], v[0:1], v[140:141]
	v_mul_f32_e32 v140, v2, v142
	v_cvt_pk_bf16_f32 v134, v134, v135
	v_mov_b32_e32 v141, v3

;     __device__ __forceinline__ void operator()(const f32x4 (&acc)[2][2][4][2], const Unit& u, int wr, int wc, int fr, int fq) const {
;     ...
;             BC_LOAD(0, 0);
; #pragma unroll
;             for (int g = 0; g < 16; ++g) {
;                 const int ai = g >> 3, m = (g >> 1) & 3, bj = g & 1;
;                 const int r = row0 + ai * HALF + m * 16;
;                 if (g + 1 < 16) BC_LOAD((g + 1) & 1, g + 1);
;                 {
;                     {
;                         const int col = cb + bj * HALF + lc;
;                         const size_t hoff = ((size_t)((r >> 11) * 4 + (col >> 7)) * SEQ + (r & (SEQ - 1))) * 128 + (col & 127);
;                         const f32x4 b0 = bc[g & 1][0], b1 = bc[g & 1][1];
;                         const f32x4 v0 = acc[ai][bj][m][0], v1 = acc[ai][bj][m][1];
;                         const float L2E = 1.4426950408889634f;
;                         if (isq) {
;                             const float s = 0.08838834764831845f;
;                             u32x4 o; o[0] = cvt_pk_bf16(v0[0] * s * __builtin_amdgcn_exp2f(b0[0] * L2E), v0[1] * s * __builtin_amdgcn_exp2f(b0[1] * L2E));
;                             o[1] = cvt_pk_bf16(v0[2] * s * __builtin_amdgcn_exp2f(b0[2] * L2E), v0[3] * s * __builtin_amdgcn_exp2f(b0[3] * L2E));
;                             o[2] = cvt_pk_bf16(v1[0] * s * __builtin_amdgcn_exp2f(b1[0] * L2E), v1[1] * s * __builtin_amdgcn_exp2f(b1[1] * L2E));
;                             o[3] = cvt_pk_bf16(v1[2] * s * __builtin_amdgcn_exp2f(b1[2] * L2E), v1[3] * s * __builtin_amdgcn_exp2f(b1[3] * L2E));
;                             __builtin_nontemporal_store(o, (u32x4*)(d0 + hoff));
;                         } else {
;                             u32x4 o;
;                             o[0] = cvt_pk_bf16(v0[0] * __builtin_amdgcn_exp2f(-b0[0] * L2E), v0[1] * __builtin_amdgcn_exp2f(-b0[1] * L2E));
;                             o[1] = cvt_pk_bf16(v0[2] * __builtin_amdgcn_exp2f(-b0[2] * L2E), v0[3] * __builtin_amdgcn_exp2f(-b0[3] * L2E));
;                             o[2] = cvt_pk_bf16(v1[0] * __builtin_amdgcn_exp2f(-b1[0] * L2E), v1[1] * __builtin_amdgcn_exp2f(-b1[1] * L2E));
;                             o[3] = cvt_pk_bf16(v1[2] * __builtin_amdgcn_exp2f(-b1[2] * L2E), v1[3] * __builtin_amdgcn_exp2f(-b1[3] * L2E));
;                             __builtin_nontemporal_store(o, (u32x4*)(d0 + hoff));
.LBB0_421:
	v_mul_f32_e32 v128, s2, v131
	v_exp_f32_e32 v130, v128
	v_lshl_add_u64 v[128:129], v[154:155], 0, v[168:169]
	v_mov_b32_e32 v149, v169
	v_lshl_add_u64 v[128:129], v[128:129], 0, v[148:149]
	v_mul_f32_e32 v130, v141, v130
	v_cvt_pk_bf16_f32 v135, v140, v130
	global_store_dwordx4 v[128:129], v[132:135], off
	s_mov_b64 s[2:3], 0

; __device__ __forceinline__ unsigned cvt_pk_bf16(float lo, float hi) { const bf16x2_t r = __builtin_convertvector((f32x2_t){lo, hi}, bf16x2_t); return __builtin_bit_cast(unsigned, r); }
;     __device__ __forceinline__ void operator()(const f32x4 (&acc)[2][2][4][2], const Unit& u, int wr, int wc, int fr, int fq) const {
;     ...
;         } else if (u.pn < 12) {
;             bf16_t* dst = (bf16_t*)(ws + WS_VT);
; #pragma unroll
;             for (int ai = 0; ai < 2; ++ai)
; #pragma unroll
;                 for (int m = 0; m < 4; ++m) {
;                     const int r = row0 + ai * HALF + m * 16;
; #pragma unroll
;                     for (int bj = 0; bj < 2; ++bj) {
;                         const f32x4 v0 = acc[ai][bj][m][0], v1 = acc[ai][bj][m][1];
;                         u32x4 o; o[0] = cvt_pk_bf16(v0[0], v0[1]); o[1] = cvt_pk_bf16(v0[2], v0[3]); o[2] = cvt_pk_bf16(v1[0], v1[1]); o[3] = cvt_pk_bf16(v1[2], v1[3]);
;                         __builtin_nontemporal_store(o, (u32x4*)(dst + ((size_t)((r >> 11) * 8 + (u.pn - 8) * 2 + bj) * SEQ + (r & (SEQ - 1))) * 128 + lc));
;                     }
;                 }
.LBB0_423:
	s_lshl_b32 s2, s78, 1
	s_add_i32 s10, s2, -16
	s_ashr_i32 s2, s15, 8
	s_and_b32 s2, s2, -8
	s_add_i32 s2, s2, s10
	v_lshlrev_b32_e32 v128, 8, v192
	s_ashr_i32 s3, s2, 31
	v_and_b32_e32 v168, 0x7cf00, v128
	s_lshl_b64 s[8:9], s[2:3], 19
	s_or_b32 s2, s2, 1
	v_lshl_add_u64 v[132:133], v[180:181], 0, v[168:169]
	s_ashr_i32 s3, s2, 31
	v_cvt_pk_bf16_f32 v128, v124, v125
	v_cvt_pk_bf16_f32 v129, v126, v127
	v_cvt_pk_bf16_f32 v130, v120, v121
	v_cvt_pk_bf16_f32 v131, v122, v123
	v_lshl_add_u64 v[134:135], v[132:133], 0, s[8:9]
	s_lshl_b64 s[2:3], s[2:3], 19
	global_store_dwordx4 v[134:135], v[128:131], off
	v_lshl_add_u64 v[134:135], v[132:133], 0, s[2:3]
	s_nop 0
	v_cvt_pk_bf16_f32 v128, v116, v117
	v_cvt_pk_bf16_f32 v129, v118, v119
	v_cvt_pk_bf16_f32 v130, v112, v113
	v_cvt_pk_bf16_f32 v131, v114, v115
	global_store_dwordx4 v[134:135], v[128:131], off
	v_lshl_add_u64 v[134:135], v[132:133], 0, s[36:37]
	v_lshl_add_u64 v[136:137], v[134:135], 0, s[8:9]
	v_cvt_pk_bf16_f32 v128, v108, v109
	v_cvt_pk_bf16_f32 v129, v110, v111
	v_cvt_pk_bf16_f32 v130, v104, v105
	v_cvt_pk_bf16_f32 v131, v106, v107
	global_store_dwordx4 v[136:137], v[128:131], off
	v_lshl_add_u64 v[134:135], v[134:135], 0, s[2:3]
	s_nop 0
	v_cvt_pk_bf16_f32 v128, v100, v101
	v_cvt_pk_bf16_f32 v129, v102, v103
	v_cvt_pk_bf16_f32 v130, v96, v97
	v_cvt_pk_bf16_f32 v131, v98, v99
	global_store_dwordx4 v[134:135], v[128:131], off
	v_lshl_add_u64 v[134:135], v[132:133], 0, s[38:39]
	v_lshl_add_u64 v[136:137], v[134:135], 0, s[8:9]
	v_cvt_pk_bf16_f32 v128, v92, v93
	v_cvt_pk_bf16_f32 v129, v94, v95
	v_cvt_pk_bf16_f32 v130, v88, v89
	v_cvt_pk_bf16_f32 v131, v90, v91
	global_store_dwordx4 v[136:137], v[128:131], off
	v_lshl_add_u64 v[134:135], v[134:135], 0, s[2:3]
	v_lshl_add_u64 v[132:133], v[132:133], 0, s[40:41]
	v_cvt_pk_bf16_f32 v128, v84, v85
	v_cvt_pk_bf16_f32 v129, v86, v87
	v_cvt_pk_bf16_f32 v130, v80, v81
	v_cvt_pk_bf16_f32 v131, v82, v83
	global_store_dwordx4 v[134:135], v[128:131], off
	v_lshl_add_u64 v[134:135], v[132:133], 0, s[8:9]
	v_lshl_add_u64 v[132:133], v[132:133], 0, s[2:3]
	v_cvt_pk_bf16_f32 v128, v76, v77
	v_cvt_pk_bf16_f32 v129, v78, v79
	v_cvt_pk_bf16_f32 v130, v72, v73
	v_cvt_pk_bf16_f32 v131, v74, v75
	global_store_dwordx4 v[134:135], v[128:131], off
	s_nop 1
	v_cvt_pk_bf16_f32 v128, v68, v69
	v_cvt_pk_bf16_f32 v129, v70, v71
	v_cvt_pk_bf16_f32 v130, v64, v65
	v_cvt_pk_bf16_f32 v131, v66, v67
	global_store_dwordx4 v[132:133], v[128:131], off
	s_nop 1
	v_add_u32_e32 v128, 0x80, v192
	v_ashrrev_i32_e32 v129, 8, v128
	v_and_b32_e32 v129, -8, v129
	v_add_u32_e32 v132, s10, v129
	v_lshlrev_b32_e32 v128, 8, v128
	v_ashrrev_i32_e32 v133, 31, v132
	v_and_b32_e32 v168, 0x7cf00, v128
	v_lshlrev_b64 v[136:137], 19, v[132:133]
	v_or_b32_e32 v132, 1, v132
	v_lshl_add_u64 v[134:135], v[180:181], 0, v[168:169]
	v_ashrrev_i32_e32 v133, 31, v132
	v_cvt_pk_bf16_f32 v128, v60, v61
	v_cvt_pk_bf16_f32 v129, v62, v63
	v_cvt_pk_bf16_f32 v130, v56, v57
	v_cvt_pk_bf16_f32 v131, v58, v59
	v_lshl_add_u64 v[138:139], v[134:135], 0, v[136:137]
	v_lshlrev_b64 v[132:133], 19, v[132:133]
	global_store_dwordx4 v[138:139], v[128:131], off
	v_lshl_add_u64 v[138:139], v[134:135], 0, v[132:133]
	s_nop 0
	v_cvt_pk_bf16_f32 v128, v52, v53
	v_cvt_pk_bf16_f32 v129, v54, v55
	v_cvt_pk_bf16_f32 v130, v48, v49
	v_cvt_pk_bf16_f32 v131, v50, v51
	global_store_dwordx4 v[138:139], v[128:131], off
	v_lshl_add_u64 v[138:139], v[134:135], 0, s[36:37]
	v_lshl_add_u64 v[140:141], v[138:139], 0, v[136:137]
	v_cvt_pk_bf16_f32 v128, v44, v45
	v_cvt_pk_bf16_f32 v129, v46, v47
	v_cvt_pk_bf16_f32 v130, v40, v41
	v_cvt_pk_bf16_f32 v131, v42, v43
	global_store_dwordx4 v[140:141], v[128:131], off
	v_lshl_add_u64 v[138:139], v[138:139], 0, v[132:133]
	s_nop 0
	v_cvt_pk_bf16_f32 v128, v36, v37
	v_cvt_pk_bf16_f32 v129, v38, v39
	v_cvt_pk_bf16_f32 v130, v32, v33
	v_cvt_pk_bf16_f32 v131, v34, v35
	global_store_dwordx4 v[138:139], v[128:131], off
	v_lshl_add_u64 v[138:139], v[134:135], 0, s[38:39]
	v_lshl_add_u64 v[140:141], v[138:139], 0, v[136:137]
	v_cvt_pk_bf16_f32 v128, v28, v29
	v_cvt_pk_bf16_f32 v129, v30, v31
	v_cvt_pk_bf16_f32 v130, v24, v25
	v_cvt_pk_bf16_f32 v131, v26, v27
	global_store_dwordx4 v[140:141], v[128:131], off
	v_lshl_add_u64 v[138:139], v[138:139], 0, v[132:133]
	v_lshl_add_u64 v[134:135], v[134:135], 0, s[40:41]
	v_cvt_pk_bf16_f32 v128, v20, v21
	v_cvt_pk_bf16_f32 v129, v22, v23
	v_cvt_pk_bf16_f32 v130, v16, v17
	v_cvt_pk_bf16_f32 v131, v18, v19
	global_store_dwordx4 v[138:139], v[128:131], off
	v_lshl_add_u64 v[136:137], v[134:135], 0, v[136:137]
	v_lshl_add_u64 v[132:133], v[134:135], 0, v[132:133]
	v_cvt_pk_bf16_f32 v128, v12, v13
	v_cvt_pk_bf16_f32 v129, v14, v15
	v_cvt_pk_bf16_f32 v130, v8, v9
	v_cvt_pk_bf16_f32 v131, v10, v11
	global_store_dwordx4 v[136:137], v[128:131], off
	s_nop 1
	v_cvt_pk_bf16_f32 v128, v4, v5
	v_cvt_pk_bf16_f32 v129, v6, v7
	v_cvt_pk_bf16_f32 v130, v0, v1
	v_cvt_pk_bf16_f32 v131, v2, v3
	global_store_dwordx4 v[132:133], v[128:131], off

;     __device__ __forceinline__ void operator()(const f32x4 (&acc)[2][2][4][2], const Unit& u, int wr, int wc, int fr, int fq) const {
;     ...
;             const bool isq = u.pn < 4;
;             bf16_t* dst = (bf16_t*)(ws + (isq ? WS_Q : WS_K));
;             const int cb = (u.pn & 3) * 256;
;             const float scale = isq ? QSCALE : 1.0f;
;             float ks[2][8];
; #pragma unroll
;             for (int bj = 0; bj < 2; ++bj)
; #pragma unroll
;                 for (int i = 0; i < 8; ++i) ks[bj][i] = 0.f;
;             f32x4 rc[2][4];
;     ...
;             if (wc == 0) ROPE_LOAD(0, 0);
; #pragma unroll
;             for (int g = 0; g < 8; ++g) {
;                 const int ai = g >> 2, m = g & 3;
;                 const int r = row0 + ai * HALF + m * 16;
;                 if (wc == 0 && g + 1 < 8) ROPE_LOAD((g + 1) & 1, g + 1);
; #pragma unroll
;                 for (int bj = 0; bj < 2; ++bj) {
;                     float v[8] = {acc[ai][bj][m][0][0], acc[ai][bj][m][0][1], acc[ai][bj][m][0][2], acc[ai][bj][m][0][3],
;                                   acc[ai][bj][m][1][0], acc[ai][bj][m][1][1], acc[ai][bj][m][1][2], acc[ai][bj][m][1][3]};
;                     if (wc == 0) {
;                         const f32x4 c0 = rc[g & 1][0], c1 = rc[g & 1][1], s0 = rc[g & 1][2], s1 = rc[g & 1][3];
;                         const float cs[8] = {c0[0], c0[1], c0[2], c0[3], c1[0], c1[1], c1[2], c1[3]}, sn[8] = {s0[0], s0[1], s0[2], s0[3], s1[0], s1[1], s1[2], s1[3]};
; #pragma unroll
;                         for (int i = 0; i < 8; ++i) {
;                             const float pv = __shfl_xor(v[i], 32);
;                             v[i] = (fq < 2) ? (v[i] * cs[i] - pv * sn[i]) : (v[i] * cs[i] + pv * sn[i]);
;                         }
;                     }
;                     if (!isq) {
; #pragma unroll
;                         for (int i = 0; i < 8; ++i) ks[bj][i] += v[i];
;                     }
;                     u32x4 o; o[0] = cvt_pk_bf16(v[0] * scale, v[1] * scale); o[1] = cvt_pk_bf16(v[2] * scale, v[3] * scale);
;                     o[2] = cvt_pk_bf16(v[4] * scale, v[5] * scale); o[3] = cvt_pk_bf16(v[6] * scale, v[7] * scale);
;                     __builtin_nontemporal_store(o, (u32x4*)(dst + ((size_t)((r >> 11) * 8 + (u.pn & 3) * 2 + bj) * SEQ + (r & (SEQ - 1))) * 128 + lc));
;                 }
.LBB0_433:
	s_and_b64 s[2:3], s[10:11], exec
	s_mov_b32 s2, 0x40188000
	s_cselect_b32 s18, s2, 0x42188000
	s_lshl_b32 s2, s78, 1
	s_and_b32 s17, s2, 6
	s_ashr_i32 s2, s15, 8
	s_and_b32 s2, s2, -8
	s_or_b32 s42, s2, s17
	v_lshlrev_b32_e32 v168, 8, v192
	v_cndmask_b32_e64 v194, 1.0, v212, s[10:11]
	v_lshl_add_u64 v[196:197], v[174:175], 0, s[18:19]
	v_and_b32_e32 v168, 0x7cf00, v168
	v_pk_mul_f32 v[124:125], v[194:195], v[124:125] op_sel_hi:[0,1]
	v_pk_mul_f32 v[126:127], v[194:195], v[126:127] op_sel_hi:[0,1]
	v_pk_mul_f32 v[120:121], v[194:195], v[120:121] op_sel_hi:[0,1]
	s_ashr_i32 s43, s42, 31
	v_lshl_add_u64 v[198:199], v[196:197], 0, v[168:169]
	v_cvt_pk_bf16_f32 v124, v124, v125
	v_cvt_pk_bf16_f32 v125, v126, v127
	v_cvt_pk_bf16_f32 v126, v120, v121
	v_pk_mul_f32 v[120:121], v[194:195], v[122:123] op_sel_hi:[0,1]
	s_lshl_b64 s[2:3], s[42:43], 19
	v_cvt_pk_bf16_f32 v127, v120, v121
	v_lshl_add_u64 v[120:121], v[198:199], 0, s[2:3]
	s_and_b64 vcc, exec, s[8:9]
	global_store_dwordx4 v[120:121], v[124:127], off
	s_cbranch_vccz .LBB0_439
	s_and_b64 vcc, exec, s[54:55]
	s_cbranch_vccz .LBB0_440

;     __device__ __forceinline__ void operator()(const f32x4 (&acc)[2][2][4][2], const Unit& u, int wr, int wc, int fr, int fq) const {
;     ...
;             const bool isq = u.pn < 4;
;             bf16_t* dst = (bf16_t*)(ws + (isq ? WS_Q : WS_K));
;             const int cb = (u.pn & 3) * 256;
;             const float scale = isq ? QSCALE : 1.0f;
;             float ks[2][8];
; #pragma unroll
;             for (int bj = 0; bj < 2; ++bj)
; #pragma unroll
;                 for (int i = 0; i < 8; ++i) ks[bj][i] = 0.f;
;             f32x4 rc[2][4];
;     ...
;             if (wc == 0) ROPE_LOAD(0, 0);
; #pragma unroll
;             for (int g = 0; g < 8; ++g) {
;                 const int ai = g >> 2, m = g & 3;
;                 const int r = row0 + ai * HALF + m * 16;
;                 if (wc == 0 && g + 1 < 8) ROPE_LOAD((g + 1) & 1, g + 1);
; #pragma unroll
;                 for (int bj = 0; bj < 2; ++bj) {
;                     float v[8] = {acc[ai][bj][m][0][0], acc[ai][bj][m][0][1], acc[ai][bj][m][0][2], acc[ai][bj][m][0][3],
;                                   acc[ai][bj][m][1][0], acc[ai][bj][m][1][1], acc[ai][bj][m][1][2], acc[ai][bj][m][1][3]};
;                     if (wc == 0) {
;                         const f32x4 c0 = rc[g & 1][0], c1 = rc[g & 1][1], s0 = rc[g & 1][2], s1 = rc[g & 1][3];
;                         const float cs[8] = {c0[0], c0[1], c0[2], c0[3], c1[0], c1[1], c1[2], c1[3]}, sn[8] = {s0[0], s0[1], s0[2], s0[3], s1[0], s1[1], s1[2], s1[3]};
; #pragma unroll
;                         for (int i = 0; i < 8; ++i) {
;                             const float pv = __shfl_xor(v[i], 32);
;                             v[i] = (fq < 2) ? (v[i] * cs[i] - pv * sn[i]) : (v[i] * cs[i] + pv * sn[i]);
;                         }
;                     }
;                     if (!isq) {
; #pragma unroll
;                         for (int i = 0; i < 8; ++i) ks[bj][i] += v[i];
;                     }
;                     u32x4 o; o[0] = cvt_pk_bf16(v[0] * scale, v[1] * scale); o[1] = cvt_pk_bf16(v[2] * scale, v[3] * scale);
;                     o[2] = cvt_pk_bf16(v[4] * scale, v[5] * scale); o[3] = cvt_pk_bf16(v[6] * scale, v[7] * scale);
;                     __builtin_nontemporal_store(o, (u32x4*)(dst + ((size_t)((r >> 11) * 8 + (u.pn & 3) * 2 + bj) * SEQ + (r & (SEQ - 1))) * 128 + lc));
;                 }
.LBB0_442:
	v_mov_b32_e32 v195, v194
	s_or_b32 s10, s42, 1
	v_pk_mul_f32 v[116:117], v[194:195], v[116:117]
	v_pk_mul_f32 v[118:119], v[194:195], v[118:119]
	v_pk_mul_f32 v[112:113], v[194:195], v[112:113]
	s_ashr_i32 s11, s10, 31
	v_cvt_pk_bf16_f32 v116, v116, v117
	v_cvt_pk_bf16_f32 v117, v118, v119
	v_cvt_pk_bf16_f32 v118, v112, v113
	v_pk_mul_f32 v[112:113], v[194:195], v[114:115]
	s_lshl_b64 s[10:11], s[10:11], 19
	v_cvt_pk_bf16_f32 v119, v112, v113
	v_lshl_add_u64 v[112:113], v[198:199], 0, s[10:11]
	s_and_b64 vcc, exec, s[8:9]
	global_store_dwordx4 v[112:113], v[116:119], off
	s_cbranch_vccz .LBB0_446
	s_and_b64 vcc, exec, s[8:9]
	s_cbranch_vccz .LBB0_447

;     __device__ __forceinline__ void operator()(const f32x4 (&acc)[2][2][4][2], const Unit& u, int wr, int wc, int fr, int fq) const {
;     ...
;             const bool isq = u.pn < 4;
;             bf16_t* dst = (bf16_t*)(ws + (isq ? WS_Q : WS_K));
;             const int cb = (u.pn & 3) * 256;
;             const float scale = isq ? QSCALE : 1.0f;
;             float ks[2][8];
; #pragma unroll
;             for (int bj = 0; bj < 2; ++bj)
; #pragma unroll
;                 for (int i = 0; i < 8; ++i) ks[bj][i] = 0.f;
;             f32x4 rc[2][4];
;     ...
;             if (wc == 0) ROPE_LOAD(0, 0);
; #pragma unroll
;             for (int g = 0; g < 8; ++g) {
;                 const int ai = g >> 2, m = g & 3;
;                 const int r = row0 + ai * HALF + m * 16;
;                 if (wc == 0 && g + 1 < 8) ROPE_LOAD((g + 1) & 1, g + 1);
; #pragma unroll
;                 for (int bj = 0; bj < 2; ++bj) {
;                     float v[8] = {acc[ai][bj][m][0][0], acc[ai][bj][m][0][1], acc[ai][bj][m][0][2], acc[ai][bj][m][0][3],
;                                   acc[ai][bj][m][1][0], acc[ai][bj][m][1][1], acc[ai][bj][m][1][2], acc[ai][bj][m][1][3]};
;                     if (wc == 0) {
;                         const f32x4 c0 = rc[g & 1][0], c1 = rc[g & 1][1], s0 = rc[g & 1][2], s1 = rc[g & 1][3];
;                         const float cs[8] = {c0[0], c0[1], c0[2], c0[3], c1[0], c1[1], c1[2], c1[3]}, sn[8] = {s0[0], s0[1], s0[2], s0[3], s1[0], s1[1], s1[2], s1[3]};
; #pragma unroll
;                         for (int i = 0; i < 8; ++i) {
;                             const float pv = __shfl_xor(v[i], 32);
;                             v[i] = (fq < 2) ? (v[i] * cs[i] - pv * sn[i]) : (v[i] * cs[i] + pv * sn[i]);
;                         }
;                     }
;                     if (!isq) {
; #pragma unroll
;                         for (int i = 0; i < 8; ++i) ks[bj][i] += v[i];
;                     }
;                     u32x4 o; o[0] = cvt_pk_bf16(v[0] * scale, v[1] * scale); o[1] = cvt_pk_bf16(v[2] * scale, v[3] * scale);
;                     o[2] = cvt_pk_bf16(v[4] * scale, v[5] * scale); o[3] = cvt_pk_bf16(v[6] * scale, v[7] * scale);
;                     __builtin_nontemporal_store(o, (u32x4*)(dst + ((size_t)((r >> 11) * 8 + (u.pn & 3) * 2 + bj) * SEQ + (r & (SEQ - 1))) * 128 + lc));
;                 }
.LBB0_450:
	v_pk_mul_f32 v[108:109], v[194:195], v[108:109]
	v_pk_mul_f32 v[110:111], v[194:195], v[110:111]
	v_pk_mul_f32 v[104:105], v[194:195], v[104:105]
	v_lshl_add_u64 v[200:201], v[198:199], 0, s[36:37]
	v_cvt_pk_bf16_f32 v108, v108, v109
	v_cvt_pk_bf16_f32 v109, v110, v111
	v_cvt_pk_bf16_f32 v110, v104, v105
	v_pk_mul_f32 v[104:105], v[194:195], v[106:107]
	s_and_b64 vcc, exec, s[8:9]
	v_cvt_pk_bf16_f32 v111, v104, v105
	v_lshl_add_u64 v[104:105], v[200:201], 0, s[2:3]
	global_store_dwordx4 v[104:105], v[108:111], off
	s_cbranch_vccz .LBB0_453
	s_and_b64 vcc, exec, s[54:55]
	s_cbranch_vccz .LBB0_454

;     __device__ __forceinline__ void operator()(const f32x4 (&acc)[2][2][4][2], const Unit& u, int wr, int wc, int fr, int fq) const {
;     ...
;             const bool isq = u.pn < 4;
;             bf16_t* dst = (bf16_t*)(ws + (isq ? WS_Q : WS_K));
;             const int cb = (u.pn & 3) * 256;
;             const float scale = isq ? QSCALE : 1.0f;
;             float ks[2][8];
; #pragma unroll
;             for (int bj = 0; bj < 2; ++bj)
; #pragma unroll
;                 for (int i = 0; i < 8; ++i) ks[bj][i] = 0.f;
;             f32x4 rc[2][4];
;     ...
;             if (wc == 0) ROPE_LOAD(0, 0);
; #pragma unroll
;             for (int g = 0; g < 8; ++g) {
;                 const int ai = g >> 2, m = g & 3;
;                 const int r = row0 + ai * HALF + m * 16;
;                 if (wc == 0 && g + 1 < 8) ROPE_LOAD((g + 1) & 1, g + 1);
; #pragma unroll
;                 for (int bj = 0; bj < 2; ++bj) {
;                     float v[8] = {acc[ai][bj][m][0][0], acc[ai][bj][m][0][1], acc[ai][bj][m][0][2], acc[ai][bj][m][0][3],
;                                   acc[ai][bj][m][1][0], acc[ai][bj][m][1][1], acc[ai][bj][m][1][2], acc[ai][bj][m][1][3]};
;                     if (wc == 0) {
;                         const f32x4 c0 = rc[g & 1][0], c1 = rc[g & 1][1], s0 = rc[g & 1][2], s1 = rc[g & 1][3];
;                         const float cs[8] = {c0[0], c0[1], c0[2], c0[3], c1[0], c1[1], c1[2], c1[3]}, sn[8] = {s0[0], s0[1], s0[2], s0[3], s1[0], s1[1], s1[2], s1[3]};
; #pragma unroll
;                         for (int i = 0; i < 8; ++i) {
;                             const float pv = __shfl_xor(v[i], 32);
;                             v[i] = (fq < 2) ? (v[i] * cs[i] - pv * sn[i]) : (v[i] * cs[i] + pv * sn[i]);
;                         }
;                     }
;                     if (!isq) {
; #pragma unroll
;                         for (int i = 0; i < 8; ++i) ks[bj][i] += v[i];
;                     }
;                     u32x4 o; o[0] = cvt_pk_bf16(v[0] * scale, v[1] * scale); o[1] = cvt_pk_bf16(v[2] * scale, v[3] * scale);
;                     o[2] = cvt_pk_bf16(v[4] * scale, v[5] * scale); o[3] = cvt_pk_bf16(v[6] * scale, v[7] * scale);
;                     __builtin_nontemporal_store(o, (u32x4*)(dst + ((size_t)((r >> 11) * 8 + (u.pn & 3) * 2 + bj) * SEQ + (r & (SEQ - 1))) * 128 + lc));
;                 }
.LBB0_456:
	v_pk_mul_f32 v[100:101], v[194:195], v[100:101]
	v_pk_mul_f32 v[102:103], v[194:195], v[102:103]
	v_pk_mul_f32 v[96:97], v[194:195], v[96:97]
	v_cvt_pk_bf16_f32 v100, v100, v101
	v_cvt_pk_bf16_f32 v101, v102, v103
	v_cvt_pk_bf16_f32 v102, v96, v97
	v_pk_mul_f32 v[96:97], v[194:195], v[98:99]
	s_and_b64 vcc, exec, s[8:9]
	v_cvt_pk_bf16_f32 v103, v96, v97
	v_lshl_add_u64 v[96:97], v[200:201], 0, s[10:11]
	global_store_dwordx4 v[96:97], v[100:103], off
	s_cbranch_vccz .LBB0_460
	s_and_b64 vcc, exec, s[8:9]
	s_cbranch_vccz .LBB0_461

;     __device__ __forceinline__ void operator()(const f32x4 (&acc)[2][2][4][2], const Unit& u, int wr, int wc, int fr, int fq) const {
;     ...
;             const bool isq = u.pn < 4;
;             bf16_t* dst = (bf16_t*)(ws + (isq ? WS_Q : WS_K));
;             const int cb = (u.pn & 3) * 256;
;             const float scale = isq ? QSCALE : 1.0f;
;             float ks[2][8];
; #pragma unroll
;             for (int bj = 0; bj < 2; ++bj)
; #pragma unroll
;                 for (int i = 0; i < 8; ++i) ks[bj][i] = 0.f;
;             f32x4 rc[2][4];
;     ...
;             if (wc == 0) ROPE_LOAD(0, 0);
; #pragma unroll
;             for (int g = 0; g < 8; ++g) {
;                 const int ai = g >> 2, m = g & 3;
;                 const int r = row0 + ai * HALF + m * 16;
;                 if (wc == 0 && g + 1 < 8) ROPE_LOAD((g + 1) & 1, g + 1);
; #pragma unroll
;                 for (int bj = 0; bj < 2; ++bj) {
;                     float v[8] = {acc[ai][bj][m][0][0], acc[ai][bj][m][0][1], acc[ai][bj][m][0][2], acc[ai][bj][m][0][3],
;                                   acc[ai][bj][m][1][0], acc[ai][bj][m][1][1], acc[ai][bj][m][1][2], acc[ai][bj][m][1][3]};
;                     if (wc == 0) {
;                         const f32x4 c0 = rc[g & 1][0], c1 = rc[g & 1][1], s0 = rc[g & 1][2], s1 = rc[g & 1][3];
;                         const float cs[8] = {c0[0], c0[1], c0[2], c0[3], c1[0], c1[1], c1[2], c1[3]}, sn[8] = {s0[0], s0[1], s0[2], s0[3], s1[0], s1[1], s1[2], s1[3]};
; #pragma unroll
;                         for (int i = 0; i < 8; ++i) {
;                             const float pv = __shfl_xor(v[i], 32);
;                             v[i] = (fq < 2) ? (v[i] * cs[i] - pv * sn[i]) : (v[i] * cs[i] + pv * sn[i]);
;                         }
;                     }
;                     if (!isq) {
; #pragma unroll
;                         for (int i = 0; i < 8; ++i) ks[bj][i] += v[i];
;                     }
;                     u32x4 o; o[0] = cvt_pk_bf16(v[0] * scale, v[1] * scale); o[1] = cvt_pk_bf16(v[2] * scale, v[3] * scale);
;                     o[2] = cvt_pk_bf16(v[4] * scale, v[5] * scale); o[3] = cvt_pk_bf16(v[6] * scale, v[7] * scale);
;                     __builtin_nontemporal_store(o, (u32x4*)(dst + ((size_t)((r >> 11) * 8 + (u.pn & 3) * 2 + bj) * SEQ + (r & (SEQ - 1))) * 128 + lc));
;                 }
.LBB0_464:
	v_pk_mul_f32 v[92:93], v[194:195], v[92:93]
	v_pk_mul_f32 v[94:95], v[194:195], v[94:95]
	v_pk_mul_f32 v[88:89], v[194:195], v[88:89]
	v_lshl_add_u64 v[114:115], v[198:199], 0, s[38:39]
	v_cvt_pk_bf16_f32 v92, v92, v93
	v_cvt_pk_bf16_f32 v93, v94, v95
	v_cvt_pk_bf16_f32 v94, v88, v89
	v_pk_mul_f32 v[88:89], v[194:195], v[90:91]
	s_and_b64 vcc, exec, s[8:9]
	v_cvt_pk_bf16_f32 v95, v88, v89
	v_lshl_add_u64 v[88:89], v[114:115], 0, s[2:3]
	global_store_dwordx4 v[88:89], v[92:95], off
	s_cbranch_vccz .LBB0_467
	s_and_b64 vcc, exec, s[54:55]
	s_cbranch_vccz .LBB0_468

;     __device__ __forceinline__ void operator()(const f32x4 (&acc)[2][2][4][2], const Unit& u, int wr, int wc, int fr, int fq) const {
;     ...
;             const bool isq = u.pn < 4;
;             bf16_t* dst = (bf16_t*)(ws + (isq ? WS_Q : WS_K));
;             const int cb = (u.pn & 3) * 256;
;             const float scale = isq ? QSCALE : 1.0f;
;             float ks[2][8];
; #pragma unroll
;             for (int bj = 0; bj < 2; ++bj)
; #pragma unroll
;                 for (int i = 0; i < 8; ++i) ks[bj][i] = 0.f;
;             f32x4 rc[2][4];
;     ...
;             if (wc == 0) ROPE_LOAD(0, 0);
; #pragma unroll
;             for (int g = 0; g < 8; ++g) {
;                 const int ai = g >> 2, m = g & 3;
;                 const int r = row0 + ai * HALF + m * 16;
;                 if (wc == 0 && g + 1 < 8) ROPE_LOAD((g + 1) & 1, g + 1);
; #pragma unroll
;                 for (int bj = 0; bj < 2; ++bj) {
;                     float v[8] = {acc[ai][bj][m][0][0], acc[ai][bj][m][0][1], acc[ai][bj][m][0][2], acc[ai][bj][m][0][3],
;                                   acc[ai][bj][m][1][0], acc[ai][bj][m][1][1], acc[ai][bj][m][1][2], acc[ai][bj][m][1][3]};
;                     if (wc == 0) {
;                         const f32x4 c0 = rc[g & 1][0], c1 = rc[g & 1][1], s0 = rc[g & 1][2], s1 = rc[g & 1][3];
;                         const float cs[8] = {c0[0], c0[1], c0[2], c0[3], c1[0], c1[1], c1[2], c1[3]}, sn[8] = {s0[0], s0[1], s0[2], s0[3], s1[0], s1[1], s1[2], s1[3]};
; #pragma unroll
;                         for (int i = 0; i < 8; ++i) {
;                             const float pv = __shfl_xor(v[i], 32);
;                             v[i] = (fq < 2) ? (v[i] * cs[i] - pv * sn[i]) : (v[i] * cs[i] + pv * sn[i]);
;                         }
;                     }
;                     if (!isq) {
; #pragma unroll
;                         for (int i = 0; i < 8; ++i) ks[bj][i] += v[i];
;                     }
;                     u32x4 o; o[0] = cvt_pk_bf16(v[0] * scale, v[1] * scale); o[1] = cvt_pk_bf16(v[2] * scale, v[3] * scale);
;                     o[2] = cvt_pk_bf16(v[4] * scale, v[5] * scale); o[3] = cvt_pk_bf16(v[6] * scale, v[7] * scale);
;                     __builtin_nontemporal_store(o, (u32x4*)(dst + ((size_t)((r >> 11) * 8 + (u.pn & 3) * 2 + bj) * SEQ + (r & (SEQ - 1))) * 128 + lc));
;                 }
.LBB0_470:
	v_pk_mul_f32 v[84:85], v[194:195], v[84:85]
	v_pk_mul_f32 v[86:87], v[194:195], v[86:87]
	v_pk_mul_f32 v[80:81], v[194:195], v[80:81]
	v_cvt_pk_bf16_f32 v84, v84, v85
	v_cvt_pk_bf16_f32 v85, v86, v87
	v_cvt_pk_bf16_f32 v86, v80, v81
	v_pk_mul_f32 v[80:81], v[194:195], v[82:83]
	s_and_b64 vcc, exec, s[8:9]
	v_cvt_pk_bf16_f32 v87, v80, v81
	v_lshl_add_u64 v[80:81], v[114:115], 0, s[10:11]
	global_store_dwordx4 v[80:81], v[84:87], off
	s_cbranch_vccz .LBB0_474
	s_and_b64 vcc, exec, s[8:9]
	s_cbranch_vccz .LBB0_475

;     __device__ __forceinline__ void operator()(const f32x4 (&acc)[2][2][4][2], const Unit& u, int wr, int wc, int fr, int fq) const {
;     ...
;             const bool isq = u.pn < 4;
;             bf16_t* dst = (bf16_t*)(ws + (isq ? WS_Q : WS_K));
;             const int cb = (u.pn & 3) * 256;
;             const float scale = isq ? QSCALE : 1.0f;
;             float ks[2][8];
; #pragma unroll
;             for (int bj = 0; bj < 2; ++bj)
; #pragma unroll
;                 for (int i = 0; i < 8; ++i) ks[bj][i] = 0.f;
;             f32x4 rc[2][4];
;     ...
;             if (wc == 0) ROPE_LOAD(0, 0);
; #pragma unroll
;             for (int g = 0; g < 8; ++g) {
;                 const int ai = g >> 2, m = g & 3;
;                 const int r = row0 + ai * HALF + m * 16;
;                 if (wc == 0 && g + 1 < 8) ROPE_LOAD((g + 1) & 1, g + 1);
; #pragma unroll
;                 for (int bj = 0; bj < 2; ++bj) {
;                     float v[8] = {acc[ai][bj][m][0][0], acc[ai][bj][m][0][1], acc[ai][bj][m][0][2], acc[ai][bj][m][0][3],
;                                   acc[ai][bj][m][1][0], acc[ai][bj][m][1][1], acc[ai][bj][m][1][2], acc[ai][bj][m][1][3]};
;                     if (wc == 0) {
;                         const f32x4 c0 = rc[g & 1][0], c1 = rc[g & 1][1], s0 = rc[g & 1][2], s1 = rc[g & 1][3];
;                         const float cs[8] = {c0[0], c0[1], c0[2], c0[3], c1[0], c1[1], c1[2], c1[3]}, sn[8] = {s0[0], s0[1], s0[2], s0[3], s1[0], s1[1], s1[2], s1[3]};
; #pragma unroll
;                         for (int i = 0; i < 8; ++i) {
;                             const float pv = __shfl_xor(v[i], 32);
;                             v[i] = (fq < 2) ? (v[i] * cs[i] - pv * sn[i]) : (v[i] * cs[i] + pv * sn[i]);
;                         }
;                     }
;                     if (!isq) {
; #pragma unroll
;                         for (int i = 0; i < 8; ++i) ks[bj][i] += v[i];
;                     }
;                     u32x4 o; o[0] = cvt_pk_bf16(v[0] * scale, v[1] * scale); o[1] = cvt_pk_bf16(v[2] * scale, v[3] * scale);
;                     o[2] = cvt_pk_bf16(v[4] * scale, v[5] * scale); o[3] = cvt_pk_bf16(v[6] * scale, v[7] * scale);
;                     __builtin_nontemporal_store(o, (u32x4*)(dst + ((size_t)((r >> 11) * 8 + (u.pn & 3) * 2 + bj) * SEQ + (r & (SEQ - 1))) * 128 + lc));
;                 }
.LBB0_478:
	v_pk_mul_f32 v[76:77], v[194:195], v[76:77]
	v_pk_mul_f32 v[78:79], v[194:195], v[78:79]
	v_pk_mul_f32 v[72:73], v[194:195], v[72:73]
	v_lshl_add_u64 v[96:97], v[198:199], 0, s[40:41]
	v_cvt_pk_bf16_f32 v76, v76, v77
	v_cvt_pk_bf16_f32 v77, v78, v79
	v_cvt_pk_bf16_f32 v78, v72, v73
	v_pk_mul_f32 v[72:73], v[194:195], v[74:75]
	s_and_b64 vcc, exec, s[8:9]
	v_cvt_pk_bf16_f32 v79, v72, v73
	v_lshl_add_u64 v[72:73], v[96:97], 0, s[2:3]
	global_store_dwordx4 v[72:73], v[76:79], off
	s_cbranch_vccz .LBB0_481
	s_and_b64 vcc, exec, s[54:55]
	s_cbranch_vccz .LBB0_482

;     __device__ __forceinline__ void operator()(const f32x4 (&acc)[2][2][4][2], const Unit& u, int wr, int wc, int fr, int fq) const {
;     ...
;             const bool isq = u.pn < 4;
;             bf16_t* dst = (bf16_t*)(ws + (isq ? WS_Q : WS_K));
;             const int cb = (u.pn & 3) * 256;
;             const float scale = isq ? QSCALE : 1.0f;
;             float ks[2][8];
; #pragma unroll
;             for (int bj = 0; bj < 2; ++bj)
; #pragma unroll
;                 for (int i = 0; i < 8; ++i) ks[bj][i] = 0.f;
;             f32x4 rc[2][4];
;     ...
;             if (wc == 0) ROPE_LOAD(0, 0);
; #pragma unroll
;             for (int g = 0; g < 8; ++g) {
;                 const int ai = g >> 2, m = g & 3;
;                 const int r = row0 + ai * HALF + m * 16;
;                 if (wc == 0 && g + 1 < 8) ROPE_LOAD((g + 1) & 1, g + 1);
; #pragma unroll
;                 for (int bj = 0; bj < 2; ++bj) {
;                     float v[8] = {acc[ai][bj][m][0][0], acc[ai][bj][m][0][1], acc[ai][bj][m][0][2], acc[ai][bj][m][0][3],
;                                   acc[ai][bj][m][1][0], acc[ai][bj][m][1][1], acc[ai][bj][m][1][2], acc[ai][bj][m][1][3]};
;                     if (wc == 0) {
;                         const f32x4 c0 = rc[g & 1][0], c1 = rc[g & 1][1], s0 = rc[g & 1][2], s1 = rc[g & 1][3];
;                         const float cs[8] = {c0[0], c0[1], c0[2], c0[3], c1[0], c1[1], c1[2], c1[3]}, sn[8] = {s0[0], s0[1], s0[2], s0[3], s1[0], s1[1], s1[2], s1[3]};
; #pragma unroll
;                         for (int i = 0; i < 8; ++i) {
;                             const float pv = __shfl_xor(v[i], 32);
;                             v[i] = (fq < 2) ? (v[i] * cs[i] - pv * sn[i]) : (v[i] * cs[i] + pv * sn[i]);
;                         }
;                     }
;                     if (!isq) {
; #pragma unroll
;                         for (int i = 0; i < 8; ++i) ks[bj][i] += v[i];
;                     }
;                     u32x4 o; o[0] = cvt_pk_bf16(v[0] * scale, v[1] * scale); o[1] = cvt_pk_bf16(v[2] * scale, v[3] * scale);
;                     o[2] = cvt_pk_bf16(v[4] * scale, v[5] * scale); o[3] = cvt_pk_bf16(v[6] * scale, v[7] * scale);
;                     __builtin_nontemporal_store(o, (u32x4*)(dst + ((size_t)((r >> 11) * 8 + (u.pn & 3) * 2 + bj) * SEQ + (r & (SEQ - 1))) * 128 + lc));
;                 }
.LBB0_484:
	v_pk_mul_f32 v[68:69], v[194:195], v[68:69]
	v_pk_mul_f32 v[70:71], v[194:195], v[70:71]
	v_pk_mul_f32 v[64:65], v[194:195], v[64:65]
	v_cvt_pk_bf16_f32 v68, v68, v69
	v_cvt_pk_bf16_f32 v69, v70, v71
	v_cvt_pk_bf16_f32 v70, v64, v65
	v_pk_mul_f32 v[64:65], v[194:195], v[66:67]
	s_and_b64 vcc, exec, s[8:9]
	v_cvt_pk_bf16_f32 v71, v64, v65
	v_lshl_add_u64 v[64:65], v[96:97], 0, s[10:11]
	v_add_u32_e32 v88, 0x80, v192
	global_store_dwordx4 v[64:65], v[68:71], off
	s_cbranch_vccz .LBB0_488
	s_and_b64 vcc, exec, s[8:9]
	s_cbranch_vccz .LBB0_489

;     __device__ __forceinline__ void operator()(const f32x4 (&acc)[2][2][4][2], const Unit& u, int wr, int wc, int fr, int fq) const {
;     ...
;             const bool isq = u.pn < 4;
;             bf16_t* dst = (bf16_t*)(ws + (isq ? WS_Q : WS_K));
;             const int cb = (u.pn & 3) * 256;
;             const float scale = isq ? QSCALE : 1.0f;
;             float ks[2][8];
; #pragma unroll
;             for (int bj = 0; bj < 2; ++bj)
; #pragma unroll
;                 for (int i = 0; i < 8; ++i) ks[bj][i] = 0.f;
;             f32x4 rc[2][4];
;     ...
;             if (wc == 0) ROPE_LOAD(0, 0);
; #pragma unroll
;             for (int g = 0; g < 8; ++g) {
;                 const int ai = g >> 2, m = g & 3;
;                 const int r = row0 + ai * HALF + m * 16;
;                 if (wc == 0 && g + 1 < 8) ROPE_LOAD((g + 1) & 1, g + 1);
; #pragma unroll
;                 for (int bj = 0; bj < 2; ++bj) {
;                     float v[8] = {acc[ai][bj][m][0][0], acc[ai][bj][m][0][1], acc[ai][bj][m][0][2], acc[ai][bj][m][0][3],
;                                   acc[ai][bj][m][1][0], acc[ai][bj][m][1][1], acc[ai][bj][m][1][2], acc[ai][bj][m][1][3]};
;                     if (wc == 0) {
;                         const f32x4 c0 = rc[g & 1][0], c1 = rc[g & 1][1], s0 = rc[g & 1][2], s1 = rc[g & 1][3];
;                         const float cs[8] = {c0[0], c0[1], c0[2], c0[3], c1[0], c1[1], c1[2], c1[3]}, sn[8] = {s0[0], s0[1], s0[2], s0[3], s1[0], s1[1], s1[2], s1[3]};
; #pragma unroll
;                         for (int i = 0; i < 8; ++i) {
;                             const float pv = __shfl_xor(v[i], 32);
;                             v[i] = (fq < 2) ? (v[i] * cs[i] - pv * sn[i]) : (v[i] * cs[i] + pv * sn[i]);
;                         }
;                     }
;                     if (!isq) {
; #pragma unroll
;                         for (int i = 0; i < 8; ++i) ks[bj][i] += v[i];
;                     }
;                     u32x4 o; o[0] = cvt_pk_bf16(v[0] * scale, v[1] * scale); o[1] = cvt_pk_bf16(v[2] * scale, v[3] * scale);
;                     o[2] = cvt_pk_bf16(v[4] * scale, v[5] * scale); o[3] = cvt_pk_bf16(v[6] * scale, v[7] * scale);
;                     __builtin_nontemporal_store(o, (u32x4*)(dst + ((size_t)((r >> 11) * 8 + (u.pn & 3) * 2 + bj) * SEQ + (r & (SEQ - 1))) * 128 + lc));
;                 }
.LBB0_492:
	v_ashrrev_i32_e32 v64, 8, v88
	v_and_or_b32 v82, v64, -8, s17
	v_lshlrev_b32_e32 v64, 8, v88
	v_pk_mul_f32 v[60:61], v[194:195], v[60:61]
	v_pk_mul_f32 v[62:63], v[194:195], v[62:63]
	v_pk_mul_f32 v[56:57], v[194:195], v[56:57]
	v_and_b32_e32 v168, 0x7cf00, v64
	v_cvt_pk_bf16_f32 v60, v60, v61
	v_cvt_pk_bf16_f32 v61, v62, v63
	v_cvt_pk_bf16_f32 v62, v56, v57
	v_pk_mul_f32 v[56:57], v[194:195], v[58:59]
	v_ashrrev_i32_e32 v83, 31, v82
	v_lshl_add_u64 v[64:65], v[196:197], 0, v[168:169]
	v_cvt_pk_bf16_f32 v63, v56, v57
	v_lshlrev_b64 v[56:57], 19, v[82:83]
	v_lshl_add_u64 v[58:59], v[64:65], 0, v[56:57]
	s_and_b64 vcc, exec, s[8:9]
	global_store_dwordx4 v[58:59], v[60:63], off
	s_cbranch_vccz .LBB0_495
	s_and_b64 vcc, exec, s[54:55]
	s_cbranch_vccz .LBB0_496

;     __device__ __forceinline__ void operator()(const f32x4 (&acc)[2][2][4][2], const Unit& u, int wr, int wc, int fr, int fq) const {
;     ...
;             const bool isq = u.pn < 4;
;             bf16_t* dst = (bf16_t*)(ws + (isq ? WS_Q : WS_K));
;             const int cb = (u.pn & 3) * 256;
;             const float scale = isq ? QSCALE : 1.0f;
;             float ks[2][8];
; #pragma unroll
;             for (int bj = 0; bj < 2; ++bj)
; #pragma unroll
;                 for (int i = 0; i < 8; ++i) ks[bj][i] = 0.f;
;             f32x4 rc[2][4];
;     ...
;             if (wc == 0) ROPE_LOAD(0, 0);
; #pragma unroll
;             for (int g = 0; g < 8; ++g) {
;                 const int ai = g >> 2, m = g & 3;
;                 const int r = row0 + ai * HALF + m * 16;
;                 if (wc == 0 && g + 1 < 8) ROPE_LOAD((g + 1) & 1, g + 1);
; #pragma unroll
;                 for (int bj = 0; bj < 2; ++bj) {
;                     float v[8] = {acc[ai][bj][m][0][0], acc[ai][bj][m][0][1], acc[ai][bj][m][0][2], acc[ai][bj][m][0][3],
;                                   acc[ai][bj][m][1][0], acc[ai][bj][m][1][1], acc[ai][bj][m][1][2], acc[ai][bj][m][1][3]};
;                     if (wc == 0) {
;                         const f32x4 c0 = rc[g & 1][0], c1 = rc[g & 1][1], s0 = rc[g & 1][2], s1 = rc[g & 1][3];
;                         const float cs[8] = {c0[0], c0[1], c0[2], c0[3], c1[0], c1[1], c1[2], c1[3]}, sn[8] = {s0[0], s0[1], s0[2], s0[3], s1[0], s1[1], s1[2], s1[3]};
; #pragma unroll
;                         for (int i = 0; i < 8; ++i) {
;                             const float pv = __shfl_xor(v[i], 32);
;                             v[i] = (fq < 2) ? (v[i] * cs[i] - pv * sn[i]) : (v[i] * cs[i] + pv * sn[i]);
;                         }
;                     }
;                     if (!isq) {
; #pragma unroll
;                         for (int i = 0; i < 8; ++i) ks[bj][i] += v[i];
;                     }
;                     u32x4 o; o[0] = cvt_pk_bf16(v[0] * scale, v[1] * scale); o[1] = cvt_pk_bf16(v[2] * scale, v[3] * scale);
;                     o[2] = cvt_pk_bf16(v[4] * scale, v[5] * scale); o[3] = cvt_pk_bf16(v[6] * scale, v[7] * scale);
;                     __builtin_nontemporal_store(o, (u32x4*)(dst + ((size_t)((r >> 11) * 8 + (u.pn & 3) * 2 + bj) * SEQ + (r & (SEQ - 1))) * 128 + lc));
;                 }
.LBB0_498:
	v_pk_mul_f32 v[52:53], v[194:195], v[52:53]
	v_pk_mul_f32 v[54:55], v[194:195], v[54:55]
	v_pk_mul_f32 v[48:49], v[194:195], v[48:49]
	v_cvt_pk_bf16_f32 v52, v52, v53
	v_cvt_pk_bf16_f32 v53, v54, v55
	v_cvt_pk_bf16_f32 v54, v48, v49
	v_pk_mul_f32 v[48:49], v[194:195], v[50:51]
	s_and_b64 vcc, exec, s[8:9]
	v_cvt_pk_bf16_f32 v55, v48, v49
	v_or_b32_e32 v48, 1, v82
	v_ashrrev_i32_e32 v49, 31, v48
	v_lshlrev_b64 v[48:49], 19, v[48:49]
	v_lshl_add_u64 v[50:51], v[64:65], 0, v[48:49]
	global_store_dwordx4 v[50:51], v[52:55], off
	s_cbranch_vccz .LBB0_502
	s_and_b64 vcc, exec, s[8:9]
	s_cbranch_vccz .LBB0_503

;     __device__ __forceinline__ void operator()(const f32x4 (&acc)[2][2][4][2], const Unit& u, int wr, int wc, int fr, int fq) const {
;     ...
;             const bool isq = u.pn < 4;
;             bf16_t* dst = (bf16_t*)(ws + (isq ? WS_Q : WS_K));
;             const int cb = (u.pn & 3) * 256;
;             const float scale = isq ? QSCALE : 1.0f;
;             float ks[2][8];
; #pragma unroll
;             for (int bj = 0; bj < 2; ++bj)
; #pragma unroll
;                 for (int i = 0; i < 8; ++i) ks[bj][i] = 0.f;
;             f32x4 rc[2][4];
;     ...
;             if (wc == 0) ROPE_LOAD(0, 0);
; #pragma unroll
;             for (int g = 0; g < 8; ++g) {
;                 const int ai = g >> 2, m = g & 3;
;                 const int r = row0 + ai * HALF + m * 16;
;                 if (wc == 0 && g + 1 < 8) ROPE_LOAD((g + 1) & 1, g + 1);
; #pragma unroll
;                 for (int bj = 0; bj < 2; ++bj) {
;                     float v[8] = {acc[ai][bj][m][0][0], acc[ai][bj][m][0][1], acc[ai][bj][m][0][2], acc[ai][bj][m][0][3],
;                                   acc[ai][bj][m][1][0], acc[ai][bj][m][1][1], acc[ai][bj][m][1][2], acc[ai][bj][m][1][3]};
;                     if (wc == 0) {
;                         const f32x4 c0 = rc[g & 1][0], c1 = rc[g & 1][1], s0 = rc[g & 1][2], s1 = rc[g & 1][3];
;                         const float cs[8] = {c0[0], c0[1], c0[2], c0[3], c1[0], c1[1], c1[2], c1[3]}, sn[8] = {s0[0], s0[1], s0[2], s0[3], s1[0], s1[1], s1[2], s1[3]};
; #pragma unroll
;                         for (int i = 0; i < 8; ++i) {
;                             const float pv = __shfl_xor(v[i], 32);
;                             v[i] = (fq < 2) ? (v[i] * cs[i] - pv * sn[i]) : (v[i] * cs[i] + pv * sn[i]);
;                         }
;                     }
;                     if (!isq) {
; #pragma unroll
;                         for (int i = 0; i < 8; ++i) ks[bj][i] += v[i];
;                     }
;                     u32x4 o; o[0] = cvt_pk_bf16(v[0] * scale, v[1] * scale); o[1] = cvt_pk_bf16(v[2] * scale, v[3] * scale);
;                     o[2] = cvt_pk_bf16(v[4] * scale, v[5] * scale); o[3] = cvt_pk_bf16(v[6] * scale, v[7] * scale);
;                     __builtin_nontemporal_store(o, (u32x4*)(dst + ((size_t)((r >> 11) * 8 + (u.pn & 3) * 2 + bj) * SEQ + (r & (SEQ - 1))) * 128 + lc));
;                 }
.LBB0_506:
	v_pk_mul_f32 v[44:45], v[194:195], v[44:45]
	v_pk_mul_f32 v[46:47], v[194:195], v[46:47]
	v_pk_mul_f32 v[40:41], v[194:195], v[40:41]
	v_lshl_add_u64 v[66:67], v[64:65], 0, s[36:37]
	v_cvt_pk_bf16_f32 v44, v44, v45
	v_cvt_pk_bf16_f32 v45, v46, v47
	v_cvt_pk_bf16_f32 v46, v40, v41
	v_pk_mul_f32 v[40:41], v[194:195], v[42:43]
	s_and_b64 vcc, exec, s[8:9]
	v_cvt_pk_bf16_f32 v47, v40, v41
	v_lshl_add_u64 v[40:41], v[66:67], 0, v[56:57]
	global_store_dwordx4 v[40:41], v[44:47], off
	s_cbranch_vccz .LBB0_509
	s_and_b64 vcc, exec, s[54:55]
	s_cbranch_vccz .LBB0_510

;     __device__ __forceinline__ void operator()(const f32x4 (&acc)[2][2][4][2], const Unit& u, int wr, int wc, int fr, int fq) const {
;     ...
;             const bool isq = u.pn < 4;
;             bf16_t* dst = (bf16_t*)(ws + (isq ? WS_Q : WS_K));
;             const int cb = (u.pn & 3) * 256;
;             const float scale = isq ? QSCALE : 1.0f;
;             float ks[2][8];
; #pragma unroll
;             for (int bj = 0; bj < 2; ++bj)
; #pragma unroll
;                 for (int i = 0; i < 8; ++i) ks[bj][i] = 0.f;
;             f32x4 rc[2][4];
;     ...
;             if (wc == 0) ROPE_LOAD(0, 0);
; #pragma unroll
;             for (int g = 0; g < 8; ++g) {
;                 const int ai = g >> 2, m = g & 3;
;                 const int r = row0 + ai * HALF + m * 16;
;                 if (wc == 0 && g + 1 < 8) ROPE_LOAD((g + 1) & 1, g + 1);
; #pragma unroll
;                 for (int bj = 0; bj < 2; ++bj) {
;                     float v[8] = {acc[ai][bj][m][0][0], acc[ai][bj][m][0][1], acc[ai][bj][m][0][2], acc[ai][bj][m][0][3],
;                                   acc[ai][bj][m][1][0], acc[ai][bj][m][1][1], acc[ai][bj][m][1][2], acc[ai][bj][m][1][3]};
;                     if (wc == 0) {
;                         const f32x4 c0 = rc[g & 1][0], c1 = rc[g & 1][1], s0 = rc[g & 1][2], s1 = rc[g & 1][3];
;                         const float cs[8] = {c0[0], c0[1], c0[2], c0[3], c1[0], c1[1], c1[2], c1[3]}, sn[8] = {s0[0], s0[1], s0[2], s0[3], s1[0], s1[1], s1[2], s1[3]};
; #pragma unroll
;                         for (int i = 0; i < 8; ++i) {
;                             const float pv = __shfl_xor(v[i], 32);
;                             v[i] = (fq < 2) ? (v[i] * cs[i] - pv * sn[i]) : (v[i] * cs[i] + pv * sn[i]);
;                         }
;                     }
;                     if (!isq) {
; #pragma unroll
;                         for (int i = 0; i < 8; ++i) ks[bj][i] += v[i];
;                     }
;                     u32x4 o; o[0] = cvt_pk_bf16(v[0] * scale, v[1] * scale); o[1] = cvt_pk_bf16(v[2] * scale, v[3] * scale);
;                     o[2] = cvt_pk_bf16(v[4] * scale, v[5] * scale); o[3] = cvt_pk_bf16(v[6] * scale, v[7] * scale);
;                     __builtin_nontemporal_store(o, (u32x4*)(dst + ((size_t)((r >> 11) * 8 + (u.pn & 3) * 2 + bj) * SEQ + (r & (SEQ - 1))) * 128 + lc));
;                 }
.LBB0_512:
	v_pk_mul_f32 v[36:37], v[194:195], v[36:37]
	v_pk_mul_f32 v[38:39], v[194:195], v[38:39]
	v_pk_mul_f32 v[32:33], v[194:195], v[32:33]
	v_cvt_pk_bf16_f32 v36, v36, v37
	v_cvt_pk_bf16_f32 v37, v38, v39
	v_cvt_pk_bf16_f32 v38, v32, v33
	v_pk_mul_f32 v[32:33], v[194:195], v[34:35]
	s_and_b64 vcc, exec, s[8:9]
	v_cvt_pk_bf16_f32 v39, v32, v33
	v_lshl_add_u64 v[32:33], v[66:67], 0, v[48:49]
	global_store_dwordx4 v[32:33], v[36:39], off
	s_cbranch_vccz .LBB0_516
	s_and_b64 vcc, exec, s[8:9]
	s_cbranch_vccz .LBB0_517

;     __device__ __forceinline__ void operator()(const f32x4 (&acc)[2][2][4][2], const Unit& u, int wr, int wc, int fr, int fq) const {
;     ...
;             const bool isq = u.pn < 4;
;             bf16_t* dst = (bf16_t*)(ws + (isq ? WS_Q : WS_K));
;             const int cb = (u.pn & 3) * 256;
;             const float scale = isq ? QSCALE : 1.0f;
;             float ks[2][8];
; #pragma unroll
;             for (int bj = 0; bj < 2; ++bj)
; #pragma unroll
;                 for (int i = 0; i < 8; ++i) ks[bj][i] = 0.f;
;             f32x4 rc[2][4];
;     ...
;             if (wc == 0) ROPE_LOAD(0, 0);
; #pragma unroll
;             for (int g = 0; g < 8; ++g) {
;                 const int ai = g >> 2, m = g & 3;
;                 const int r = row0 + ai * HALF + m * 16;
;                 if (wc == 0 && g + 1 < 8) ROPE_LOAD((g + 1) & 1, g + 1);
; #pragma unroll
;                 for (int bj = 0; bj < 2; ++bj) {
;                     float v[8] = {acc[ai][bj][m][0][0], acc[ai][bj][m][0][1], acc[ai][bj][m][0][2], acc[ai][bj][m][0][3],
;                                   acc[ai][bj][m][1][0], acc[ai][bj][m][1][1], acc[ai][bj][m][1][2], acc[ai][bj][m][1][3]};
;                     if (wc == 0) {
;                         const f32x4 c0 = rc[g & 1][0], c1 = rc[g & 1][1], s0 = rc[g & 1][2], s1 = rc[g & 1][3];
;                         const float cs[8] = {c0[0], c0[1], c0[2], c0[3], c1[0], c1[1], c1[2], c1[3]}, sn[8] = {s0[0], s0[1], s0[2], s0[3], s1[0], s1[1], s1[2], s1[3]};
; #pragma unroll
;                         for (int i = 0; i < 8; ++i) {
;                             const float pv = __shfl_xor(v[i], 32);
;                             v[i] = (fq < 2) ? (v[i] * cs[i] - pv * sn[i]) : (v[i] * cs[i] + pv * sn[i]);
;                         }
;                     }
;                     if (!isq) {
; #pragma unroll
;                         for (int i = 0; i < 8; ++i) ks[bj][i] += v[i];
;                     }
;                     u32x4 o; o[0] = cvt_pk_bf16(v[0] * scale, v[1] * scale); o[1] = cvt_pk_bf16(v[2] * scale, v[3] * scale);
;                     o[2] = cvt_pk_bf16(v[4] * scale, v[5] * scale); o[3] = cvt_pk_bf16(v[6] * scale, v[7] * scale);
;                     __builtin_nontemporal_store(o, (u32x4*)(dst + ((size_t)((r >> 11) * 8 + (u.pn & 3) * 2 + bj) * SEQ + (r & (SEQ - 1))) * 128 + lc));
;                 }
.LBB0_520:
	v_pk_mul_f32 v[28:29], v[194:195], v[28:29]
	v_pk_mul_f32 v[30:31], v[194:195], v[30:31]
	v_pk_mul_f32 v[24:25], v[194:195], v[24:25]
	v_lshl_add_u64 v[50:51], v[64:65], 0, s[38:39]
	v_cvt_pk_bf16_f32 v28, v28, v29
	v_cvt_pk_bf16_f32 v29, v30, v31
	v_cvt_pk_bf16_f32 v30, v24, v25
	v_pk_mul_f32 v[24:25], v[194:195], v[26:27]
	s_and_b64 vcc, exec, s[8:9]
	v_cvt_pk_bf16_f32 v31, v24, v25
	v_lshl_add_u64 v[24:25], v[50:51], 0, v[56:57]
	global_store_dwordx4 v[24:25], v[28:31], off
	s_cbranch_vccz .LBB0_523
	s_and_b64 vcc, exec, s[54:55]
	s_cbranch_vccz .LBB0_524

;     __device__ __forceinline__ void operator()(const f32x4 (&acc)[2][2][4][2], const Unit& u, int wr, int wc, int fr, int fq) const {
;     ...
;             const bool isq = u.pn < 4;
;             bf16_t* dst = (bf16_t*)(ws + (isq ? WS_Q : WS_K));
;             const int cb = (u.pn & 3) * 256;
;             const float scale = isq ? QSCALE : 1.0f;
;             float ks[2][8];
; #pragma unroll
;             for (int bj = 0; bj < 2; ++bj)
; #pragma unroll
;                 for (int i = 0; i < 8; ++i) ks[bj][i] = 0.f;
;             f32x4 rc[2][4];
;     ...
;             if (wc == 0) ROPE_LOAD(0, 0);
; #pragma unroll
;             for (int g = 0; g < 8; ++g) {
;                 const int ai = g >> 2, m = g & 3;
;                 const int r = row0 + ai * HALF + m * 16;
;                 if (wc == 0 && g + 1 < 8) ROPE_LOAD((g + 1) & 1, g + 1);
; #pragma unroll
;                 for (int bj = 0; bj < 2; ++bj) {
;                     float v[8] = {acc[ai][bj][m][0][0], acc[ai][bj][m][0][1], acc[ai][bj][m][0][2], acc[ai][bj][m][0][3],
;                                   acc[ai][bj][m][1][0], acc[ai][bj][m][1][1], acc[ai][bj][m][1][2], acc[ai][bj][m][1][3]};
;                     if (wc == 0) {
;                         const f32x4 c0 = rc[g & 1][0], c1 = rc[g & 1][1], s0 = rc[g & 1][2], s1 = rc[g & 1][3];
;                         const float cs[8] = {c0[0], c0[1], c0[2], c0[3], c1[0], c1[1], c1[2], c1[3]}, sn[8] = {s0[0], s0[1], s0[2], s0[3], s1[0], s1[1], s1[2], s1[3]};
; #pragma unroll
;                         for (int i = 0; i < 8; ++i) {
;                             const float pv = __shfl_xor(v[i], 32);
;                             v[i] = (fq < 2) ? (v[i] * cs[i] - pv * sn[i]) : (v[i] * cs[i] + pv * sn[i]);
;                         }
;                     }
;                     if (!isq) {
; #pragma unroll
;                         for (int i = 0; i < 8; ++i) ks[bj][i] += v[i];
;                     }
;                     u32x4 o; o[0] = cvt_pk_bf16(v[0] * scale, v[1] * scale); o[1] = cvt_pk_bf16(v[2] * scale, v[3] * scale);
;                     o[2] = cvt_pk_bf16(v[4] * scale, v[5] * scale); o[3] = cvt_pk_bf16(v[6] * scale, v[7] * scale);
;                     __builtin_nontemporal_store(o, (u32x4*)(dst + ((size_t)((r >> 11) * 8 + (u.pn & 3) * 2 + bj) * SEQ + (r & (SEQ - 1))) * 128 + lc));
;                 }
.LBB0_526:
	v_pk_mul_f32 v[20:21], v[194:195], v[20:21]
	v_pk_mul_f32 v[22:23], v[194:195], v[22:23]
	v_pk_mul_f32 v[16:17], v[194:195], v[16:17]
	v_cvt_pk_bf16_f32 v20, v20, v21
	v_cvt_pk_bf16_f32 v21, v22, v23
	v_cvt_pk_bf16_f32 v22, v16, v17
	v_pk_mul_f32 v[16:17], v[194:195], v[18:19]
	s_and_b64 vcc, exec, s[8:9]
	v_cvt_pk_bf16_f32 v23, v16, v17
	v_lshl_add_u64 v[16:17], v[50:51], 0, v[48:49]
	global_store_dwordx4 v[16:17], v[20:23], off
	s_cbranch_vccz .LBB0_529
	s_and_b64 vcc, exec, s[54:55]
	s_cbranch_vccz .LBB0_530

;     __device__ __forceinline__ void operator()(const f32x4 (&acc)[2][2][4][2], const Unit& u, int wr, int wc, int fr, int fq) const {
;     ...
;             const bool isq = u.pn < 4;
;             bf16_t* dst = (bf16_t*)(ws + (isq ? WS_Q : WS_K));
;             const int cb = (u.pn & 3) * 256;
;             const float scale = isq ? QSCALE : 1.0f;
;             float ks[2][8];
; #pragma unroll
;             for (int bj = 0; bj < 2; ++bj)
; #pragma unroll
;                 for (int i = 0; i < 8; ++i) ks[bj][i] = 0.f;
;             f32x4 rc[2][4];
;     ...
;             if (wc == 0) ROPE_LOAD(0, 0);
; #pragma unroll
;             for (int g = 0; g < 8; ++g) {
;                 const int ai = g >> 2, m = g & 3;
;                 const int r = row0 + ai * HALF + m * 16;
;                 if (wc == 0 && g + 1 < 8) ROPE_LOAD((g + 1) & 1, g + 1);
; #pragma unroll
;                 for (int bj = 0; bj < 2; ++bj) {
;                     float v[8] = {acc[ai][bj][m][0][0], acc[ai][bj][m][0][1], acc[ai][bj][m][0][2], acc[ai][bj][m][0][3],
;                                   acc[ai][bj][m][1][0], acc[ai][bj][m][1][1], acc[ai][bj][m][1][2], acc[ai][bj][m][1][3]};
;                     if (wc == 0) {
;                         const f32x4 c0 = rc[g & 1][0], c1 = rc[g & 1][1], s0 = rc[g & 1][2], s1 = rc[g & 1][3];
;                         const float cs[8] = {c0[0], c0[1], c0[2], c0[3], c1[0], c1[1], c1[2], c1[3]}, sn[8] = {s0[0], s0[1], s0[2], s0[3], s1[0], s1[1], s1[2], s1[3]};
; #pragma unroll
;                         for (int i = 0; i < 8; ++i) {
;                             const float pv = __shfl_xor(v[i], 32);
;                             v[i] = (fq < 2) ? (v[i] * cs[i] - pv * sn[i]) : (v[i] * cs[i] + pv * sn[i]);
;                         }
;                     }
;                     if (!isq) {
; #pragma unroll
;                         for (int i = 0; i < 8; ++i) ks[bj][i] += v[i];
;                     }
;                     u32x4 o; o[0] = cvt_pk_bf16(v[0] * scale, v[1] * scale); o[1] = cvt_pk_bf16(v[2] * scale, v[3] * scale);
;                     o[2] = cvt_pk_bf16(v[4] * scale, v[5] * scale); o[3] = cvt_pk_bf16(v[6] * scale, v[7] * scale);
;                     __builtin_nontemporal_store(o, (u32x4*)(dst + ((size_t)((r >> 11) * 8 + (u.pn & 3) * 2 + bj) * SEQ + (r & (SEQ - 1))) * 128 + lc));
;                 }
.LBB0_532:
	v_pk_mul_f32 v[12:13], v[194:195], v[12:13]
	v_pk_mul_f32 v[14:15], v[194:195], v[14:15]
	v_pk_mul_f32 v[8:9], v[194:195], v[8:9]
	v_lshl_add_u64 v[32:33], v[64:65], 0, s[40:41]
	v_cvt_pk_bf16_f32 v12, v12, v13
	v_cvt_pk_bf16_f32 v13, v14, v15
	v_cvt_pk_bf16_f32 v14, v8, v9
	v_pk_mul_f32 v[8:9], v[194:195], v[10:11]
	s_and_b64 vcc, exec, s[8:9]
	v_cvt_pk_bf16_f32 v15, v8, v9
	v_lshl_add_u64 v[8:9], v[32:33], 0, v[56:57]
	global_store_dwordx4 v[8:9], v[12:15], off
	s_cbranch_vccz .LBB0_535
	s_and_b64 vcc, exec, s[54:55]
	s_cbranch_vccz .LBB0_536

; __device__ __forceinline__ unsigned cvt_pk_bf16(float lo, float hi) { const bf16x2_t r = __builtin_convertvector((f32x2_t){lo, hi}, bf16x2_t); return __builtin_bit_cast(unsigned, r); }
;     __device__ __forceinline__ void operator()(const f32x4 (&acc)[2][2][4][2], const Unit& u, int wr, int wc, int fr, int fq) const {
;     ...
;                     u32x4 o; o[0] = cvt_pk_bf16(v[0] * scale, v[1] * scale); o[1] = cvt_pk_bf16(v[2] * scale, v[3] * scale);
;                     o[2] = cvt_pk_bf16(v[4] * scale, v[5] * scale); o[3] = cvt_pk_bf16(v[6] * scale, v[7] * scale);
;                     __builtin_nontemporal_store(o, (u32x4*)(dst + ((size_t)((r >> 11) * 8 + (u.pn & 3) * 2 + bj) * SEQ + (r & (SEQ - 1))) * 128 + lc));
;                 }
;             }
;     ...
;             if (!isq) {
;                 const int b = u.pm >> 3, blk = u.pm & 7;
; #pragma unroll
;                 for (int bj = 0; bj < 2; ++bj) {
;                     const int h = (u.pn & 3) * 2 + bj;
; #pragma unroll
;                     for (int i = 0; i < 8; ++i) {
;                         float s = ks[bj][i];
;                         s += __shfl_xor(s, 1); s += __shfl_xor(s, 2); s += __shfl_xor(s, 4); s += __shfl_xor(s, 8);
;                         if (fr == 0) atomicAdd(kmean + (((size_t)b * 8 + h) * 8 + blk) * 128 + lc + i, s * (1.0f / 256.0f));
;                     }
.LBB0_538:
	v_pk_mul_f32 v[4:5], v[194:195], v[4:5]
	v_pk_mul_f32 v[6:7], v[194:195], v[6:7]
	v_pk_mul_f32 v[0:1], v[194:195], v[0:1]
	v_cvt_pk_bf16_f32 v4, v4, v5
	v_cvt_pk_bf16_f32 v5, v6, v7
	v_cvt_pk_bf16_f32 v6, v0, v1
	v_pk_mul_f32 v[0:1], v[194:195], v[2:3]
	s_andn2_b64 vcc, exec, s[54:55]
	v_cvt_pk_bf16_f32 v7, v0, v1
	v_lshl_add_u64 v[0:1], v[32:33], 0, v[48:49]
	global_store_dwordx4 v[0:1], v[4:7], off
	s_cbranch_vccnz .LBB0_315
	v_and_b32_e32 v1, 64, v211
	v_xor_b32_e32 v0, 1, v211
	v_add_u32_e32 v1, 64, v1
	v_cmp_lt_i32_e32 vcc, v0, v1
	s_ashr_i32 s2, s77, 3
	s_ashr_i32 s3, s2, 31
	v_cndmask_b32_e32 v0, v211, v0, vcc
	v_lshlrev_b32_e32 v2, 2, v0
	ds_bpermute_b32 v4, v2, v22
	v_xor_b32_e32 v0, 2, v211
	v_cmp_lt_i32_e32 vcc, v0, v1
	s_and_b32 s8, s77, 7
	s_lshl_b64 s[2:3], s[2:3], 6
	v_cndmask_b32_e32 v0, v211, v0, vcc
	v_lshlrev_b32_e32 v3, 2, v0
	s_waitcnt lgkmcnt(0)
	v_add_f32_e32 v5, v22, v4
	ds_bpermute_b32 v6, v3, v5
	v_xor_b32_e32 v0, 4, v211
	v_cmp_lt_i32_e32 vcc, v0, v1
	s_or_b32 s2, s2, s8
	s_lshl_b32 s8, s17, 3
	v_cndmask_b32_e32 v0, v211, v0, vcc
	v_lshlrev_b32_e32 v4, 2, v0
	v_xor_b32_e32 v0, 8, v211
	v_cmp_lt_i32_e32 vcc, v0, v1
	s_waitcnt lgkmcnt(0)
	v_add_f32_e32 v1, v5, v6
	ds_bpermute_b32 v6, v4, v1
	v_cndmask_b32_e32 v0, v211, v0, vcc
	v_lshlrev_b32_e32 v5, 2, v0
	s_or_b32 s2, s2, s8
	s_lshl_b64 s[8:9], s[2:3], 9
	s_waitcnt lgkmcnt(0)
	v_add_f32_e32 v6, v1, v6
	ds_bpermute_b32 v7, v5, v6
	v_lshl_add_u64 v[0:1], v[178:179], 0, s[8:9]
	s_and_saveexec_b64 s[8:9], s[4:5]
	s_cbranch_execz .LBB0_541
	s_waitcnt lgkmcnt(0)
	v_add_f32_e32 v6, v6, v7
	v_mul_f32_e32 v6, 0x3b800000, v6
	global_atomic_add_f32 v[0:1], v6, off

; __device__ __forceinline__ unsigned cvt_pk_bf16(float lo, float hi) { const bf16x2_t r = __builtin_convertvector((f32x2_t){lo, hi}, bf16x2_t); return __builtin_bit_cast(unsigned, r); }
; __device__ __forceinline__ float silu_fast(float x) { return x * __builtin_amdgcn_rcpf(1.0f + __builtin_amdgcn_exp2f(-x * 1.4426950408889634f)); }
;     __device__ __forceinline__ void operator()(const f32x4 (&acc)[2][2][4][2], const Unit& u, int wr, int wc, int fr, int fq) const {
;     ...
;         } else {
;             const bool isog = u.pn >= 20;
;             size_t woff; int cb;
;             if (u.pn < 20) { woff = WS_VG; cb = (u.pn - 16) * 256; }
;             else { woff = WS_OG; cb = (u.pn - 20) * 256; }
;             bf16_t* dst = (bf16_t*)(ws + woff);
; #pragma unroll
;             for (int ai = 0; ai < 2; ++ai)
; #pragma unroll
;                 for (int m = 0; m < 4; ++m) {
;                     const int r = row0 + ai * HALF + m * 16;
; #pragma unroll
;                     for (int bj = 0; bj < 2; ++bj) {
;                         f32x4 v0 = acc[ai][bj][m][0], v1 = acc[ai][bj][m][1];
;                         if (isog) {
; #pragma unroll
;                             for (int i = 0; i < 4; ++i) { v0[i] = silu_fast(v0[i]); v1[i] = silu_fast(v1[i]); }
;                         }
;                         u32x4 o; o[0] = cvt_pk_bf16(v0[0], v0[1]); o[1] = cvt_pk_bf16(v0[2], v0[3]); o[2] = cvt_pk_bf16(v1[0], v1[1]); o[3] = cvt_pk_bf16(v1[2], v1[3]);
;                         __builtin_nontemporal_store(o, (u32x4*)(dst + ((size_t)((r >> 11) * 4 + (cb >> 8)) * SEQ + (r & (SEQ - 1))) * 256 + bj * HALF + lc));
;                     }
;                 }
.LBB0_1382:
	s_cmp_lt_u32 s76, 20
	s_cselect_b64 s[8:9], -1, 0
	s_and_b64 s[8:9], s[8:9], exec
	s_mov_b32 s8, 0x48188000
	s_cselect_b32 s18, s8, 0x4a188000
	s_mov_b32 s8, 0xfffff0
	s_cselect_b32 s8, s8, 0xffffec
	s_add_i32 s8, s8, s76
	s_and_b32 s10, s8, 0xffffff
	s_ashr_i32 s8, s15, 9
	s_and_b32 s8, s8, -4
	s_add_i32 s8, s8, s10
	s_ashr_i32 s9, s8, 31
	v_lshl_add_u64 v[136:137], v[174:175], 0, s[18:19]
	s_lshl_b64 s[8:9], s[8:9], 20
	v_lshlrev_b32_e32 v140, 9, v192
	v_lshl_add_u64 v[138:139], v[136:137], 0, s[8:9]
	v_and_b32_e32 v168, 0xf9e00, v140
	v_lshl_add_u64 v[138:139], v[138:139], 0, v[168:169]
	v_cvt_pk_bf16_f32 v128, v128, v129
	v_cvt_pk_bf16_f32 v129, v130, v131
	v_cvt_pk_bf16_f32 v130, v132, v133
	v_cvt_pk_bf16_f32 v131, v134, v135
	global_store_dwordx4 v[138:139], v[128:131], off
	v_mov_b64_e32 v[134:135], v[114:115]
	s_andn2_b64 vcc, exec, s[2:3]
	v_cndmask_b32_e64 v128, 0, 1, s[2:3]
	v_cmp_ne_u32_e64 s[8:9], 1, v128
	v_mov_b64_e32 v[130:131], v[118:119]
	v_mov_b64_e32 v[128:129], v[116:117]
	v_mov_b64_e32 v[132:133], v[112:113]
	s_cbranch_vccnz .LBB0_1384
	v_mul_f32_e32 v129, 0xbfb8aa3b, v112
	v_mul_f32_e32 v130, 0xbfb8aa3b, v117
	v_exp_f32_e32 v129, v129
	v_exp_f32_e32 v130, v130
	v_mul_f32_e32 v131, 0xbfb8aa3b, v118
	v_mul_f32_e32 v133, 0xbfb8aa3b, v114
	v_add_f32_e32 v129, 1.0, v129
	v_rcp_f32_e32 v132, v129
	v_add_f32_e32 v129, 1.0, v130
	v_mul_f32_e32 v130, 0xbfb8aa3b, v113
	v_exp_f32_e32 v130, v130
	v_exp_f32_e32 v131, v131
	v_exp_f32_e32 v133, v133
	v_mul_f32_e32 v128, 0xbfb8aa3b, v116
	v_add_f32_e32 v140, 1.0, v130
	v_add_f32_e32 v130, 1.0, v131
	v_add_f32_e32 v131, 1.0, v133
	v_mul_f32_e32 v133, 0xbfb8aa3b, v119
	v_mul_f32_e32 v134, 0xbfb8aa3b, v115
	v_exp_f32_e32 v128, v128
	v_exp_f32_e32 v133, v133
	v_exp_f32_e32 v135, v134
	v_rcp_f32_e32 v134, v131
	v_add_f32_e32 v128, 1.0, v128
	v_add_f32_e32 v131, 1.0, v133
	v_add_f32_e32 v133, 1.0, v135
	v_rcp_f32_e32 v128, v128
	v_rcp_f32_e32 v129, v129
	v_rcp_f32_e32 v130, v130
	v_rcp_f32_e32 v131, v131
	v_rcp_f32_e32 v135, v133
	v_rcp_f32_e32 v133, v140
	v_pk_mul_f32 v[128:129], v[116:117], v[128:129]
	v_pk_mul_f32 v[130:131], v[118:119], v[130:131]
	v_pk_mul_f32 v[134:135], v[114:115], v[134:135]
	v_pk_mul_f32 v[132:133], v[112:113], v[132:133]

;     __device__ __forceinline__ void operator()(const f32x4 (&acc)[2][2][4][2], const Unit& u, int wr, int wc, int fr, int fq) const {
;     ...
;             BC_LOAD(0, 0);
; #pragma unroll
;             for (int g = 0; g < 16; ++g) {
;                 const int ai = g >> 3, m = (g >> 1) & 3, bj = g & 1;
;                 const int r = row0 + ai * HALF + m * 16;
;                 if (g + 1 < 16) BC_LOAD((g + 1) & 1, g + 1);
;                 {
;                     {
;                         const int col = cb + bj * HALF + lc;
;                         const size_t hoff = ((size_t)((r >> 11) * 4 + (col >> 7)) * SEQ + (r & (SEQ - 1))) * 128 + (col & 127);
;                         const f32x4 b0 = bc[g & 1][0], b1 = bc[g & 1][1];
;                         const f32x4 v0 = acc[ai][bj][m][0], v1 = acc[ai][bj][m][1];
;                         const float L2E = 1.4426950408889634f;
;                         if (isq) {
;                             const float s = 0.08838834764831845f;
;                             u32x4 o; o[0] = cvt_pk_bf16(v0[0] * s * __builtin_amdgcn_exp2f(b0[0] * L2E), v0[1] * s * __builtin_amdgcn_exp2f(b0[1] * L2E));
;                             o[1] = cvt_pk_bf16(v0[2] * s * __builtin_amdgcn_exp2f(b0[2] * L2E), v0[3] * s * __builtin_amdgcn_exp2f(b0[3] * L2E));
;                             o[2] = cvt_pk_bf16(v1[0] * s * __builtin_amdgcn_exp2f(b1[0] * L2E), v1[1] * s * __builtin_amdgcn_exp2f(b1[1] * L2E));
;                             o[3] = cvt_pk_bf16(v1[2] * s * __builtin_amdgcn_exp2f(b1[2] * L2E), v1[3] * s * __builtin_amdgcn_exp2f(b1[3] * L2E));
;                             __builtin_nontemporal_store(o, (u32x4*)(d0 + hoff));
;                         } else {
;                             u32x4 o;
;                             o[0] = cvt_pk_bf16(v0[0] * __builtin_amdgcn_exp2f(-b0[0] * L2E), v0[1] * __builtin_amdgcn_exp2f(-b0[1] * L2E));
;                             o[1] = cvt_pk_bf16(v0[2] * __builtin_amdgcn_exp2f(-b0[2] * L2E), v0[3] * __builtin_amdgcn_exp2f(-b0[3] * L2E));
;                             o[2] = cvt_pk_bf16(v1[0] * __builtin_amdgcn_exp2f(-b1[0] * L2E), v1[1] * __builtin_amdgcn_exp2f(-b1[1] * L2E));
;                             o[3] = cvt_pk_bf16(v1[2] * __builtin_amdgcn_exp2f(-b1[2] * L2E), v1[3] * __builtin_amdgcn_exp2f(-b1[3] * L2E));
;                             __builtin_nontemporal_store(o, (u32x4*)(d0 + hoff));
.LBB0_1418:
	s_and_b64 s[2:3], s[2:3], exec
	s_cselect_b32 s2, s72, 0x47188000
	v_readlane_b32 s80, v252, 28
	v_readlane_b32 s81, v252, 29
	s_add_u32 s2, s80, s2
	s_addc_u32 s3, s81, 0
	s_ashr_i32 s9, s15, 9
	s_and_b32 s33, s9, -4
	s_lshl_b32 s17, s10, 1
	s_waitcnt vmcnt(2)
	v_mul_f32_e32 v132, s8, v135
	s_add_i32 s10, s33, s17
	v_exp_f32_e32 v132, v132
	s_ashr_i32 s11, s10, 31
	v_lshlrev_b32_e32 v133, 7, v192
	s_lshl_b64 s[8:9], s[10:11], 19
	v_and_b32_e32 v156, 0x3e780, v133
	s_add_u32 s10, s2, s8
	v_mul_f32_e32 v132, v149, v132
	s_addc_u32 s11, s3, s9
	v_lshlrev_b32_e32 v150, 1, v156
	v_mov_b32_e32 v151, v169
	v_cvt_pk_bf16_f32 v143, v148, v132
	v_lshl_add_u64 v[132:133], s[10:11], 0, v[150:151]
	v_lshlrev_b32_e32 v148, 1, v170
	v_mov_b32_e32 v149, v169
	v_lshl_add_u64 v[132:133], v[132:133], 0, v[148:149]
	global_store_dwordx4 v[132:133], v[140:143], off
	v_or_b32_e32 v132, 16, v192
	v_ashrrev_i32_e32 v133, 31, v132
	v_lshlrev_b64 v[132:133], 11, v[132:133]
	v_lshl_add_u64 v[132:133], s[22:23], 0, v[132:133]
	v_lshl_add_u64 v[152:153], v[168:169], 2, v[132:133]
	global_load_dwordx4 v[132:135], v[152:153], off offset:16
	global_load_dwordx4 v[140:143], v[152:153], off
	s_waitcnt vmcnt(3)
	v_cndmask_b32_e64 v144, 0, 1, s[42:43]
	v_cmp_ne_u32_e64 s[8:9], 1, v144
	s_andn2_b64 vcc, exec, s[42:43]
	s_mov_b64 s[42:43], -1
	v_readlane_b32 s82, v252, 30
	v_readlane_b32 s83, v252, 31
	s_cbranch_vccnz .LBB0_1420
	v_mul_f32_e32 v144, 0xbfb8aa3b, v136
	v_mul_f32_e32 v145, 0xbfb8aa3b, v137
	v_exp_f32_e32 v144, v144
	v_exp_f32_e32 v145, v145
	v_mul_f32_e32 v146, 0xbfb8aa3b, v138
	v_mul_f32_e32 v147, 0xbfb8aa3b, v139
	v_exp_f32_e32 v146, v146
	v_pk_mul_f32 v[144:145], v[116:117], v[144:145]
	v_exp_f32_e32 v147, v147
	v_cvt_pk_bf16_f32 v144, v144, v145
	v_mul_f32_e32 v145, 0xbfb8aa3b, v128
	v_exp_f32_e32 v154, v145
	v_mul_f32_e32 v145, 0xbfb8aa3b, v129
	v_exp_f32_e32 v155, v145
	v_mul_f32_e32 v145, 0xbfb8aa3b, v130
	v_exp_f32_e32 v149, v145
	v_pk_mul_f32 v[146:147], v[118:119], v[146:147]
	s_mov_b64 s[42:43], 0
	v_cvt_pk_bf16_f32 v145, v146, v147
	v_pk_mul_f32 v[146:147], v[112:113], v[154:155]
	v_mul_f32_e32 v154, v114, v149
	v_cvt_pk_bf16_f32 v146, v146, v147
	v_mov_b32_e32 v155, v115

;     __device__ __forceinline__ void operator()(const f32x4 (&acc)[2][2][4][2], const Unit& u, int wr, int wc, int fr, int fq) const {
;     ...
;             BC_LOAD(0, 0);
; #pragma unroll
;             for (int g = 0; g < 16; ++g) {
;                 const int ai = g >> 3, m = (g >> 1) & 3, bj = g & 1;
;                 const int r = row0 + ai * HALF + m * 16;
;                 if (g + 1 < 16) BC_LOAD((g + 1) & 1, g + 1);
;                 {
;                     {
;                         const int col = cb + bj * HALF + lc;
;                         const size_t hoff = ((size_t)((r >> 11) * 4 + (col >> 7)) * SEQ + (r & (SEQ - 1))) * 128 + (col & 127);
;                         const f32x4 b0 = bc[g & 1][0], b1 = bc[g & 1][1];
;                         const f32x4 v0 = acc[ai][bj][m][0], v1 = acc[ai][bj][m][1];
;                         const float L2E = 1.4426950408889634f;
;                         if (isq) {
;                             const float s = 0.08838834764831845f;
;                             u32x4 o; o[0] = cvt_pk_bf16(v0[0] * s * __builtin_amdgcn_exp2f(b0[0] * L2E), v0[1] * s * __builtin_amdgcn_exp2f(b0[1] * L2E));
;                             o[1] = cvt_pk_bf16(v0[2] * s * __builtin_amdgcn_exp2f(b0[2] * L2E), v0[3] * s * __builtin_amdgcn_exp2f(b0[3] * L2E));
;                             o[2] = cvt_pk_bf16(v1[0] * s * __builtin_amdgcn_exp2f(b1[0] * L2E), v1[1] * s * __builtin_amdgcn_exp2f(b1[1] * L2E));
;                             o[3] = cvt_pk_bf16(v1[2] * s * __builtin_amdgcn_exp2f(b1[2] * L2E), v1[3] * s * __builtin_amdgcn_exp2f(b1[3] * L2E));
;                             __builtin_nontemporal_store(o, (u32x4*)(d0 + hoff));
;                         } else {
;                             u32x4 o;
;                             o[0] = cvt_pk_bf16(v0[0] * __builtin_amdgcn_exp2f(-b0[0] * L2E), v0[1] * __builtin_amdgcn_exp2f(-b0[1] * L2E));
;                             o[1] = cvt_pk_bf16(v0[2] * __builtin_amdgcn_exp2f(-b0[2] * L2E), v0[3] * __builtin_amdgcn_exp2f(-b0[3] * L2E));
;                             o[2] = cvt_pk_bf16(v1[0] * __builtin_amdgcn_exp2f(-b1[0] * L2E), v1[1] * __builtin_amdgcn_exp2f(-b1[1] * L2E));
;                             o[3] = cvt_pk_bf16(v1[2] * __builtin_amdgcn_exp2f(-b1[2] * L2E), v1[3] * __builtin_amdgcn_exp2f(-b1[3] * L2E));
;                             __builtin_nontemporal_store(o, (u32x4*)(d0 + hoff));
.LBB0_1422:
	v_mul_f32_e32 v128, s18, v131
	s_or_b32 s18, s17, 1
	v_exp_f32_e32 v128, v128
	s_add_i32 s42, s33, s18
	s_ashr_i32 s43, s42, 31
	s_lshl_b64 s[42:43], s[42:43], 19
	s_add_u32 s42, s2, s42
	v_mul_f32_e32 v128, v155, v128
	s_addc_u32 s43, s3, s43
	v_mov_b32_e32 v151, v169
	v_cvt_pk_bf16_f32 v147, v154, v128
	v_lshl_add_u64 v[128:129], s[42:43], 0, v[150:151]
	v_mov_b32_e32 v149, v169
	v_lshl_add_u64 v[128:129], v[128:129], 0, v[148:149]
	global_store_dwordx4 v[128:129], v[144:147], off
	global_load_dwordx4 v[128:131], v[152:153], off offset:528
	s_nop 0
	global_load_dwordx4 v[136:139], v[152:153], off offset:512
	s_and_b64 vcc, exec, s[8:9]
	s_mov_b64 s[48:49], -1
	s_cbranch_vccnz .LBB0_1424
	s_waitcnt vmcnt(3)
	v_mul_f32_e32 v144, 0xbfb8aa3b, v140
	v_mul_f32_e32 v145, 0xbfb8aa3b, v141
	v_exp_f32_e32 v144, v144
	v_exp_f32_e32 v145, v145
	v_mul_f32_e32 v146, 0xbfb8aa3b, v142
	v_mul_f32_e32 v147, 0xbfb8aa3b, v143
	v_exp_f32_e32 v146, v146
	v_pk_mul_f32 v[144:145], v[108:109], v[144:145]
	v_exp_f32_e32 v147, v147
	v_cvt_pk_bf16_f32 v144, v144, v145
	v_mul_f32_e32 v145, 0xbfb8aa3b, v132
	v_exp_f32_e32 v150, v145
	v_mul_f32_e32 v145, 0xbfb8aa3b, v133
	v_exp_f32_e32 v151, v145
	v_mul_f32_e32 v145, 0xbfb8aa3b, v134
	v_exp_f32_e32 v149, v145
	v_pk_mul_f32 v[146:147], v[110:111], v[146:147]
	s_mov_b64 s[48:49], 0
	v_cvt_pk_bf16_f32 v145, v146, v147
	v_pk_mul_f32 v[146:147], v[104:105], v[150:151]
	v_mul_f32_e32 v152, v106, v149
	v_cvt_pk_bf16_f32 v146, v146, v147
	v_mov_b32_e32 v153, v107

;     __device__ __forceinline__ void operator()(const f32x4 (&acc)[2][2][4][2], const Unit& u, int wr, int wc, int fr, int fq) const {
;     ...
;             BC_LOAD(0, 0);
; #pragma unroll
;             for (int g = 0; g < 16; ++g) {
;                 const int ai = g >> 3, m = (g >> 1) & 3, bj = g & 1;
;                 const int r = row0 + ai * HALF + m * 16;
;                 if (g + 1 < 16) BC_LOAD((g + 1) & 1, g + 1);
;                 {
;                     {
;                         const int col = cb + bj * HALF + lc;
;                         const size_t hoff = ((size_t)((r >> 11) * 4 + (col >> 7)) * SEQ + (r & (SEQ - 1))) * 128 + (col & 127);
;                         const f32x4 b0 = bc[g & 1][0], b1 = bc[g & 1][1];
;                         const f32x4 v0 = acc[ai][bj][m][0], v1 = acc[ai][bj][m][1];
;                         const float L2E = 1.4426950408889634f;
;                         if (isq) {
;                             const float s = 0.08838834764831845f;
;                             u32x4 o; o[0] = cvt_pk_bf16(v0[0] * s * __builtin_amdgcn_exp2f(b0[0] * L2E), v0[1] * s * __builtin_amdgcn_exp2f(b0[1] * L2E));
;                             o[1] = cvt_pk_bf16(v0[2] * s * __builtin_amdgcn_exp2f(b0[2] * L2E), v0[3] * s * __builtin_amdgcn_exp2f(b0[3] * L2E));
;                             o[2] = cvt_pk_bf16(v1[0] * s * __builtin_amdgcn_exp2f(b1[0] * L2E), v1[1] * s * __builtin_amdgcn_exp2f(b1[1] * L2E));
;                             o[3] = cvt_pk_bf16(v1[2] * s * __builtin_amdgcn_exp2f(b1[2] * L2E), v1[3] * s * __builtin_amdgcn_exp2f(b1[3] * L2E));
;                             __builtin_nontemporal_store(o, (u32x4*)(d0 + hoff));
;                         } else {
;                             u32x4 o;
;                             o[0] = cvt_pk_bf16(v0[0] * __builtin_amdgcn_exp2f(-b0[0] * L2E), v0[1] * __builtin_amdgcn_exp2f(-b0[1] * L2E));
;                             o[1] = cvt_pk_bf16(v0[2] * __builtin_amdgcn_exp2f(-b0[2] * L2E), v0[3] * __builtin_amdgcn_exp2f(-b0[3] * L2E));
;                             o[2] = cvt_pk_bf16(v1[0] * __builtin_amdgcn_exp2f(-b1[0] * L2E), v1[1] * __builtin_amdgcn_exp2f(-b1[1] * L2E));
;                             o[3] = cvt_pk_bf16(v1[2] * __builtin_amdgcn_exp2f(-b1[2] * L2E), v1[3] * __builtin_amdgcn_exp2f(-b1[3] * L2E));
;                             __builtin_nontemporal_store(o, (u32x4*)(d0 + hoff));
.LBB0_1426:
	s_waitcnt vmcnt(3)
	v_mul_f32_e32 v132, s33, v135
	v_exp_f32_e32 v132, v132
	v_or_b32_e32 v133, 0x800, v156
	v_mov_b32_e32 v151, v169
	v_lshlrev_b32_e32 v150, 1, v133
	v_mul_f32_e32 v132, v153, v132
	v_cvt_pk_bf16_f32 v147, v152, v132
	v_lshl_add_u64 v[132:133], s[10:11], 0, v[150:151]
	v_mov_b32_e32 v149, v169
	v_lshl_add_u64 v[132:133], v[132:133], 0, v[148:149]
	global_store_dwordx4 v[132:133], v[144:147], off
	v_or_b32_e32 v132, 32, v192
	v_ashrrev_i32_e32 v133, 31, v132
	v_lshlrev_b64 v[132:133], 11, v[132:133]
	v_lshl_add_u64 v[132:133], s[22:23], 0, v[132:133]
	v_lshl_add_u64 v[152:153], v[168:169], 2, v[132:133]
	global_load_dwordx4 v[132:135], v[152:153], off offset:16
	global_load_dwordx4 v[140:143], v[152:153], off
	s_waitcnt vmcnt(3)
	s_and_b64 vcc, exec, s[8:9]
	s_mov_b64 s[48:49], -1
	s_cbranch_vccnz .LBB0_1428
	v_mul_f32_e32 v144, 0xbfb8aa3b, v136
	v_mul_f32_e32 v145, 0xbfb8aa3b, v137
	v_exp_f32_e32 v144, v144
	v_exp_f32_e32 v145, v145
	v_mul_f32_e32 v146, 0xbfb8aa3b, v138
	v_mul_f32_e32 v147, 0xbfb8aa3b, v139
	v_exp_f32_e32 v146, v146
	v_pk_mul_f32 v[144:145], v[100:101], v[144:145]
	v_exp_f32_e32 v147, v147
	v_cvt_pk_bf16_f32 v144, v144, v145
	v_mul_f32_e32 v145, 0xbfb8aa3b, v128
	v_exp_f32_e32 v154, v145
	v_mul_f32_e32 v145, 0xbfb8aa3b, v129
	v_exp_f32_e32 v155, v145
	v_mul_f32_e32 v145, 0xbfb8aa3b, v130
	v_exp_f32_e32 v149, v145
	v_pk_mul_f32 v[146:147], v[102:103], v[146:147]
	s_mov_b64 s[48:49], 0
	v_cvt_pk_bf16_f32 v145, v146, v147
	v_pk_mul_f32 v[146:147], v[96:97], v[154:155]
	v_mul_f32_e32 v154, v98, v149
	v_cvt_pk_bf16_f32 v146, v146, v147
	v_mov_b32_e32 v155, v99

;     __device__ __forceinline__ void operator()(const f32x4 (&acc)[2][2][4][2], const Unit& u, int wr, int wc, int fr, int fq) const {
;     ...
;             BC_LOAD(0, 0);
; #pragma unroll
;             for (int g = 0; g < 16; ++g) {
;                 const int ai = g >> 3, m = (g >> 1) & 3, bj = g & 1;
;                 const int r = row0 + ai * HALF + m * 16;
;                 if (g + 1 < 16) BC_LOAD((g + 1) & 1, g + 1);
;                 {
;                     {
;                         const int col = cb + bj * HALF + lc;
;                         const size_t hoff = ((size_t)((r >> 11) * 4 + (col >> 7)) * SEQ + (r & (SEQ - 1))) * 128 + (col & 127);
;                         const f32x4 b0 = bc[g & 1][0], b1 = bc[g & 1][1];
;                         const f32x4 v0 = acc[ai][bj][m][0], v1 = acc[ai][bj][m][1];
;                         const float L2E = 1.4426950408889634f;
;                         if (isq) {
;                             const float s = 0.08838834764831845f;
;                             u32x4 o; o[0] = cvt_pk_bf16(v0[0] * s * __builtin_amdgcn_exp2f(b0[0] * L2E), v0[1] * s * __builtin_amdgcn_exp2f(b0[1] * L2E));
;                             o[1] = cvt_pk_bf16(v0[2] * s * __builtin_amdgcn_exp2f(b0[2] * L2E), v0[3] * s * __builtin_amdgcn_exp2f(b0[3] * L2E));
;                             o[2] = cvt_pk_bf16(v1[0] * s * __builtin_amdgcn_exp2f(b1[0] * L2E), v1[1] * s * __builtin_amdgcn_exp2f(b1[1] * L2E));
;                             o[3] = cvt_pk_bf16(v1[2] * s * __builtin_amdgcn_exp2f(b1[2] * L2E), v1[3] * s * __builtin_amdgcn_exp2f(b1[3] * L2E));
;                             __builtin_nontemporal_store(o, (u32x4*)(d0 + hoff));
;                         } else {
;                             u32x4 o;
;                             o[0] = cvt_pk_bf16(v0[0] * __builtin_amdgcn_exp2f(-b0[0] * L2E), v0[1] * __builtin_amdgcn_exp2f(-b0[1] * L2E));
;                             o[1] = cvt_pk_bf16(v0[2] * __builtin_amdgcn_exp2f(-b0[2] * L2E), v0[3] * __builtin_amdgcn_exp2f(-b0[3] * L2E));
;                             o[2] = cvt_pk_bf16(v1[0] * __builtin_amdgcn_exp2f(-b1[0] * L2E), v1[1] * __builtin_amdgcn_exp2f(-b1[1] * L2E));
;                             o[3] = cvt_pk_bf16(v1[2] * __builtin_amdgcn_exp2f(-b1[2] * L2E), v1[3] * __builtin_amdgcn_exp2f(-b1[3] * L2E));
;                             __builtin_nontemporal_store(o, (u32x4*)(d0 + hoff));
.LBB0_1430:
	v_mul_f32_e32 v128, s33, v131
	v_exp_f32_e32 v130, v128
	v_mov_b32_e32 v151, v169
	v_mov_b32_e32 v149, v169
	v_lshl_add_u64 v[128:129], s[42:43], 0, v[150:151]
	v_mul_f32_e32 v130, v155, v130
	v_cvt_pk_bf16_f32 v147, v154, v130
	v_lshl_add_u64 v[128:129], v[128:129], 0, v[148:149]
	global_store_dwordx4 v[128:129], v[144:147], off
	global_load_dwordx4 v[128:131], v[152:153], off offset:528
	s_nop 0
	global_load_dwordx4 v[136:139], v[152:153], off offset:512
	s_and_b64 vcc, exec, s[8:9]
	s_mov_b64 s[48:49], -1
	s_cbranch_vccnz .LBB0_1432
	s_waitcnt vmcnt(3)
	v_mul_f32_e32 v144, 0xbfb8aa3b, v140
	v_mul_f32_e32 v145, 0xbfb8aa3b, v141
	v_exp_f32_e32 v144, v144
	v_exp_f32_e32 v145, v145
	v_mul_f32_e32 v146, 0xbfb8aa3b, v142
	v_mul_f32_e32 v147, 0xbfb8aa3b, v143
	v_exp_f32_e32 v146, v146
	v_pk_mul_f32 v[144:145], v[92:93], v[144:145]
	v_exp_f32_e32 v147, v147
	v_cvt_pk_bf16_f32 v144, v144, v145
	v_mul_f32_e32 v145, 0xbfb8aa3b, v132
	v_exp_f32_e32 v150, v145
	v_mul_f32_e32 v145, 0xbfb8aa3b, v133
	v_exp_f32_e32 v151, v145
	v_mul_f32_e32 v145, 0xbfb8aa3b, v134
	v_exp_f32_e32 v149, v145
	v_pk_mul_f32 v[146:147], v[94:95], v[146:147]
	s_mov_b64 s[48:49], 0
	v_cvt_pk_bf16_f32 v145, v146, v147
	v_pk_mul_f32 v[146:147], v[88:89], v[150:151]
	v_mul_f32_e32 v152, v90, v149
	v_cvt_pk_bf16_f32 v146, v146, v147
	v_mov_b32_e32 v153, v91

;     __device__ __forceinline__ void operator()(const f32x4 (&acc)[2][2][4][2], const Unit& u, int wr, int wc, int fr, int fq) const {
;     ...
;             BC_LOAD(0, 0);
; #pragma unroll
;             for (int g = 0; g < 16; ++g) {
;                 const int ai = g >> 3, m = (g >> 1) & 3, bj = g & 1;
;                 const int r = row0 + ai * HALF + m * 16;
;                 if (g + 1 < 16) BC_LOAD((g + 1) & 1, g + 1);
;                 {
;                     {
;                         const int col = cb + bj * HALF + lc;
;                         const size_t hoff = ((size_t)((r >> 11) * 4 + (col >> 7)) * SEQ + (r & (SEQ - 1))) * 128 + (col & 127);
;                         const f32x4 b0 = bc[g & 1][0], b1 = bc[g & 1][1];
;                         const f32x4 v0 = acc[ai][bj][m][0], v1 = acc[ai][bj][m][1];
;                         const float L2E = 1.4426950408889634f;
;                         if (isq) {
;                             const float s = 0.08838834764831845f;
;                             u32x4 o; o[0] = cvt_pk_bf16(v0[0] * s * __builtin_amdgcn_exp2f(b0[0] * L2E), v0[1] * s * __builtin_amdgcn_exp2f(b0[1] * L2E));
;                             o[1] = cvt_pk_bf16(v0[2] * s * __builtin_amdgcn_exp2f(b0[2] * L2E), v0[3] * s * __builtin_amdgcn_exp2f(b0[3] * L2E));
;                             o[2] = cvt_pk_bf16(v1[0] * s * __builtin_amdgcn_exp2f(b1[0] * L2E), v1[1] * s * __builtin_amdgcn_exp2f(b1[1] * L2E));
;                             o[3] = cvt_pk_bf16(v1[2] * s * __builtin_amdgcn_exp2f(b1[2] * L2E), v1[3] * s * __builtin_amdgcn_exp2f(b1[3] * L2E));
;                             __builtin_nontemporal_store(o, (u32x4*)(d0 + hoff));
;                         } else {
;                             u32x4 o;
;                             o[0] = cvt_pk_bf16(v0[0] * __builtin_amdgcn_exp2f(-b0[0] * L2E), v0[1] * __builtin_amdgcn_exp2f(-b0[1] * L2E));
;                             o[1] = cvt_pk_bf16(v0[2] * __builtin_amdgcn_exp2f(-b0[2] * L2E), v0[3] * __builtin_amdgcn_exp2f(-b0[3] * L2E));
;                             o[2] = cvt_pk_bf16(v1[0] * __builtin_amdgcn_exp2f(-b1[0] * L2E), v1[1] * __builtin_amdgcn_exp2f(-b1[1] * L2E));
;                             o[3] = cvt_pk_bf16(v1[2] * __builtin_amdgcn_exp2f(-b1[2] * L2E), v1[3] * __builtin_amdgcn_exp2f(-b1[3] * L2E));
;                             __builtin_nontemporal_store(o, (u32x4*)(d0 + hoff));
.LBB0_1434:
	s_waitcnt vmcnt(3)
	v_mul_f32_e32 v132, s33, v135
	v_exp_f32_e32 v132, v132
	v_or_b32_e32 v133, 0x1000, v156
	v_mov_b32_e32 v151, v169
	v_lshlrev_b32_e32 v150, 1, v133
	v_mul_f32_e32 v132, v153, v132
	v_cvt_pk_bf16_f32 v147, v152, v132
	v_lshl_add_u64 v[132:133], s[10:11], 0, v[150:151]
	v_mov_b32_e32 v149, v169
	v_lshl_add_u64 v[132:133], v[132:133], 0, v[148:149]
	global_store_dwordx4 v[132:133], v[144:147], off
	v_or_b32_e32 v132, 48, v192
	v_ashrrev_i32_e32 v133, 31, v132
	v_lshlrev_b64 v[132:133], 11, v[132:133]
	v_lshl_add_u64 v[132:133], s[22:23], 0, v[132:133]
	v_lshl_add_u64 v[152:153], v[168:169], 2, v[132:133]
	global_load_dwordx4 v[132:135], v[152:153], off offset:16
	global_load_dwordx4 v[140:143], v[152:153], off
	s_waitcnt vmcnt(3)
	s_and_b64 vcc, exec, s[8:9]
	s_mov_b64 s[48:49], -1
	s_cbranch_vccnz .LBB0_1436
	v_mul_f32_e32 v144, 0xbfb8aa3b, v136
	v_mul_f32_e32 v145, 0xbfb8aa3b, v137
	v_exp_f32_e32 v144, v144
	v_exp_f32_e32 v145, v145
	v_mul_f32_e32 v146, 0xbfb8aa3b, v138
	v_mul_f32_e32 v147, 0xbfb8aa3b, v139
	v_exp_f32_e32 v146, v146
	v_pk_mul_f32 v[144:145], v[84:85], v[144:145]
	v_exp_f32_e32 v147, v147
	v_cvt_pk_bf16_f32 v144, v144, v145
	v_mul_f32_e32 v145, 0xbfb8aa3b, v128
	v_exp_f32_e32 v154, v145
	v_mul_f32_e32 v145, 0xbfb8aa3b, v129
	v_exp_f32_e32 v155, v145
	v_mul_f32_e32 v145, 0xbfb8aa3b, v130
	v_exp_f32_e32 v149, v145
	v_pk_mul_f32 v[146:147], v[86:87], v[146:147]
	s_mov_b64 s[48:49], 0
	v_cvt_pk_bf16_f32 v145, v146, v147
	v_pk_mul_f32 v[146:147], v[80:81], v[154:155]
	v_mul_f32_e32 v154, v82, v149
	v_cvt_pk_bf16_f32 v146, v146, v147
	v_mov_b32_e32 v155, v83

;     __device__ __forceinline__ void operator()(const f32x4 (&acc)[2][2][4][2], const Unit& u, int wr, int wc, int fr, int fq) const {
;     ...
;             BC_LOAD(0, 0);
; #pragma unroll
;             for (int g = 0; g < 16; ++g) {
;                 const int ai = g >> 3, m = (g >> 1) & 3, bj = g & 1;
;                 const int r = row0 + ai * HALF + m * 16;
;                 if (g + 1 < 16) BC_LOAD((g + 1) & 1, g + 1);
;                 {
;                     {
;                         const int col = cb + bj * HALF + lc;
;                         const size_t hoff = ((size_t)((r >> 11) * 4 + (col >> 7)) * SEQ + (r & (SEQ - 1))) * 128 + (col & 127);
;                         const f32x4 b0 = bc[g & 1][0], b1 = bc[g & 1][1];
;                         const f32x4 v0 = acc[ai][bj][m][0], v1 = acc[ai][bj][m][1];
;                         const float L2E = 1.4426950408889634f;
;                         if (isq) {
;                             const float s = 0.08838834764831845f;
;                             u32x4 o; o[0] = cvt_pk_bf16(v0[0] * s * __builtin_amdgcn_exp2f(b0[0] * L2E), v0[1] * s * __builtin_amdgcn_exp2f(b0[1] * L2E));
;                             o[1] = cvt_pk_bf16(v0[2] * s * __builtin_amdgcn_exp2f(b0[2] * L2E), v0[3] * s * __builtin_amdgcn_exp2f(b0[3] * L2E));
;                             o[2] = cvt_pk_bf16(v1[0] * s * __builtin_amdgcn_exp2f(b1[0] * L2E), v1[1] * s * __builtin_amdgcn_exp2f(b1[1] * L2E));
;                             o[3] = cvt_pk_bf16(v1[2] * s * __builtin_amdgcn_exp2f(b1[2] * L2E), v1[3] * s * __builtin_amdgcn_exp2f(b1[3] * L2E));
;                             __builtin_nontemporal_store(o, (u32x4*)(d0 + hoff));
;                         } else {
;                             u32x4 o;
;                             o[0] = cvt_pk_bf16(v0[0] * __builtin_amdgcn_exp2f(-b0[0] * L2E), v0[1] * __builtin_amdgcn_exp2f(-b0[1] * L2E));
;                             o[1] = cvt_pk_bf16(v0[2] * __builtin_amdgcn_exp2f(-b0[2] * L2E), v0[3] * __builtin_amdgcn_exp2f(-b0[3] * L2E));
;                             o[2] = cvt_pk_bf16(v1[0] * __builtin_amdgcn_exp2f(-b1[0] * L2E), v1[1] * __builtin_amdgcn_exp2f(-b1[1] * L2E));
;                             o[3] = cvt_pk_bf16(v1[2] * __builtin_amdgcn_exp2f(-b1[2] * L2E), v1[3] * __builtin_amdgcn_exp2f(-b1[3] * L2E));
;                             __builtin_nontemporal_store(o, (u32x4*)(d0 + hoff));
.LBB0_1438:
	v_mul_f32_e32 v128, s33, v131
	v_exp_f32_e32 v130, v128
	v_mov_b32_e32 v151, v169
	v_mov_b32_e32 v149, v169
	v_lshl_add_u64 v[128:129], s[42:43], 0, v[150:151]
	v_mul_f32_e32 v130, v155, v130
	v_cvt_pk_bf16_f32 v147, v154, v130
	v_lshl_add_u64 v[128:129], v[128:129], 0, v[148:149]
	global_store_dwordx4 v[128:129], v[144:147], off
	global_load_dwordx4 v[128:131], v[152:153], off offset:528
	s_nop 0
	global_load_dwordx4 v[136:139], v[152:153], off offset:512
	s_and_b64 vcc, exec, s[8:9]
	s_mov_b64 s[48:49], -1
	s_cbranch_vccnz .LBB0_1440
	s_waitcnt vmcnt(3)
	v_mul_f32_e32 v144, 0xbfb8aa3b, v140
	v_mul_f32_e32 v145, 0xbfb8aa3b, v141
	v_exp_f32_e32 v144, v144
	v_exp_f32_e32 v145, v145
	v_mul_f32_e32 v146, 0xbfb8aa3b, v142
	v_mul_f32_e32 v147, 0xbfb8aa3b, v143
	v_exp_f32_e32 v146, v146
	v_pk_mul_f32 v[144:145], v[76:77], v[144:145]
	v_exp_f32_e32 v147, v147
	v_cvt_pk_bf16_f32 v144, v144, v145
	v_mul_f32_e32 v145, 0xbfb8aa3b, v132
	v_exp_f32_e32 v150, v145
	v_mul_f32_e32 v145, 0xbfb8aa3b, v133
	v_exp_f32_e32 v151, v145
	v_mul_f32_e32 v145, 0xbfb8aa3b, v134
	v_exp_f32_e32 v149, v145
	v_pk_mul_f32 v[146:147], v[78:79], v[146:147]
	s_mov_b64 s[48:49], 0
	v_cvt_pk_bf16_f32 v145, v146, v147
	v_pk_mul_f32 v[146:147], v[72:73], v[150:151]
	v_mul_f32_e32 v150, v74, v149
	v_cvt_pk_bf16_f32 v146, v146, v147
	v_mov_b32_e32 v151, v75

;     __device__ __forceinline__ void operator()(const f32x4 (&acc)[2][2][4][2], const Unit& u, int wr, int wc, int fr, int fq) const {
;     ...
;             BC_LOAD(0, 0);
; #pragma unroll
;             for (int g = 0; g < 16; ++g) {
;                 const int ai = g >> 3, m = (g >> 1) & 3, bj = g & 1;
;                 const int r = row0 + ai * HALF + m * 16;
;                 if (g + 1 < 16) BC_LOAD((g + 1) & 1, g + 1);
;                 {
;                     {
;                         const int col = cb + bj * HALF + lc;
;                         const size_t hoff = ((size_t)((r >> 11) * 4 + (col >> 7)) * SEQ + (r & (SEQ - 1))) * 128 + (col & 127);
;                         const f32x4 b0 = bc[g & 1][0], b1 = bc[g & 1][1];
;                         const f32x4 v0 = acc[ai][bj][m][0], v1 = acc[ai][bj][m][1];
;                         const float L2E = 1.4426950408889634f;
;                         if (isq) {
;                             const float s = 0.08838834764831845f;
;                             u32x4 o; o[0] = cvt_pk_bf16(v0[0] * s * __builtin_amdgcn_exp2f(b0[0] * L2E), v0[1] * s * __builtin_amdgcn_exp2f(b0[1] * L2E));
;                             o[1] = cvt_pk_bf16(v0[2] * s * __builtin_amdgcn_exp2f(b0[2] * L2E), v0[3] * s * __builtin_amdgcn_exp2f(b0[3] * L2E));
;                             o[2] = cvt_pk_bf16(v1[0] * s * __builtin_amdgcn_exp2f(b1[0] * L2E), v1[1] * s * __builtin_amdgcn_exp2f(b1[1] * L2E));
;                             o[3] = cvt_pk_bf16(v1[2] * s * __builtin_amdgcn_exp2f(b1[2] * L2E), v1[3] * s * __builtin_amdgcn_exp2f(b1[3] * L2E));
;                             __builtin_nontemporal_store(o, (u32x4*)(d0 + hoff));
;                         } else {
;                             u32x4 o;
;                             o[0] = cvt_pk_bf16(v0[0] * __builtin_amdgcn_exp2f(-b0[0] * L2E), v0[1] * __builtin_amdgcn_exp2f(-b0[1] * L2E));
;                             o[1] = cvt_pk_bf16(v0[2] * __builtin_amdgcn_exp2f(-b0[2] * L2E), v0[3] * __builtin_amdgcn_exp2f(-b0[3] * L2E));
;                             o[2] = cvt_pk_bf16(v1[0] * __builtin_amdgcn_exp2f(-b1[0] * L2E), v1[1] * __builtin_amdgcn_exp2f(-b1[1] * L2E));
;                             o[3] = cvt_pk_bf16(v1[2] * __builtin_amdgcn_exp2f(-b1[2] * L2E), v1[3] * __builtin_amdgcn_exp2f(-b1[3] * L2E));
;                             __builtin_nontemporal_store(o, (u32x4*)(d0 + hoff));
.LBB0_1442:
	s_waitcnt vmcnt(3)
	v_mul_f32_e32 v132, s33, v135
	v_exp_f32_e32 v132, v132
	v_or_b32_e32 v133, 0x1800, v156
	v_mov_b32_e32 v153, v169
	v_lshlrev_b32_e32 v152, 1, v133
	v_mul_f32_e32 v132, v151, v132
	v_cvt_pk_bf16_f32 v147, v150, v132
	v_lshl_add_u64 v[132:133], s[10:11], 0, v[152:153]
	v_mov_b32_e32 v149, v169
	v_add_u32_e32 v150, 0x80, v192
	v_lshl_add_u64 v[132:133], v[132:133], 0, v[148:149]
	v_ashrrev_i32_e32 v151, 31, v150
	global_store_dwordx4 v[132:133], v[144:147], off
	v_lshlrev_b64 v[132:133], 11, v[150:151]
	v_lshl_add_u64 v[132:133], s[22:23], 0, v[132:133]
	v_lshl_add_u64 v[154:155], v[168:169], 2, v[132:133]
	global_load_dwordx4 v[132:135], v[154:155], off offset:16
	global_load_dwordx4 v[140:143], v[154:155], off
	s_waitcnt vmcnt(3)
	s_and_b64 vcc, exec, s[8:9]
	s_mov_b64 s[10:11], -1
	s_cbranch_vccnz .LBB0_1444
	v_mul_f32_e32 v144, 0xbfb8aa3b, v136
	v_mul_f32_e32 v145, 0xbfb8aa3b, v137
	v_exp_f32_e32 v144, v144
	v_exp_f32_e32 v145, v145
	v_mul_f32_e32 v146, 0xbfb8aa3b, v138
	v_mul_f32_e32 v147, 0xbfb8aa3b, v139
	v_exp_f32_e32 v146, v146
	v_pk_mul_f32 v[144:145], v[68:69], v[144:145]
	v_exp_f32_e32 v147, v147
	v_cvt_pk_bf16_f32 v144, v144, v145
	v_mul_f32_e32 v145, 0xbfb8aa3b, v128
	v_exp_f32_e32 v156, v145
	v_mul_f32_e32 v145, 0xbfb8aa3b, v129
	v_exp_f32_e32 v157, v145
	v_mul_f32_e32 v145, 0xbfb8aa3b, v130
	v_exp_f32_e32 v149, v145
	v_pk_mul_f32 v[146:147], v[70:71], v[146:147]
	s_mov_b64 s[10:11], 0
	v_cvt_pk_bf16_f32 v145, v146, v147
	v_pk_mul_f32 v[146:147], v[64:65], v[156:157]
	v_mul_f32_e32 v156, v66, v149
	v_cvt_pk_bf16_f32 v146, v146, v147
	v_mov_b32_e32 v157, v67

;     __device__ __forceinline__ void operator()(const f32x4 (&acc)[2][2][4][2], const Unit& u, int wr, int wc, int fr, int fq) const {
;     ...
;             BC_LOAD(0, 0);
; #pragma unroll
;             for (int g = 0; g < 16; ++g) {
;                 const int ai = g >> 3, m = (g >> 1) & 3, bj = g & 1;
;                 const int r = row0 + ai * HALF + m * 16;
;                 if (g + 1 < 16) BC_LOAD((g + 1) & 1, g + 1);
;                 {
;                     {
;                         const int col = cb + bj * HALF + lc;
;                         const size_t hoff = ((size_t)((r >> 11) * 4 + (col >> 7)) * SEQ + (r & (SEQ - 1))) * 128 + (col & 127);
;                         const f32x4 b0 = bc[g & 1][0], b1 = bc[g & 1][1];
;                         const f32x4 v0 = acc[ai][bj][m][0], v1 = acc[ai][bj][m][1];
;                         const float L2E = 1.4426950408889634f;
;                         if (isq) {
;                             const float s = 0.08838834764831845f;
;                             u32x4 o; o[0] = cvt_pk_bf16(v0[0] * s * __builtin_amdgcn_exp2f(b0[0] * L2E), v0[1] * s * __builtin_amdgcn_exp2f(b0[1] * L2E));
;                             o[1] = cvt_pk_bf16(v0[2] * s * __builtin_amdgcn_exp2f(b0[2] * L2E), v0[3] * s * __builtin_amdgcn_exp2f(b0[3] * L2E));
;                             o[2] = cvt_pk_bf16(v1[0] * s * __builtin_amdgcn_exp2f(b1[0] * L2E), v1[1] * s * __builtin_amdgcn_exp2f(b1[1] * L2E));
;                             o[3] = cvt_pk_bf16(v1[2] * s * __builtin_amdgcn_exp2f(b1[2] * L2E), v1[3] * s * __builtin_amdgcn_exp2f(b1[3] * L2E));
;                             __builtin_nontemporal_store(o, (u32x4*)(d0 + hoff));
;                         } else {
;                             u32x4 o;
;                             o[0] = cvt_pk_bf16(v0[0] * __builtin_amdgcn_exp2f(-b0[0] * L2E), v0[1] * __builtin_amdgcn_exp2f(-b0[1] * L2E));
;                             o[1] = cvt_pk_bf16(v0[2] * __builtin_amdgcn_exp2f(-b0[2] * L2E), v0[3] * __builtin_amdgcn_exp2f(-b0[3] * L2E));
;                             o[2] = cvt_pk_bf16(v1[0] * __builtin_amdgcn_exp2f(-b1[0] * L2E), v1[1] * __builtin_amdgcn_exp2f(-b1[1] * L2E));
;                             o[3] = cvt_pk_bf16(v1[2] * __builtin_amdgcn_exp2f(-b1[2] * L2E), v1[3] * __builtin_amdgcn_exp2f(-b1[3] * L2E));
;                             __builtin_nontemporal_store(o, (u32x4*)(d0 + hoff));
.LBB0_1446:
	v_mul_f32_e32 v128, s10, v131
	v_exp_f32_e32 v130, v128
	v_mov_b32_e32 v153, v169
	v_mov_b32_e32 v149, v169
	v_lshl_add_u64 v[128:129], s[42:43], 0, v[152:153]
	v_mul_f32_e32 v130, v157, v130
	v_cvt_pk_bf16_f32 v147, v156, v130
	v_lshl_add_u64 v[128:129], v[128:129], 0, v[148:149]
	global_store_dwordx4 v[128:129], v[144:147], off
	global_load_dwordx4 v[128:131], v[154:155], off offset:528
	s_nop 0
	global_load_dwordx4 v[136:139], v[154:155], off offset:512
	s_and_b64 vcc, exec, s[8:9]
	s_mov_b64 s[10:11], -1
	s_cbranch_vccnz .LBB0_1448
	s_waitcnt vmcnt(3)
	v_mul_f32_e32 v144, 0xbfb8aa3b, v140
	v_mul_f32_e32 v145, 0xbfb8aa3b, v141
	v_exp_f32_e32 v144, v144
	v_exp_f32_e32 v145, v145
	v_mul_f32_e32 v146, 0xbfb8aa3b, v142
	v_mul_f32_e32 v147, 0xbfb8aa3b, v143
	v_exp_f32_e32 v146, v146
	v_pk_mul_f32 v[144:145], v[60:61], v[144:145]
	v_exp_f32_e32 v147, v147
	v_cvt_pk_bf16_f32 v144, v144, v145
	v_mul_f32_e32 v145, 0xbfb8aa3b, v132
	v_exp_f32_e32 v152, v145
	v_mul_f32_e32 v145, 0xbfb8aa3b, v133
	v_exp_f32_e32 v153, v145
	v_mul_f32_e32 v145, 0xbfb8aa3b, v134
	v_exp_f32_e32 v149, v145
	v_pk_mul_f32 v[146:147], v[62:63], v[146:147]
	s_mov_b64 s[10:11], 0
	v_cvt_pk_bf16_f32 v145, v146, v147
	v_pk_mul_f32 v[146:147], v[56:57], v[152:153]
	v_mul_f32_e32 v152, v58, v149
	v_cvt_pk_bf16_f32 v146, v146, v147
	v_mov_b32_e32 v153, v59

;     __device__ __forceinline__ void operator()(const f32x4 (&acc)[2][2][4][2], const Unit& u, int wr, int wc, int fr, int fq) const {
;     ...
;             BC_LOAD(0, 0);
; #pragma unroll
;             for (int g = 0; g < 16; ++g) {
;                 const int ai = g >> 3, m = (g >> 1) & 3, bj = g & 1;
;                 const int r = row0 + ai * HALF + m * 16;
;                 if (g + 1 < 16) BC_LOAD((g + 1) & 1, g + 1);
;                 {
;                     {
;                         const int col = cb + bj * HALF + lc;
;                         const size_t hoff = ((size_t)((r >> 11) * 4 + (col >> 7)) * SEQ + (r & (SEQ - 1))) * 128 + (col & 127);
;                         const f32x4 b0 = bc[g & 1][0], b1 = bc[g & 1][1];
;                         const f32x4 v0 = acc[ai][bj][m][0], v1 = acc[ai][bj][m][1];
;                         const float L2E = 1.4426950408889634f;
;                         if (isq) {
;                             const float s = 0.08838834764831845f;
;                             u32x4 o; o[0] = cvt_pk_bf16(v0[0] * s * __builtin_amdgcn_exp2f(b0[0] * L2E), v0[1] * s * __builtin_amdgcn_exp2f(b0[1] * L2E));
;                             o[1] = cvt_pk_bf16(v0[2] * s * __builtin_amdgcn_exp2f(b0[2] * L2E), v0[3] * s * __builtin_amdgcn_exp2f(b0[3] * L2E));
;                             o[2] = cvt_pk_bf16(v1[0] * s * __builtin_amdgcn_exp2f(b1[0] * L2E), v1[1] * s * __builtin_amdgcn_exp2f(b1[1] * L2E));
;                             o[3] = cvt_pk_bf16(v1[2] * s * __builtin_amdgcn_exp2f(b1[2] * L2E), v1[3] * s * __builtin_amdgcn_exp2f(b1[3] * L2E));
;                             __builtin_nontemporal_store(o, (u32x4*)(d0 + hoff));
;                         } else {
;                             u32x4 o;
;                             o[0] = cvt_pk_bf16(v0[0] * __builtin_amdgcn_exp2f(-b0[0] * L2E), v0[1] * __builtin_amdgcn_exp2f(-b0[1] * L2E));
;                             o[1] = cvt_pk_bf16(v0[2] * __builtin_amdgcn_exp2f(-b0[2] * L2E), v0[3] * __builtin_amdgcn_exp2f(-b0[3] * L2E));
;                             o[2] = cvt_pk_bf16(v1[0] * __builtin_amdgcn_exp2f(-b1[0] * L2E), v1[1] * __builtin_amdgcn_exp2f(-b1[1] * L2E));
;                             o[3] = cvt_pk_bf16(v1[2] * __builtin_amdgcn_exp2f(-b1[2] * L2E), v1[3] * __builtin_amdgcn_exp2f(-b1[3] * L2E));
;                             __builtin_nontemporal_store(o, (u32x4*)(d0 + hoff));
.LBB0_1450:
	s_waitcnt vmcnt(3)
	v_mul_f32_e32 v133, s10, v135
	v_ashrrev_i32_e32 v132, 9, v150
	v_exp_f32_e32 v134, v133
	v_and_b32_e32 v151, -4, v132
	v_add_u32_e32 v132, s17, v151
	v_ashrrev_i32_e32 v133, 31, v132
	v_lshlrev_b32_e32 v135, 7, v150
	v_and_b32_e32 v193, 0x3e780, v135
	v_mul_f32_e32 v134, v153, v134
	v_lshlrev_b64 v[132:133], 19, v[132:133]
	v_cvt_pk_bf16_f32 v147, v152, v134
	v_lshl_add_u64 v[152:153], s[2:3], 0, v[132:133]
	v_lshlrev_b32_e32 v156, 1, v193
	v_mov_b32_e32 v157, v169
	v_lshl_add_u64 v[132:133], v[152:153], 0, v[156:157]
	v_mov_b32_e32 v149, v169
	v_lshl_add_u64 v[132:133], v[132:133], 0, v[148:149]
	global_store_dwordx4 v[132:133], v[144:147], off
	v_or_b32_e32 v132, 16, v150
	v_ashrrev_i32_e32 v133, 31, v132
	v_lshlrev_b64 v[132:133], 11, v[132:133]
	v_lshl_add_u64 v[132:133], s[22:23], 0, v[132:133]
	v_lshl_add_u64 v[158:159], v[168:169], 2, v[132:133]
	global_load_dwordx4 v[132:135], v[158:159], off offset:16
	global_load_dwordx4 v[140:143], v[158:159], off
	s_waitcnt vmcnt(3)
	s_and_b64 vcc, exec, s[8:9]
	s_mov_b64 s[10:11], -1
	s_cbranch_vccnz .LBB0_1452
	v_mul_f32_e32 v144, 0xbfb8aa3b, v136
	v_mul_f32_e32 v145, 0xbfb8aa3b, v137
	v_exp_f32_e32 v144, v144
	v_exp_f32_e32 v145, v145
	v_mul_f32_e32 v146, 0xbfb8aa3b, v138
	v_mul_f32_e32 v147, 0xbfb8aa3b, v139
	v_exp_f32_e32 v146, v146
	v_pk_mul_f32 v[144:145], v[52:53], v[144:145]
	v_exp_f32_e32 v147, v147
	v_cvt_pk_bf16_f32 v144, v144, v145
	v_mul_f32_e32 v145, 0xbfb8aa3b, v128
	v_exp_f32_e32 v154, v145
	v_mul_f32_e32 v145, 0xbfb8aa3b, v129
	v_exp_f32_e32 v155, v145
	v_mul_f32_e32 v145, 0xbfb8aa3b, v130
	v_exp_f32_e32 v149, v145
	v_pk_mul_f32 v[146:147], v[54:55], v[146:147]
	s_mov_b64 s[10:11], 0
	v_cvt_pk_bf16_f32 v145, v146, v147
	v_pk_mul_f32 v[146:147], v[48:49], v[154:155]
	v_mul_f32_e32 v154, v50, v149
	v_cvt_pk_bf16_f32 v146, v146, v147
	v_mov_b32_e32 v155, v51

;     __device__ __forceinline__ void operator()(const f32x4 (&acc)[2][2][4][2], const Unit& u, int wr, int wc, int fr, int fq) const {
;     ...
;             BC_LOAD(0, 0);
; #pragma unroll
;             for (int g = 0; g < 16; ++g) {
;                 const int ai = g >> 3, m = (g >> 1) & 3, bj = g & 1;
;                 const int r = row0 + ai * HALF + m * 16;
;                 if (g + 1 < 16) BC_LOAD((g + 1) & 1, g + 1);
;                 {
;                     {
;                         const int col = cb + bj * HALF + lc;
;                         const size_t hoff = ((size_t)((r >> 11) * 4 + (col >> 7)) * SEQ + (r & (SEQ - 1))) * 128 + (col & 127);
;                         const f32x4 b0 = bc[g & 1][0], b1 = bc[g & 1][1];
;                         const f32x4 v0 = acc[ai][bj][m][0], v1 = acc[ai][bj][m][1];
;                         const float L2E = 1.4426950408889634f;
;                         if (isq) {
;                             const float s = 0.08838834764831845f;
;                             u32x4 o; o[0] = cvt_pk_bf16(v0[0] * s * __builtin_amdgcn_exp2f(b0[0] * L2E), v0[1] * s * __builtin_amdgcn_exp2f(b0[1] * L2E));
;                             o[1] = cvt_pk_bf16(v0[2] * s * __builtin_amdgcn_exp2f(b0[2] * L2E), v0[3] * s * __builtin_amdgcn_exp2f(b0[3] * L2E));
;                             o[2] = cvt_pk_bf16(v1[0] * s * __builtin_amdgcn_exp2f(b1[0] * L2E), v1[1] * s * __builtin_amdgcn_exp2f(b1[1] * L2E));
;                             o[3] = cvt_pk_bf16(v1[2] * s * __builtin_amdgcn_exp2f(b1[2] * L2E), v1[3] * s * __builtin_amdgcn_exp2f(b1[3] * L2E));
;                             __builtin_nontemporal_store(o, (u32x4*)(d0 + hoff));
;                         } else {
;                             u32x4 o;
;                             o[0] = cvt_pk_bf16(v0[0] * __builtin_amdgcn_exp2f(-b0[0] * L2E), v0[1] * __builtin_amdgcn_exp2f(-b0[1] * L2E));
;                             o[1] = cvt_pk_bf16(v0[2] * __builtin_amdgcn_exp2f(-b0[2] * L2E), v0[3] * __builtin_amdgcn_exp2f(-b0[3] * L2E));
;                             o[2] = cvt_pk_bf16(v1[0] * __builtin_amdgcn_exp2f(-b1[0] * L2E), v1[1] * __builtin_amdgcn_exp2f(-b1[1] * L2E));
;                             o[3] = cvt_pk_bf16(v1[2] * __builtin_amdgcn_exp2f(-b1[2] * L2E), v1[3] * __builtin_amdgcn_exp2f(-b1[3] * L2E));
;                             __builtin_nontemporal_store(o, (u32x4*)(d0 + hoff));
.LBB0_1454:
	v_mul_f32_e32 v128, s10, v131
	v_exp_f32_e32 v130, v128
	v_add_u32_e32 v128, s18, v151
	v_ashrrev_i32_e32 v129, 31, v128
	v_lshlrev_b64 v[128:129], 19, v[128:129]
	v_mul_f32_e32 v130, v155, v130
	v_cvt_pk_bf16_f32 v147, v154, v130
	v_lshl_add_u64 v[154:155], s[2:3], 0, v[128:129]
	v_mov_b32_e32 v157, v169
	v_lshl_add_u64 v[128:129], v[154:155], 0, v[156:157]
	v_mov_b32_e32 v149, v169
	v_lshl_add_u64 v[128:129], v[128:129], 0, v[148:149]
	global_store_dwordx4 v[128:129], v[144:147], off
	global_load_dwordx4 v[128:131], v[158:159], off offset:528
	s_nop 0
	global_load_dwordx4 v[136:139], v[158:159], off offset:512
	s_and_b64 vcc, exec, s[8:9]
	s_mov_b64 s[2:3], -1
	s_cbranch_vccnz .LBB0_1456
	s_waitcnt vmcnt(3)
	v_mul_f32_e32 v144, 0xbfb8aa3b, v140
	v_mul_f32_e32 v145, 0xbfb8aa3b, v141
	v_exp_f32_e32 v144, v144
	v_exp_f32_e32 v145, v145
	v_mul_f32_e32 v146, 0xbfb8aa3b, v142
	v_mul_f32_e32 v147, 0xbfb8aa3b, v143
	v_exp_f32_e32 v146, v146
	v_pk_mul_f32 v[144:145], v[44:45], v[144:145]
	v_exp_f32_e32 v147, v147
	v_cvt_pk_bf16_f32 v144, v144, v145
	v_mul_f32_e32 v145, 0xbfb8aa3b, v132
	v_exp_f32_e32 v156, v145
	v_mul_f32_e32 v145, 0xbfb8aa3b, v133
	v_exp_f32_e32 v157, v145
	v_mul_f32_e32 v145, 0xbfb8aa3b, v134
	v_exp_f32_e32 v149, v145
	v_pk_mul_f32 v[146:147], v[46:47], v[146:147]
	s_mov_b64 s[2:3], 0
	v_cvt_pk_bf16_f32 v145, v146, v147
	v_pk_mul_f32 v[146:147], v[40:41], v[156:157]
	v_mul_f32_e32 v158, v42, v149
	v_cvt_pk_bf16_f32 v146, v146, v147
	v_mov_b32_e32 v159, v43

;     __device__ __forceinline__ void operator()(const f32x4 (&acc)[2][2][4][2], const Unit& u, int wr, int wc, int fr, int fq) const {
;     ...
;             BC_LOAD(0, 0);
; #pragma unroll
;             for (int g = 0; g < 16; ++g) {
;                 const int ai = g >> 3, m = (g >> 1) & 3, bj = g & 1;
;                 const int r = row0 + ai * HALF + m * 16;
;                 if (g + 1 < 16) BC_LOAD((g + 1) & 1, g + 1);
;                 {
;                     {
;                         const int col = cb + bj * HALF + lc;
;                         const size_t hoff = ((size_t)((r >> 11) * 4 + (col >> 7)) * SEQ + (r & (SEQ - 1))) * 128 + (col & 127);
;                         const f32x4 b0 = bc[g & 1][0], b1 = bc[g & 1][1];
;                         const f32x4 v0 = acc[ai][bj][m][0], v1 = acc[ai][bj][m][1];
;                         const float L2E = 1.4426950408889634f;
;                         if (isq) {
;                             const float s = 0.08838834764831845f;
;                             u32x4 o; o[0] = cvt_pk_bf16(v0[0] * s * __builtin_amdgcn_exp2f(b0[0] * L2E), v0[1] * s * __builtin_amdgcn_exp2f(b0[1] * L2E));
;                             o[1] = cvt_pk_bf16(v0[2] * s * __builtin_amdgcn_exp2f(b0[2] * L2E), v0[3] * s * __builtin_amdgcn_exp2f(b0[3] * L2E));
;                             o[2] = cvt_pk_bf16(v1[0] * s * __builtin_amdgcn_exp2f(b1[0] * L2E), v1[1] * s * __builtin_amdgcn_exp2f(b1[1] * L2E));
;                             o[3] = cvt_pk_bf16(v1[2] * s * __builtin_amdgcn_exp2f(b1[2] * L2E), v1[3] * s * __builtin_amdgcn_exp2f(b1[3] * L2E));
;                             __builtin_nontemporal_store(o, (u32x4*)(d0 + hoff));
;                         } else {
;                             u32x4 o;
;                             o[0] = cvt_pk_bf16(v0[0] * __builtin_amdgcn_exp2f(-b0[0] * L2E), v0[1] * __builtin_amdgcn_exp2f(-b0[1] * L2E));
;                             o[1] = cvt_pk_bf16(v0[2] * __builtin_amdgcn_exp2f(-b0[2] * L2E), v0[3] * __builtin_amdgcn_exp2f(-b0[3] * L2E));
;                             o[2] = cvt_pk_bf16(v1[0] * __builtin_amdgcn_exp2f(-b1[0] * L2E), v1[1] * __builtin_amdgcn_exp2f(-b1[1] * L2E));
;                             o[3] = cvt_pk_bf16(v1[2] * __builtin_amdgcn_exp2f(-b1[2] * L2E), v1[3] * __builtin_amdgcn_exp2f(-b1[3] * L2E));
;                             __builtin_nontemporal_store(o, (u32x4*)(d0 + hoff));
.LBB0_1458:
	s_waitcnt vmcnt(3)
	v_mul_f32_e32 v132, s2, v135
	v_exp_f32_e32 v132, v132
	v_or_b32_e32 v133, 0x800, v193
	v_mov_b32_e32 v157, v169
	v_lshlrev_b32_e32 v156, 1, v133
	v_mul_f32_e32 v132, v159, v132
	v_cvt_pk_bf16_f32 v147, v158, v132
	v_lshl_add_u64 v[132:133], v[152:153], 0, v[156:157]
	v_mov_b32_e32 v149, v169
	v_lshl_add_u64 v[132:133], v[132:133], 0, v[148:149]
	global_store_dwordx4 v[132:133], v[144:147], off
	v_or_b32_e32 v132, 32, v150
	v_ashrrev_i32_e32 v133, 31, v132
	v_lshlrev_b64 v[132:133], 11, v[132:133]
	v_lshl_add_u64 v[132:133], s[22:23], 0, v[132:133]
	v_lshl_add_u64 v[158:159], v[168:169], 2, v[132:133]
	global_load_dwordx4 v[132:135], v[158:159], off offset:16
	global_load_dwordx4 v[140:143], v[158:159], off
	s_waitcnt vmcnt(3)
	s_and_b64 vcc, exec, s[8:9]
	s_mov_b64 s[2:3], -1
	s_cbranch_vccnz .LBB0_1460
	v_mul_f32_e32 v144, 0xbfb8aa3b, v136
	v_mul_f32_e32 v145, 0xbfb8aa3b, v137
	v_exp_f32_e32 v144, v144
	v_exp_f32_e32 v145, v145
	v_mul_f32_e32 v146, 0xbfb8aa3b, v138
	v_mul_f32_e32 v147, 0xbfb8aa3b, v139
	v_exp_f32_e32 v146, v146
	v_pk_mul_f32 v[144:145], v[36:37], v[144:145]
	v_exp_f32_e32 v147, v147
	v_cvt_pk_bf16_f32 v144, v144, v145
	v_mul_f32_e32 v145, 0xbfb8aa3b, v128
	v_exp_f32_e32 v194, v145
	v_mul_f32_e32 v145, 0xbfb8aa3b, v129
	v_exp_f32_e32 v195, v145
	v_mul_f32_e32 v145, 0xbfb8aa3b, v130
	v_exp_f32_e32 v149, v145
	v_pk_mul_f32 v[146:147], v[38:39], v[146:147]
	s_mov_b64 s[2:3], 0
	v_cvt_pk_bf16_f32 v145, v146, v147
	v_pk_mul_f32 v[146:147], v[32:33], v[194:195]
	v_mul_f32_e32 v194, v34, v149
	v_cvt_pk_bf16_f32 v146, v146, v147
	v_mov_b32_e32 v195, v35

;     __device__ __forceinline__ void operator()(const f32x4 (&acc)[2][2][4][2], const Unit& u, int wr, int wc, int fr, int fq) const {
;     ...
;             BC_LOAD(0, 0);
; #pragma unroll
;             for (int g = 0; g < 16; ++g) {
;                 const int ai = g >> 3, m = (g >> 1) & 3, bj = g & 1;
;                 const int r = row0 + ai * HALF + m * 16;
;                 if (g + 1 < 16) BC_LOAD((g + 1) & 1, g + 1);
;                 {
;                     {
;                         const int col = cb + bj * HALF + lc;
;                         const size_t hoff = ((size_t)((r >> 11) * 4 + (col >> 7)) * SEQ + (r & (SEQ - 1))) * 128 + (col & 127);
;                         const f32x4 b0 = bc[g & 1][0], b1 = bc[g & 1][1];
;                         const f32x4 v0 = acc[ai][bj][m][0], v1 = acc[ai][bj][m][1];
;                         const float L2E = 1.4426950408889634f;
;                         if (isq) {
;                             const float s = 0.08838834764831845f;
;                             u32x4 o; o[0] = cvt_pk_bf16(v0[0] * s * __builtin_amdgcn_exp2f(b0[0] * L2E), v0[1] * s * __builtin_amdgcn_exp2f(b0[1] * L2E));
;                             o[1] = cvt_pk_bf16(v0[2] * s * __builtin_amdgcn_exp2f(b0[2] * L2E), v0[3] * s * __builtin_amdgcn_exp2f(b0[3] * L2E));
;                             o[2] = cvt_pk_bf16(v1[0] * s * __builtin_amdgcn_exp2f(b1[0] * L2E), v1[1] * s * __builtin_amdgcn_exp2f(b1[1] * L2E));
;                             o[3] = cvt_pk_bf16(v1[2] * s * __builtin_amdgcn_exp2f(b1[2] * L2E), v1[3] * s * __builtin_amdgcn_exp2f(b1[3] * L2E));
;                             __builtin_nontemporal_store(o, (u32x4*)(d0 + hoff));
;                         } else {
;                             u32x4 o;
;                             o[0] = cvt_pk_bf16(v0[0] * __builtin_amdgcn_exp2f(-b0[0] * L2E), v0[1] * __builtin_amdgcn_exp2f(-b0[1] * L2E));
;                             o[1] = cvt_pk_bf16(v0[2] * __builtin_amdgcn_exp2f(-b0[2] * L2E), v0[3] * __builtin_amdgcn_exp2f(-b0[3] * L2E));
;                             o[2] = cvt_pk_bf16(v1[0] * __builtin_amdgcn_exp2f(-b1[0] * L2E), v1[1] * __builtin_amdgcn_exp2f(-b1[1] * L2E));
;                             o[3] = cvt_pk_bf16(v1[2] * __builtin_amdgcn_exp2f(-b1[2] * L2E), v1[3] * __builtin_amdgcn_exp2f(-b1[3] * L2E));
;                             __builtin_nontemporal_store(o, (u32x4*)(d0 + hoff));
.LBB0_1462:
	v_mul_f32_e32 v128, s2, v131
	v_exp_f32_e32 v130, v128
	v_mov_b32_e32 v157, v169
	v_mov_b32_e32 v149, v169
	v_lshl_add_u64 v[128:129], v[154:155], 0, v[156:157]
	v_mul_f32_e32 v130, v195, v130
	v_cvt_pk_bf16_f32 v147, v194, v130
	v_lshl_add_u64 v[128:129], v[128:129], 0, v[148:149]
	global_store_dwordx4 v[128:129], v[144:147], off
	global_load_dwordx4 v[128:131], v[158:159], off offset:528
	s_nop 0
	global_load_dwordx4 v[136:139], v[158:159], off offset:512
	s_and_b64 vcc, exec, s[8:9]
	s_mov_b64 s[2:3], -1
	s_cbranch_vccnz .LBB0_1464
	s_waitcnt vmcnt(3)
	v_mul_f32_e32 v144, 0xbfb8aa3b, v140
	v_mul_f32_e32 v145, 0xbfb8aa3b, v141
	v_exp_f32_e32 v144, v144
	v_exp_f32_e32 v145, v145
	v_mul_f32_e32 v146, 0xbfb8aa3b, v142
	v_mul_f32_e32 v147, 0xbfb8aa3b, v143
	v_exp_f32_e32 v146, v146
	v_pk_mul_f32 v[144:145], v[28:29], v[144:145]
	v_exp_f32_e32 v147, v147
	v_cvt_pk_bf16_f32 v144, v144, v145
	v_mul_f32_e32 v145, 0xbfb8aa3b, v132
	v_exp_f32_e32 v156, v145
	v_mul_f32_e32 v145, 0xbfb8aa3b, v133
	v_exp_f32_e32 v157, v145
	v_mul_f32_e32 v145, 0xbfb8aa3b, v134
	v_exp_f32_e32 v149, v145
	v_pk_mul_f32 v[146:147], v[30:31], v[146:147]
	s_mov_b64 s[2:3], 0
	v_cvt_pk_bf16_f32 v145, v146, v147
	v_pk_mul_f32 v[146:147], v[24:25], v[156:157]
	v_mul_f32_e32 v158, v26, v149
	v_cvt_pk_bf16_f32 v146, v146, v147
	v_mov_b32_e32 v159, v27

;     __device__ __forceinline__ void operator()(const f32x4 (&acc)[2][2][4][2], const Unit& u, int wr, int wc, int fr, int fq) const {
;     ...
;             BC_LOAD(0, 0);
; #pragma unroll
;             for (int g = 0; g < 16; ++g) {
;                 const int ai = g >> 3, m = (g >> 1) & 3, bj = g & 1;
;                 const int r = row0 + ai * HALF + m * 16;
;                 if (g + 1 < 16) BC_LOAD((g + 1) & 1, g + 1);
;                 {
;                     {
;                         const int col = cb + bj * HALF + lc;
;                         const size_t hoff = ((size_t)((r >> 11) * 4 + (col >> 7)) * SEQ + (r & (SEQ - 1))) * 128 + (col & 127);
;                         const f32x4 b0 = bc[g & 1][0], b1 = bc[g & 1][1];
;                         const f32x4 v0 = acc[ai][bj][m][0], v1 = acc[ai][bj][m][1];
;                         const float L2E = 1.4426950408889634f;
;                         if (isq) {
;                             const float s = 0.08838834764831845f;
;                             u32x4 o; o[0] = cvt_pk_bf16(v0[0] * s * __builtin_amdgcn_exp2f(b0[0] * L2E), v0[1] * s * __builtin_amdgcn_exp2f(b0[1] * L2E));
;                             o[1] = cvt_pk_bf16(v0[2] * s * __builtin_amdgcn_exp2f(b0[2] * L2E), v0[3] * s * __builtin_amdgcn_exp2f(b0[3] * L2E));
;                             o[2] = cvt_pk_bf16(v1[0] * s * __builtin_amdgcn_exp2f(b1[0] * L2E), v1[1] * s * __builtin_amdgcn_exp2f(b1[1] * L2E));
;                             o[3] = cvt_pk_bf16(v1[2] * s * __builtin_amdgcn_exp2f(b1[2] * L2E), v1[3] * s * __builtin_amdgcn_exp2f(b1[3] * L2E));
;                             __builtin_nontemporal_store(o, (u32x4*)(d0 + hoff));
;                         } else {
;                             u32x4 o;
;                             o[0] = cvt_pk_bf16(v0[0] * __builtin_amdgcn_exp2f(-b0[0] * L2E), v0[1] * __builtin_amdgcn_exp2f(-b0[1] * L2E));
;                             o[1] = cvt_pk_bf16(v0[2] * __builtin_amdgcn_exp2f(-b0[2] * L2E), v0[3] * __builtin_amdgcn_exp2f(-b0[3] * L2E));
;                             o[2] = cvt_pk_bf16(v1[0] * __builtin_amdgcn_exp2f(-b1[0] * L2E), v1[1] * __builtin_amdgcn_exp2f(-b1[1] * L2E));
;                             o[3] = cvt_pk_bf16(v1[2] * __builtin_amdgcn_exp2f(-b1[2] * L2E), v1[3] * __builtin_amdgcn_exp2f(-b1[3] * L2E));
;                             __builtin_nontemporal_store(o, (u32x4*)(d0 + hoff));
.LBB0_1466:
	s_waitcnt vmcnt(3)
	v_mul_f32_e32 v132, s2, v135
	v_exp_f32_e32 v132, v132
	v_or_b32_e32 v133, 0x1000, v193
	v_mov_b32_e32 v157, v169
	v_lshlrev_b32_e32 v156, 1, v133
	v_mul_f32_e32 v132, v159, v132
	v_cvt_pk_bf16_f32 v147, v158, v132
	v_lshl_add_u64 v[132:133], v[152:153], 0, v[156:157]
	v_mov_b32_e32 v149, v169
	v_lshl_add_u64 v[132:133], v[132:133], 0, v[148:149]
	global_store_dwordx4 v[132:133], v[144:147], off
	v_or_b32_e32 v132, 48, v150
	v_ashrrev_i32_e32 v133, 31, v132
	v_lshlrev_b64 v[132:133], 11, v[132:133]
	v_lshl_add_u64 v[132:133], s[22:23], 0, v[132:133]
	v_lshl_add_u64 v[150:151], v[168:169], 2, v[132:133]
	global_load_dwordx4 v[132:135], v[150:151], off offset:16
	global_load_dwordx4 v[140:143], v[150:151], off
	s_waitcnt vmcnt(3)
	s_and_b64 vcc, exec, s[8:9]
	s_mov_b64 s[2:3], -1
	s_cbranch_vccnz .LBB0_1468
	v_mul_f32_e32 v144, 0xbfb8aa3b, v136
	v_mul_f32_e32 v145, 0xbfb8aa3b, v137
	v_exp_f32_e32 v144, v144
	v_exp_f32_e32 v145, v145
	v_mul_f32_e32 v146, 0xbfb8aa3b, v138
	v_mul_f32_e32 v147, 0xbfb8aa3b, v139
	v_exp_f32_e32 v146, v146
	v_pk_mul_f32 v[144:145], v[20:21], v[144:145]
	v_exp_f32_e32 v147, v147
	v_cvt_pk_bf16_f32 v144, v144, v145
	v_mul_f32_e32 v145, 0xbfb8aa3b, v128
	v_exp_f32_e32 v158, v145
	v_mul_f32_e32 v145, 0xbfb8aa3b, v129
	v_exp_f32_e32 v159, v145
	v_mul_f32_e32 v145, 0xbfb8aa3b, v130
	v_exp_f32_e32 v149, v145
	v_pk_mul_f32 v[146:147], v[22:23], v[146:147]
	s_mov_b64 s[2:3], 0
	v_cvt_pk_bf16_f32 v145, v146, v147
	v_pk_mul_f32 v[146:147], v[16:17], v[158:159]
	v_mul_f32_e32 v158, v18, v149
	v_cvt_pk_bf16_f32 v146, v146, v147
	v_mov_b32_e32 v159, v19

;     __device__ __forceinline__ void operator()(const f32x4 (&acc)[2][2][4][2], const Unit& u, int wr, int wc, int fr, int fq) const {
;     ...
;             BC_LOAD(0, 0);
; #pragma unroll
;             for (int g = 0; g < 16; ++g) {
;                 const int ai = g >> 3, m = (g >> 1) & 3, bj = g & 1;
;                 const int r = row0 + ai * HALF + m * 16;
;                 if (g + 1 < 16) BC_LOAD((g + 1) & 1, g + 1);
;                 {
;                     {
;                         const int col = cb + bj * HALF + lc;
;                         const size_t hoff = ((size_t)((r >> 11) * 4 + (col >> 7)) * SEQ + (r & (SEQ - 1))) * 128 + (col & 127);
;                         const f32x4 b0 = bc[g & 1][0], b1 = bc[g & 1][1];
;                         const f32x4 v0 = acc[ai][bj][m][0], v1 = acc[ai][bj][m][1];
;                         const float L2E = 1.4426950408889634f;
;                         if (isq) {
;                             const float s = 0.08838834764831845f;
;                             u32x4 o; o[0] = cvt_pk_bf16(v0[0] * s * __builtin_amdgcn_exp2f(b0[0] * L2E), v0[1] * s * __builtin_amdgcn_exp2f(b0[1] * L2E));
;                             o[1] = cvt_pk_bf16(v0[2] * s * __builtin_amdgcn_exp2f(b0[2] * L2E), v0[3] * s * __builtin_amdgcn_exp2f(b0[3] * L2E));
;                             o[2] = cvt_pk_bf16(v1[0] * s * __builtin_amdgcn_exp2f(b1[0] * L2E), v1[1] * s * __builtin_amdgcn_exp2f(b1[1] * L2E));
;                             o[3] = cvt_pk_bf16(v1[2] * s * __builtin_amdgcn_exp2f(b1[2] * L2E), v1[3] * s * __builtin_amdgcn_exp2f(b1[3] * L2E));
;                             __builtin_nontemporal_store(o, (u32x4*)(d0 + hoff));
;                         } else {
;                             u32x4 o;
;                             o[0] = cvt_pk_bf16(v0[0] * __builtin_amdgcn_exp2f(-b0[0] * L2E), v0[1] * __builtin_amdgcn_exp2f(-b0[1] * L2E));
;                             o[1] = cvt_pk_bf16(v0[2] * __builtin_amdgcn_exp2f(-b0[2] * L2E), v0[3] * __builtin_amdgcn_exp2f(-b0[3] * L2E));
;                             o[2] = cvt_pk_bf16(v1[0] * __builtin_amdgcn_exp2f(-b1[0] * L2E), v1[1] * __builtin_amdgcn_exp2f(-b1[1] * L2E));
;                             o[3] = cvt_pk_bf16(v1[2] * __builtin_amdgcn_exp2f(-b1[2] * L2E), v1[3] * __builtin_amdgcn_exp2f(-b1[3] * L2E));
;                             __builtin_nontemporal_store(o, (u32x4*)(d0 + hoff));
.LBB0_1470:
	v_mul_f32_e32 v128, s2, v131
	v_exp_f32_e32 v130, v128
	v_mov_b32_e32 v157, v169
	v_mov_b32_e32 v149, v169
	v_lshl_add_u64 v[128:129], v[154:155], 0, v[156:157]
	v_mul_f32_e32 v130, v159, v130
	v_cvt_pk_bf16_f32 v147, v158, v130
	v_lshl_add_u64 v[128:129], v[128:129], 0, v[148:149]
	global_store_dwordx4 v[128:129], v[144:147], off
	global_load_dwordx4 v[128:131], v[150:151], off offset:528
	s_nop 0
	global_load_dwordx4 v[136:139], v[150:151], off offset:512
	s_and_b64 vcc, exec, s[8:9]
	s_mov_b64 s[2:3], -1
	s_cbranch_vccnz .LBB0_1472
	s_waitcnt vmcnt(3)
	v_mul_f32_e32 v144, 0xbfb8aa3b, v140
	v_mul_f32_e32 v145, 0xbfb8aa3b, v141
	v_exp_f32_e32 v144, v144
	v_exp_f32_e32 v145, v145
	v_mul_f32_e32 v146, 0xbfb8aa3b, v142
	v_mul_f32_e32 v147, 0xbfb8aa3b, v143
	v_exp_f32_e32 v146, v146
	v_pk_mul_f32 v[144:145], v[12:13], v[144:145]
	v_exp_f32_e32 v147, v147
	v_cvt_pk_bf16_f32 v144, v144, v145
	v_mul_f32_e32 v145, 0xbfb8aa3b, v132
	v_exp_f32_e32 v150, v145
	v_mul_f32_e32 v145, 0xbfb8aa3b, v133
	v_exp_f32_e32 v151, v145
	v_mul_f32_e32 v145, 0xbfb8aa3b, v134
	v_exp_f32_e32 v149, v145
	v_pk_mul_f32 v[146:147], v[14:15], v[146:147]
	s_mov_b64 s[2:3], 0
	v_cvt_pk_bf16_f32 v145, v146, v147
	v_pk_mul_f32 v[146:147], v[8:9], v[150:151]
	v_mul_f32_e32 v150, v10, v149
	v_cvt_pk_bf16_f32 v146, v146, v147
	v_mov_b32_e32 v151, v11

; __device__ __forceinline__ unsigned cvt_pk_bf16(float lo, float hi) { const bf16x2_t r = __builtin_convertvector((f32x2_t){lo, hi}, bf16x2_t); return __builtin_bit_cast(unsigned, r); }
;     __device__ __forceinline__ void operator()(const f32x4 (&acc)[2][2][4][2], const Unit& u, int wr, int wc, int fr, int fq) const {
;     ...
;         } else if (u.pn < 12) {
;             bf16_t* dst = (bf16_t*)(ws + WS_VT);
; #pragma unroll
;             for (int ai = 0; ai < 2; ++ai)
; #pragma unroll
;                 for (int m = 0; m < 4; ++m) {
;                     const int r = row0 + ai * HALF + m * 16;
; #pragma unroll
;                     for (int bj = 0; bj < 2; ++bj) {
;                         const f32x4 v0 = acc[ai][bj][m][0], v1 = acc[ai][bj][m][1];
;                         u32x4 o; o[0] = cvt_pk_bf16(v0[0], v0[1]); o[1] = cvt_pk_bf16(v0[2], v0[3]); o[2] = cvt_pk_bf16(v1[0], v1[1]); o[3] = cvt_pk_bf16(v1[2], v1[3]);
;                         __builtin_nontemporal_store(o, (u32x4*)(dst + ((size_t)((r >> 11) * 8 + (u.pn - 8) * 2 + bj) * SEQ + (r & (SEQ - 1))) * 128 + lc));
;                     }
;                 }
.LBB0_1480:
	s_lshl_b32 s2, s76, 1
	s_add_i32 s10, s2, -16
	s_ashr_i32 s2, s15, 8
	s_and_b32 s2, s2, -8
	s_add_i32 s2, s2, s10
	v_lshlrev_b32_e32 v128, 8, v192
	s_ashr_i32 s3, s2, 31
	v_and_b32_e32 v168, 0x7cf00, v128
	s_lshl_b64 s[8:9], s[2:3], 19
	s_or_b32 s2, s2, 1
	v_lshl_add_u64 v[132:133], v[180:181], 0, v[168:169]
	s_ashr_i32 s3, s2, 31
	v_cvt_pk_bf16_f32 v128, v124, v125
	v_cvt_pk_bf16_f32 v129, v126, v127
	v_cvt_pk_bf16_f32 v130, v120, v121
	v_cvt_pk_bf16_f32 v131, v122, v123
	v_lshl_add_u64 v[134:135], v[132:133], 0, s[8:9]
	s_lshl_b64 s[2:3], s[2:3], 19
	global_store_dwordx4 v[134:135], v[128:131], off
	v_lshl_add_u64 v[134:135], v[132:133], 0, s[2:3]
	s_nop 0
	v_cvt_pk_bf16_f32 v128, v116, v117
	v_cvt_pk_bf16_f32 v129, v118, v119
	v_cvt_pk_bf16_f32 v130, v112, v113
	v_cvt_pk_bf16_f32 v131, v114, v115
	global_store_dwordx4 v[134:135], v[128:131], off
	v_lshl_add_u64 v[134:135], v[132:133], 0, s[36:37]
	v_lshl_add_u64 v[136:137], v[134:135], 0, s[8:9]
	v_cvt_pk_bf16_f32 v128, v108, v109
	v_cvt_pk_bf16_f32 v129, v110, v111
	v_cvt_pk_bf16_f32 v130, v104, v105
	v_cvt_pk_bf16_f32 v131, v106, v107
	global_store_dwordx4 v[136:137], v[128:131], off
	v_lshl_add_u64 v[134:135], v[134:135], 0, s[2:3]
	s_nop 0
	v_cvt_pk_bf16_f32 v128, v100, v101
	v_cvt_pk_bf16_f32 v129, v102, v103
	v_cvt_pk_bf16_f32 v130, v96, v97
	v_cvt_pk_bf16_f32 v131, v98, v99
	global_store_dwordx4 v[134:135], v[128:131], off
	v_lshl_add_u64 v[134:135], v[132:133], 0, s[38:39]
	v_lshl_add_u64 v[136:137], v[134:135], 0, s[8:9]
	v_cvt_pk_bf16_f32 v128, v92, v93
	v_cvt_pk_bf16_f32 v129, v94, v95
	v_cvt_pk_bf16_f32 v130, v88, v89
	v_cvt_pk_bf16_f32 v131, v90, v91
	global_store_dwordx4 v[136:137], v[128:131], off
	v_lshl_add_u64 v[134:135], v[134:135], 0, s[2:3]
	v_lshl_add_u64 v[132:133], v[132:133], 0, s[40:41]
	v_cvt_pk_bf16_f32 v128, v84, v85
	v_cvt_pk_bf16_f32 v129, v86, v87
	v_cvt_pk_bf16_f32 v130, v80, v81
	v_cvt_pk_bf16_f32 v131, v82, v83
	global_store_dwordx4 v[134:135], v[128:131], off
	v_lshl_add_u64 v[134:135], v[132:133], 0, s[8:9]
	v_lshl_add_u64 v[132:133], v[132:133], 0, s[2:3]
	v_cvt_pk_bf16_f32 v128, v76, v77
	v_cvt_pk_bf16_f32 v129, v78, v79
	v_cvt_pk_bf16_f32 v130, v72, v73
	v_cvt_pk_bf16_f32 v131, v74, v75
	global_store_dwordx4 v[134:135], v[128:131], off
	s_nop 1
	v_cvt_pk_bf16_f32 v128, v68, v69
	v_cvt_pk_bf16_f32 v129, v70, v71
	v_cvt_pk_bf16_f32 v130, v64, v65
	v_cvt_pk_bf16_f32 v131, v66, v67
	global_store_dwordx4 v[132:133], v[128:131], off
	s_nop 1
	v_add_u32_e32 v128, 0x80, v192
	v_ashrrev_i32_e32 v129, 8, v128
	v_and_b32_e32 v129, -8, v129
	v_add_u32_e32 v132, s10, v129
	v_lshlrev_b32_e32 v128, 8, v128
	v_ashrrev_i32_e32 v133, 31, v132
	v_and_b32_e32 v168, 0x7cf00, v128
	v_lshlrev_b64 v[136:137], 19, v[132:133]
	v_or_b32_e32 v132, 1, v132
	v_lshl_add_u64 v[134:135], v[180:181], 0, v[168:169]
	v_ashrrev_i32_e32 v133, 31, v132
	v_cvt_pk_bf16_f32 v128, v60, v61
	v_cvt_pk_bf16_f32 v129, v62, v63
	v_cvt_pk_bf16_f32 v130, v56, v57
	v_cvt_pk_bf16_f32 v131, v58, v59
	v_lshl_add_u64 v[138:139], v[134:135], 0, v[136:137]
	v_lshlrev_b64 v[132:133], 19, v[132:133]
	global_store_dwordx4 v[138:139], v[128:131], off
	v_lshl_add_u64 v[138:139], v[134:135], 0, v[132:133]
	s_nop 0
	v_cvt_pk_bf16_f32 v128, v52, v53
	v_cvt_pk_bf16_f32 v129, v54, v55
	v_cvt_pk_bf16_f32 v130, v48, v49
	v_cvt_pk_bf16_f32 v131, v50, v51
	global_store_dwordx4 v[138:139], v[128:131], off
	v_lshl_add_u64 v[138:139], v[134:135], 0, s[36:37]
	v_lshl_add_u64 v[140:141], v[138:139], 0, v[136:137]
	v_cvt_pk_bf16_f32 v128, v44, v45
	v_cvt_pk_bf16_f32 v129, v46, v47
	v_cvt_pk_bf16_f32 v130, v40, v41
	v_cvt_pk_bf16_f32 v131, v42, v43
	global_store_dwordx4 v[140:141], v[128:131], off
	v_lshl_add_u64 v[138:139], v[138:139], 0, v[132:133]
	s_nop 0
	v_cvt_pk_bf16_f32 v128, v36, v37
	v_cvt_pk_bf16_f32 v129, v38, v39
	v_cvt_pk_bf16_f32 v130, v32, v33
	v_cvt_pk_bf16_f32 v131, v34, v35
	global_store_dwordx4 v[138:139], v[128:131], off
	v_lshl_add_u64 v[138:139], v[134:135], 0, s[38:39]
	v_lshl_add_u64 v[140:141], v[138:139], 0, v[136:137]
	v_cvt_pk_bf16_f32 v128, v28, v29
	v_cvt_pk_bf16_f32 v129, v30, v31
	v_cvt_pk_bf16_f32 v130, v24, v25
	v_cvt_pk_bf16_f32 v131, v26, v27
	global_store_dwordx4 v[140:141], v[128:131], off
	v_lshl_add_u64 v[138:139], v[138:139], 0, v[132:133]
	v_lshl_add_u64 v[134:135], v[134:135], 0, s[40:41]
	v_cvt_pk_bf16_f32 v128, v20, v21
	v_cvt_pk_bf16_f32 v129, v22, v23
	v_cvt_pk_bf16_f32 v130, v16, v17
	v_cvt_pk_bf16_f32 v131, v18, v19
	global_store_dwordx4 v[138:139], v[128:131], off
	v_lshl_add_u64 v[136:137], v[134:135], 0, v[136:137]
	v_lshl_add_u64 v[132:133], v[134:135], 0, v[132:133]
	v_cvt_pk_bf16_f32 v128, v12, v13
	v_cvt_pk_bf16_f32 v129, v14, v15
	v_cvt_pk_bf16_f32 v130, v8, v9
	v_cvt_pk_bf16_f32 v131, v10, v11
	global_store_dwordx4 v[136:137], v[128:131], off
	s_nop 1
	v_cvt_pk_bf16_f32 v128, v4, v5
	v_cvt_pk_bf16_f32 v129, v6, v7
	v_cvt_pk_bf16_f32 v130, v0, v1
	v_cvt_pk_bf16_f32 v131, v2, v3
	global_store_dwordx4 v[132:133], v[128:131], off

;     __device__ __forceinline__ void operator()(const f32x4 (&acc)[2][2][4][2], const Unit& u, int wr, int wc, int fr, int fq) const {
;     ...
;             const bool isq = u.pn < 4;
;             bf16_t* dst = (bf16_t*)(ws + (isq ? WS_Q : WS_K));
;             const int cb = (u.pn & 3) * 256;
;             const float scale = isq ? QSCALE : 1.0f;
;             float ks[2][8];
; #pragma unroll
;             for (int bj = 0; bj < 2; ++bj)
; #pragma unroll
;                 for (int i = 0; i < 8; ++i) ks[bj][i] = 0.f;
;             f32x4 rc[2][4];
;     ...
;             if (wc == 0) ROPE_LOAD(0, 0);
; #pragma unroll
;             for (int g = 0; g < 8; ++g) {
;                 const int ai = g >> 2, m = g & 3;
;                 const int r = row0 + ai * HALF + m * 16;
;                 if (wc == 0 && g + 1 < 8) ROPE_LOAD((g + 1) & 1, g + 1);
; #pragma unroll
;                 for (int bj = 0; bj < 2; ++bj) {
;                     float v[8] = {acc[ai][bj][m][0][0], acc[ai][bj][m][0][1], acc[ai][bj][m][0][2], acc[ai][bj][m][0][3],
;                                   acc[ai][bj][m][1][0], acc[ai][bj][m][1][1], acc[ai][bj][m][1][2], acc[ai][bj][m][1][3]};
;                     if (wc == 0) {
;                         const f32x4 c0 = rc[g & 1][0], c1 = rc[g & 1][1], s0 = rc[g & 1][2], s1 = rc[g & 1][3];
;                         const float cs[8] = {c0[0], c0[1], c0[2], c0[3], c1[0], c1[1], c1[2], c1[3]}, sn[8] = {s0[0], s0[1], s0[2], s0[3], s1[0], s1[1], s1[2], s1[3]};
; #pragma unroll
;                         for (int i = 0; i < 8; ++i) {
;                             const float pv = __shfl_xor(v[i], 32);
;                             v[i] = (fq < 2) ? (v[i] * cs[i] - pv * sn[i]) : (v[i] * cs[i] + pv * sn[i]);
;                         }
;                     }
;                     if (!isq) {
; #pragma unroll
;                         for (int i = 0; i < 8; ++i) ks[bj][i] += v[i];
;                     }
;                     u32x4 o; o[0] = cvt_pk_bf16(v[0] * scale, v[1] * scale); o[1] = cvt_pk_bf16(v[2] * scale, v[3] * scale);
;                     o[2] = cvt_pk_bf16(v[4] * scale, v[5] * scale); o[3] = cvt_pk_bf16(v[6] * scale, v[7] * scale);
;                     __builtin_nontemporal_store(o, (u32x4*)(dst + ((size_t)((r >> 11) * 8 + (u.pn & 3) * 2 + bj) * SEQ + (r & (SEQ - 1))) * 128 + lc));
;                 }
.LBB0_1490:
	s_and_b64 s[2:3], s[10:11], exec
	s_cselect_b32 s18, s73, 0x42188000
	s_lshl_b32 s2, s76, 1
	s_and_b32 s17, s2, 6
	s_ashr_i32 s2, s15, 8
	s_and_b32 s2, s2, -8
	s_or_b32 s42, s2, s17
	v_lshlrev_b32_e32 v168, 8, v192
	v_cndmask_b32_e64 v194, 1.0, v212, s[10:11]
	v_lshl_add_u64 v[196:197], v[174:175], 0, s[18:19]
	v_and_b32_e32 v168, 0x7cf00, v168
	v_pk_mul_f32 v[124:125], v[194:195], v[124:125] op_sel_hi:[0,1]
	v_pk_mul_f32 v[126:127], v[194:195], v[126:127] op_sel_hi:[0,1]
	v_pk_mul_f32 v[120:121], v[194:195], v[120:121] op_sel_hi:[0,1]
	s_ashr_i32 s43, s42, 31
	v_lshl_add_u64 v[198:199], v[196:197], 0, v[168:169]
	v_cvt_pk_bf16_f32 v124, v124, v125
	v_cvt_pk_bf16_f32 v125, v126, v127
	v_cvt_pk_bf16_f32 v126, v120, v121
	v_pk_mul_f32 v[120:121], v[194:195], v[122:123] op_sel_hi:[0,1]
	s_lshl_b64 s[2:3], s[42:43], 19
	v_cvt_pk_bf16_f32 v127, v120, v121
	v_lshl_add_u64 v[120:121], v[198:199], 0, s[2:3]
	s_and_b64 vcc, exec, s[8:9]
	global_store_dwordx4 v[120:121], v[124:127], off
	s_cbranch_vccz .LBB0_1496
	s_and_b64 vcc, exec, s[48:49]
	s_cbranch_vccz .LBB0_1497

;     __device__ __forceinline__ void operator()(const f32x4 (&acc)[2][2][4][2], const Unit& u, int wr, int wc, int fr, int fq) const {
;     ...
;             const bool isq = u.pn < 4;
;             bf16_t* dst = (bf16_t*)(ws + (isq ? WS_Q : WS_K));
;             const int cb = (u.pn & 3) * 256;
;             const float scale = isq ? QSCALE : 1.0f;
;             float ks[2][8];
; #pragma unroll
;             for (int bj = 0; bj < 2; ++bj)
; #pragma unroll
;                 for (int i = 0; i < 8; ++i) ks[bj][i] = 0.f;
;             f32x4 rc[2][4];
;     ...
;             if (wc == 0) ROPE_LOAD(0, 0);
; #pragma unroll
;             for (int g = 0; g < 8; ++g) {
;                 const int ai = g >> 2, m = g & 3;
;                 const int r = row0 + ai * HALF + m * 16;
;                 if (wc == 0 && g + 1 < 8) ROPE_LOAD((g + 1) & 1, g + 1);
; #pragma unroll
;                 for (int bj = 0; bj < 2; ++bj) {
;                     float v[8] = {acc[ai][bj][m][0][0], acc[ai][bj][m][0][1], acc[ai][bj][m][0][2], acc[ai][bj][m][0][3],
;                                   acc[ai][bj][m][1][0], acc[ai][bj][m][1][1], acc[ai][bj][m][1][2], acc[ai][bj][m][1][3]};
;                     if (wc == 0) {
;                         const f32x4 c0 = rc[g & 1][0], c1 = rc[g & 1][1], s0 = rc[g & 1][2], s1 = rc[g & 1][3];
;                         const float cs[8] = {c0[0], c0[1], c0[2], c0[3], c1[0], c1[1], c1[2], c1[3]}, sn[8] = {s0[0], s0[1], s0[2], s0[3], s1[0], s1[1], s1[2], s1[3]};
; #pragma unroll
;                         for (int i = 0; i < 8; ++i) {
;                             const float pv = __shfl_xor(v[i], 32);
;                             v[i] = (fq < 2) ? (v[i] * cs[i] - pv * sn[i]) : (v[i] * cs[i] + pv * sn[i]);
;                         }
;                     }
;                     if (!isq) {
; #pragma unroll
;                         for (int i = 0; i < 8; ++i) ks[bj][i] += v[i];
;                     }
;                     u32x4 o; o[0] = cvt_pk_bf16(v[0] * scale, v[1] * scale); o[1] = cvt_pk_bf16(v[2] * scale, v[3] * scale);
;                     o[2] = cvt_pk_bf16(v[4] * scale, v[5] * scale); o[3] = cvt_pk_bf16(v[6] * scale, v[7] * scale);
;                     __builtin_nontemporal_store(o, (u32x4*)(dst + ((size_t)((r >> 11) * 8 + (u.pn & 3) * 2 + bj) * SEQ + (r & (SEQ - 1))) * 128 + lc));
;                 }
.LBB0_1507:
	v_pk_mul_f32 v[108:109], v[194:195], v[108:109]
	v_pk_mul_f32 v[110:111], v[194:195], v[110:111]
	v_pk_mul_f32 v[104:105], v[194:195], v[104:105]
	v_lshl_add_u64 v[200:201], v[198:199], 0, s[36:37]
	v_cvt_pk_bf16_f32 v108, v108, v109
	v_cvt_pk_bf16_f32 v109, v110, v111
	v_cvt_pk_bf16_f32 v110, v104, v105
	v_pk_mul_f32 v[104:105], v[194:195], v[106:107]
	s_and_b64 vcc, exec, s[8:9]
	v_cvt_pk_bf16_f32 v111, v104, v105
	v_lshl_add_u64 v[104:105], v[200:201], 0, s[2:3]
	global_store_dwordx4 v[104:105], v[108:111], off
	s_cbranch_vccz .LBB0_1510
	s_and_b64 vcc, exec, s[48:49]
	s_cbranch_vccz .LBB0_1511

;     __device__ __forceinline__ void operator()(const f32x4 (&acc)[2][2][4][2], const Unit& u, int wr, int wc, int fr, int fq) const {
;     ...
;             const bool isq = u.pn < 4;
;             bf16_t* dst = (bf16_t*)(ws + (isq ? WS_Q : WS_K));
;             const int cb = (u.pn & 3) * 256;
;             const float scale = isq ? QSCALE : 1.0f;
;             float ks[2][8];
; #pragma unroll
;             for (int bj = 0; bj < 2; ++bj)
; #pragma unroll
;                 for (int i = 0; i < 8; ++i) ks[bj][i] = 0.f;
;             f32x4 rc[2][4];
;     ...
;             if (wc == 0) ROPE_LOAD(0, 0);
; #pragma unroll
;             for (int g = 0; g < 8; ++g) {
;                 const int ai = g >> 2, m = g & 3;
;                 const int r = row0 + ai * HALF + m * 16;
;                 if (wc == 0 && g + 1 < 8) ROPE_LOAD((g + 1) & 1, g + 1);
; #pragma unroll
;                 for (int bj = 0; bj < 2; ++bj) {
;                     float v[8] = {acc[ai][bj][m][0][0], acc[ai][bj][m][0][1], acc[ai][bj][m][0][2], acc[ai][bj][m][0][3],
;                                   acc[ai][bj][m][1][0], acc[ai][bj][m][1][1], acc[ai][bj][m][1][2], acc[ai][bj][m][1][3]};
;                     if (wc == 0) {
;                         const f32x4 c0 = rc[g & 1][0], c1 = rc[g & 1][1], s0 = rc[g & 1][2], s1 = rc[g & 1][3];
;                         const float cs[8] = {c0[0], c0[1], c0[2], c0[3], c1[0], c1[1], c1[2], c1[3]}, sn[8] = {s0[0], s0[1], s0[2], s0[3], s1[0], s1[1], s1[2], s1[3]};
; #pragma unroll
;                         for (int i = 0; i < 8; ++i) {
;                             const float pv = __shfl_xor(v[i], 32);
;                             v[i] = (fq < 2) ? (v[i] * cs[i] - pv * sn[i]) : (v[i] * cs[i] + pv * sn[i]);
;                         }
;                     }
;                     if (!isq) {
; #pragma unroll
;                         for (int i = 0; i < 8; ++i) ks[bj][i] += v[i];
;                     }
;                     u32x4 o; o[0] = cvt_pk_bf16(v[0] * scale, v[1] * scale); o[1] = cvt_pk_bf16(v[2] * scale, v[3] * scale);
;                     o[2] = cvt_pk_bf16(v[4] * scale, v[5] * scale); o[3] = cvt_pk_bf16(v[6] * scale, v[7] * scale);
;                     __builtin_nontemporal_store(o, (u32x4*)(dst + ((size_t)((r >> 11) * 8 + (u.pn & 3) * 2 + bj) * SEQ + (r & (SEQ - 1))) * 128 + lc));
;                 }
.LBB0_1521:
	v_pk_mul_f32 v[92:93], v[194:195], v[92:93]
	v_pk_mul_f32 v[94:95], v[194:195], v[94:95]
	v_pk_mul_f32 v[88:89], v[194:195], v[88:89]
	v_lshl_add_u64 v[114:115], v[198:199], 0, s[38:39]
	v_cvt_pk_bf16_f32 v92, v92, v93
	v_cvt_pk_bf16_f32 v93, v94, v95
	v_cvt_pk_bf16_f32 v94, v88, v89
	v_pk_mul_f32 v[88:89], v[194:195], v[90:91]
	s_and_b64 vcc, exec, s[8:9]
	v_cvt_pk_bf16_f32 v95, v88, v89
	v_lshl_add_u64 v[88:89], v[114:115], 0, s[2:3]
	global_store_dwordx4 v[88:89], v[92:95], off
	s_cbranch_vccz .LBB0_1524
	s_and_b64 vcc, exec, s[48:49]
	s_cbranch_vccz .LBB0_1525

; __device__ __forceinline__ unsigned cvt_pk_bf16(float lo, float hi) { const bf16x2_t r = __builtin_convertvector((f32x2_t){lo, hi}, bf16x2_t); return __builtin_bit_cast(unsigned, r); }
;     __device__ __forceinline__ void operator()(const f32x4 (&acc)[2][2][4][2], const Unit& u, int wr, int wc, int fr, int fq) const {
;     ...
;                         for (int i = 0; i < 8; ++i) {
;                             const float pv = __shfl_xor(v[i], 32);
;                             v[i] = (fq < 2) ? (v[i] * cs[i] - pv * sn[i]) : (v[i] * cs[i] + pv * sn[i]);
;                         }
;                     }
;                     if (!isq) {
; #pragma unroll
;                         for (int i = 0; i < 8; ++i) ks[bj][i] += v[i];
;                     }
;                     u32x4 o; o[0] = cvt_pk_bf16(v[0] * scale, v[1] * scale); o[1] = cvt_pk_bf16(v[2] * scale, v[3] * scale);
;                     o[2] = cvt_pk_bf16(v[4] * scale, v[5] * scale); o[3] = cvt_pk_bf16(v[6] * scale, v[7] * scale);
;                     __builtin_nontemporal_store(o, (u32x4*)(dst + ((size_t)((r >> 11) * 8 + (u.pn & 3) * 2 + bj) * SEQ + (r & (SEQ - 1))) * 128 + lc));
.LBB0_1535:
	v_pk_mul_f32 v[76:77], v[194:195], v[76:77]
	v_pk_mul_f32 v[78:79], v[194:195], v[78:79]
	v_pk_mul_f32 v[72:73], v[194:195], v[72:73]
	v_lshl_add_u64 v[96:97], v[198:199], 0, s[40:41]
	v_cvt_pk_bf16_f32 v76, v76, v77
	v_cvt_pk_bf16_f32 v77, v78, v79
	v_cvt_pk_bf16_f32 v78, v72, v73
	v_pk_mul_f32 v[72:73], v[194:195], v[74:75]
	s_and_b64 vcc, exec, s[8:9]
	v_cvt_pk_bf16_f32 v79, v72, v73
	v_lshl_add_u64 v[72:73], v[96:97], 0, s[2:3]
	global_store_dwordx4 v[72:73], v[76:79], off
	s_cbranch_vccz .LBB0_1538
	s_and_b64 vcc, exec, s[48:49]
	s_cbranch_vccz .LBB0_1539

; __device__ __forceinline__ unsigned cvt_pk_bf16(float lo, float hi) { const bf16x2_t r = __builtin_convertvector((f32x2_t){lo, hi}, bf16x2_t); return __builtin_bit_cast(unsigned, r); }
;     __device__ __forceinline__ void operator()(const f32x4 (&acc)[2][2][4][2], const Unit& u, int wr, int wc, int fr, int fq) const {
;     ...
;                     u32x4 o; o[0] = cvt_pk_bf16(v[0] * scale, v[1] * scale); o[1] = cvt_pk_bf16(v[2] * scale, v[3] * scale);
;                     o[2] = cvt_pk_bf16(v[4] * scale, v[5] * scale); o[3] = cvt_pk_bf16(v[6] * scale, v[7] * scale);
;                     __builtin_nontemporal_store(o, (u32x4*)(dst + ((size_t)((r >> 11) * 8 + (u.pn & 3) * 2 + bj) * SEQ + (r & (SEQ - 1))) * 128 + lc));
.LBB0_1549:
	v_ashrrev_i32_e32 v64, 8, v88
	v_and_or_b32 v82, v64, -8, s17
	v_lshlrev_b32_e32 v64, 8, v88
	v_pk_mul_f32 v[60:61], v[194:195], v[60:61]
	v_pk_mul_f32 v[62:63], v[194:195], v[62:63]
	v_pk_mul_f32 v[56:57], v[194:195], v[56:57]
	v_and_b32_e32 v168, 0x7cf00, v64
	v_cvt_pk_bf16_f32 v60, v60, v61
	v_cvt_pk_bf16_f32 v61, v62, v63
	v_cvt_pk_bf16_f32 v62, v56, v57
	v_pk_mul_f32 v[56:57], v[194:195], v[58:59]
	v_ashrrev_i32_e32 v83, 31, v82
	v_lshl_add_u64 v[64:65], v[196:197], 0, v[168:169]
	v_cvt_pk_bf16_f32 v63, v56, v57
	v_lshlrev_b64 v[56:57], 19, v[82:83]
	v_lshl_add_u64 v[58:59], v[64:65], 0, v[56:57]
	s_and_b64 vcc, exec, s[8:9]
	global_store_dwordx4 v[58:59], v[60:63], off
	s_cbranch_vccz .LBB0_1552
	s_and_b64 vcc, exec, s[48:49]
	s_cbranch_vccz .LBB0_1553

; __device__ __forceinline__ unsigned cvt_pk_bf16(float lo, float hi) { const bf16x2_t r = __builtin_convertvector((f32x2_t){lo, hi}, bf16x2_t); return __builtin_bit_cast(unsigned, r); }
;     __device__ __forceinline__ void operator()(const f32x4 (&acc)[2][2][4][2], const Unit& u, int wr, int wc, int fr, int fq) const {
;     ...
;                     u32x4 o; o[0] = cvt_pk_bf16(v[0] * scale, v[1] * scale); o[1] = cvt_pk_bf16(v[2] * scale, v[3] * scale);
;                     o[2] = cvt_pk_bf16(v[4] * scale, v[5] * scale); o[3] = cvt_pk_bf16(v[6] * scale, v[7] * scale);
;                     __builtin_nontemporal_store(o, (u32x4*)(dst + ((size_t)((r >> 11) * 8 + (u.pn & 3) * 2 + bj) * SEQ + (r & (SEQ - 1))) * 128 + lc));
.LBB0_1563:
	v_pk_mul_f32 v[44:45], v[194:195], v[44:45]
	v_pk_mul_f32 v[46:47], v[194:195], v[46:47]
	v_pk_mul_f32 v[40:41], v[194:195], v[40:41]
	v_lshl_add_u64 v[66:67], v[64:65], 0, s[36:37]
	v_cvt_pk_bf16_f32 v44, v44, v45
	v_cvt_pk_bf16_f32 v45, v46, v47
	v_cvt_pk_bf16_f32 v46, v40, v41
	v_pk_mul_f32 v[40:41], v[194:195], v[42:43]
	s_and_b64 vcc, exec, s[8:9]
	v_cvt_pk_bf16_f32 v47, v40, v41
	v_lshl_add_u64 v[40:41], v[66:67], 0, v[56:57]
	global_store_dwordx4 v[40:41], v[44:47], off
	s_cbranch_vccz .LBB0_1566
	s_and_b64 vcc, exec, s[48:49]
	s_cbranch_vccz .LBB0_1567

; __device__ __forceinline__ unsigned cvt_pk_bf16(float lo, float hi) { const bf16x2_t r = __builtin_convertvector((f32x2_t){lo, hi}, bf16x2_t); return __builtin_bit_cast(unsigned, r); }
;     __device__ __forceinline__ void operator()(const f32x4 (&acc)[2][2][4][2], const Unit& u, int wr, int wc, int fr, int fq) const {
;     ...
;                     u32x4 o; o[0] = cvt_pk_bf16(v[0] * scale, v[1] * scale); o[1] = cvt_pk_bf16(v[2] * scale, v[3] * scale);
;                     o[2] = cvt_pk_bf16(v[4] * scale, v[5] * scale); o[3] = cvt_pk_bf16(v[6] * scale, v[7] * scale);
;                     __builtin_nontemporal_store(o, (u32x4*)(dst + ((size_t)((r >> 11) * 8 + (u.pn & 3) * 2 + bj) * SEQ + (r & (SEQ - 1))) * 128 + lc));
.LBB0_1577:
	v_pk_mul_f32 v[28:29], v[194:195], v[28:29]
	v_pk_mul_f32 v[30:31], v[194:195], v[30:31]
	v_pk_mul_f32 v[24:25], v[194:195], v[24:25]
	v_lshl_add_u64 v[50:51], v[64:65], 0, s[38:39]
	v_cvt_pk_bf16_f32 v28, v28, v29
	v_cvt_pk_bf16_f32 v29, v30, v31
	v_cvt_pk_bf16_f32 v30, v24, v25
	v_pk_mul_f32 v[24:25], v[194:195], v[26:27]
	s_and_b64 vcc, exec, s[8:9]
	v_cvt_pk_bf16_f32 v31, v24, v25
	v_lshl_add_u64 v[24:25], v[50:51], 0, v[56:57]
	global_store_dwordx4 v[24:25], v[28:31], off
	s_cbranch_vccz .LBB0_1580
	s_and_b64 vcc, exec, s[48:49]
	s_cbranch_vccz .LBB0_1581

; __device__ __forceinline__ unsigned cvt_pk_bf16(float lo, float hi) { const bf16x2_t r = __builtin_convertvector((f32x2_t){lo, hi}, bf16x2_t); return __builtin_bit_cast(unsigned, r); }
;     __device__ __forceinline__ void operator()(const f32x4 (&acc)[2][2][4][2], const Unit& u, int wr, int wc, int fr, int fq) const {
;     ...
;                     u32x4 o; o[0] = cvt_pk_bf16(v[0] * scale, v[1] * scale); o[1] = cvt_pk_bf16(v[2] * scale, v[3] * scale);
;                     o[2] = cvt_pk_bf16(v[4] * scale, v[5] * scale); o[3] = cvt_pk_bf16(v[6] * scale, v[7] * scale);
;                     __builtin_nontemporal_store(o, (u32x4*)(dst + ((size_t)((r >> 11) * 8 + (u.pn & 3) * 2 + bj) * SEQ + (r & (SEQ - 1))) * 128 + lc));
.LBB0_1583:
	v_pk_mul_f32 v[20:21], v[194:195], v[20:21]
	v_pk_mul_f32 v[22:23], v[194:195], v[22:23]
	v_pk_mul_f32 v[16:17], v[194:195], v[16:17]
	v_cvt_pk_bf16_f32 v20, v20, v21
	v_cvt_pk_bf16_f32 v21, v22, v23
	v_cvt_pk_bf16_f32 v22, v16, v17
	v_pk_mul_f32 v[16:17], v[194:195], v[18:19]
	s_and_b64 vcc, exec, s[8:9]
	v_cvt_pk_bf16_f32 v23, v16, v17
	v_lshl_add_u64 v[16:17], v[50:51], 0, v[48:49]
	global_store_dwordx4 v[16:17], v[20:23], off
	s_cbranch_vccz .LBB0_1586
	s_and_b64 vcc, exec, s[48:49]
	s_cbranch_vccz .LBB0_1587

; __device__ __forceinline__ unsigned cvt_pk_bf16(float lo, float hi) { const bf16x2_t r = __builtin_convertvector((f32x2_t){lo, hi}, bf16x2_t); return __builtin_bit_cast(unsigned, r); }
;     __device__ __forceinline__ void operator()(const f32x4 (&acc)[2][2][4][2], const Unit& u, int wr, int wc, int fr, int fq) const {
;     ...
;                     u32x4 o; o[0] = cvt_pk_bf16(v[0] * scale, v[1] * scale); o[1] = cvt_pk_bf16(v[2] * scale, v[3] * scale);
;                     o[2] = cvt_pk_bf16(v[4] * scale, v[5] * scale); o[3] = cvt_pk_bf16(v[6] * scale, v[7] * scale);
;                     __builtin_nontemporal_store(o, (u32x4*)(dst + ((size_t)((r >> 11) * 8 + (u.pn & 3) * 2 + bj) * SEQ + (r & (SEQ - 1))) * 128 + lc));
.LBB0_1589:
	v_pk_mul_f32 v[12:13], v[194:195], v[12:13]
	v_pk_mul_f32 v[14:15], v[194:195], v[14:15]
	v_pk_mul_f32 v[8:9], v[194:195], v[8:9]
	v_lshl_add_u64 v[32:33], v[64:65], 0, s[40:41]
	v_cvt_pk_bf16_f32 v12, v12, v13
	v_cvt_pk_bf16_f32 v13, v14, v15
	v_cvt_pk_bf16_f32 v14, v8, v9
	v_pk_mul_f32 v[8:9], v[194:195], v[10:11]
	s_and_b64 vcc, exec, s[8:9]
	v_cvt_pk_bf16_f32 v15, v8, v9
	v_lshl_add_u64 v[8:9], v[32:33], 0, v[56:57]
	global_store_dwordx4 v[8:9], v[12:15], off
	s_cbranch_vccz .LBB0_1592
	s_and_b64 vcc, exec, s[48:49]
	s_cbranch_vccz .LBB0_1593

; __device__ __forceinline__ unsigned cvt_pk_bf16(float lo, float hi) { const bf16x2_t r = __builtin_convertvector((f32x2_t){lo, hi}, bf16x2_t); return __builtin_bit_cast(unsigned, r); }
;     __device__ __forceinline__ void operator()(const f32x4 (&acc)[2][2][4][2], const Unit& u, int wr, int wc, int fr, int fq) const {
;     ...
;                     u32x4 o; o[0] = cvt_pk_bf16(v[0] * scale, v[1] * scale); o[1] = cvt_pk_bf16(v[2] * scale, v[3] * scale);
;                     o[2] = cvt_pk_bf16(v[4] * scale, v[5] * scale); o[3] = cvt_pk_bf16(v[6] * scale, v[7] * scale);
;                     __builtin_nontemporal_store(o, (u32x4*)(dst + ((size_t)((r >> 11) * 8 + (u.pn & 3) * 2 + bj) * SEQ + (r & (SEQ - 1))) * 128 + lc));
;                 }
;             }
;     ...
;             if (!isq) {
;                 const int b = u.pm >> 3, blk = u.pm & 7;
; #pragma unroll
;                 for (int bj = 0; bj < 2; ++bj) {
;                     const int h = (u.pn & 3) * 2 + bj;
; #pragma unroll
;                     for (int i = 0; i < 8; ++i) {
;                         float s = ks[bj][i];
;                         s += __shfl_xor(s, 1); s += __shfl_xor(s, 2); s += __shfl_xor(s, 4); s += __shfl_xor(s, 8);
;                         if (fr == 0) atomicAdd(kmean + (((size_t)b * 8 + h) * 8 + blk) * 128 + lc + i, s * (1.0f / 256.0f));
.LBB0_1595:
	v_pk_mul_f32 v[4:5], v[194:195], v[4:5]
	v_pk_mul_f32 v[6:7], v[194:195], v[6:7]
	v_pk_mul_f32 v[0:1], v[194:195], v[0:1]
	v_cvt_pk_bf16_f32 v4, v4, v5
	v_cvt_pk_bf16_f32 v5, v6, v7
	v_cvt_pk_bf16_f32 v6, v0, v1
	v_pk_mul_f32 v[0:1], v[194:195], v[2:3]
	s_andn2_b64 vcc, exec, s[48:49]
	v_cvt_pk_bf16_f32 v7, v0, v1
	v_lshl_add_u64 v[0:1], v[32:33], 0, v[48:49]
	global_store_dwordx4 v[0:1], v[4:7], off
	s_cbranch_vccnz .LBB0_1372
	v_and_b32_e32 v1, 64, v211
	v_xor_b32_e32 v0, 1, v211
	v_add_u32_e32 v1, 64, v1
	v_cmp_lt_i32_e32 vcc, v0, v1
	s_ashr_i32 s2, s75, 3
	s_ashr_i32 s3, s2, 31
	v_cndmask_b32_e32 v0, v211, v0, vcc
	v_lshlrev_b32_e32 v2, 2, v0
	ds_bpermute_b32 v4, v2, v22
	v_xor_b32_e32 v0, 2, v211
	v_cmp_lt_i32_e32 vcc, v0, v1
	s_and_b32 s8, s75, 7
	s_lshl_b64 s[2:3], s[2:3], 6
	v_cndmask_b32_e32 v0, v211, v0, vcc
	v_lshlrev_b32_e32 v3, 2, v0
	s_waitcnt lgkmcnt(0)
	v_add_f32_e32 v5, v22, v4
	ds_bpermute_b32 v6, v3, v5
	v_xor_b32_e32 v0, 4, v211
	v_cmp_lt_i32_e32 vcc, v0, v1
	s_or_b32 s2, s2, s8
	s_lshl_b32 s8, s17, 3
	v_cndmask_b32_e32 v0, v211, v0, vcc
	v_lshlrev_b32_e32 v4, 2, v0
	v_xor_b32_e32 v0, 8, v211
	v_cmp_lt_i32_e32 vcc, v0, v1
	s_waitcnt lgkmcnt(0)
	v_add_f32_e32 v1, v5, v6
	ds_bpermute_b32 v6, v4, v1
	v_cndmask_b32_e32 v0, v211, v0, vcc
	v_lshlrev_b32_e32 v5, 2, v0
	s_or_b32 s2, s2, s8
	s_lshl_b64 s[8:9], s[2:3], 9
	s_waitcnt lgkmcnt(0)
	v_add_f32_e32 v6, v1, v6
	ds_bpermute_b32 v7, v5, v6
	v_lshl_add_u64 v[0:1], v[178:179], 0, s[8:9]
	s_and_saveexec_b64 s[8:9], s[4:5]
	s_cbranch_execz .LBB0_1598
	s_waitcnt lgkmcnt(0)
	v_add_f32_e32 v6, v6, v7
	v_mul_f32_e32 v6, 0x3b800000, v6
	global_atomic_add_f32 v[0:1], v6, off
